# GEMM K loops: the mid-segment s_setprio 0/1 dip between the two MFMA clusters removed (priority 1 held through the whole matrix segment)
# speedup vs baseline: 1.0005x; 1.0005x over previous
.LBB0_289:
	ds_read_b128 v[130:133], v167
	ds_read_b128 v[134:137], v167 offset:1024
	ds_read_b128 v[138:141], v167 offset:2048
	ds_read_b128 v[142:145], v167 offset:3072
	ds_read_b128 v[178:181], v188
	ds_read_b128 v[182:185], v188 offset:1024
	ds_read_b128 v[190:193], v188 offset:2048
	ds_read_b128 v[194:197], v188 offset:3072
	s_add_u32 s42, s8, 0x80
	s_addc_u32 s43, s9, 0
	s_cmp_eq_u32 s33, 28
	s_cselect_b32 s53, s49, s43
	s_cselect_b32 s52, s48, s42
	s_cselect_b32 s43, s51, s14
	s_cselect_b32 s42, s50, s5
	v_lshl_add_u64 v[186:187], s[8:9], 0, v[172:173]
	s_add_i32 m0, s62, 0xc000
	ds_read_b128 v[198:201], v189
	ds_read_b128 v[202:205], v189 offset:1024
	ds_read_b128 v[206:209], v189 offset:2048
	ds_read_b128 v[210:213], v189 offset:3072
	ds_read_b128 v[214:217], v189 offset:4096
	ds_read_b128 v[218:221], v189 offset:5120
	ds_read_b128 v[222:225], v189 offset:6144
	ds_read_b128 v[230:233], v189 offset:7168
	global_load_lds_dwordx4 v[186:187], off
	v_lshl_add_u64 v[186:187], s[8:9], 0, v[170:171]
	s_add_i32 m0, s62, 0xe000
	s_nop 0
	global_load_lds_dwordx4 v[186:187], off
	s_waitcnt vmcnt(8)
	s_waitcnt lgkmcnt(0)
	s_barrier
	s_setprio 1
	s_waitcnt lgkmcnt(0)
	v_mfma_f32_16x16x32_bf16 v[126:129], v[130:133], v[198:201], v[126:129]
	v_mfma_f32_16x16x32_bf16 v[122:125], v[138:141], v[198:201], v[122:125]
	v_mfma_f32_16x16x32_bf16 v[110:113], v[130:133], v[206:209], v[110:113]
	v_mfma_f32_16x16x32_bf16 v[106:109], v[138:141], v[206:209], v[106:109]
	v_mfma_f32_16x16x32_bf16 v[94:97], v[130:133], v[214:217], v[94:97]
	v_mfma_f32_16x16x32_bf16 v[90:93], v[138:141], v[214:217], v[90:93]
	v_mfma_f32_16x16x32_bf16 v[78:81], v[130:133], v[222:225], v[78:81]
	v_mfma_f32_16x16x32_bf16 v[74:77], v[138:141], v[222:225], v[74:77]
	v_mfma_f32_16x16x32_bf16 v[126:129], v[134:137], v[202:205], v[126:129]
	v_mfma_f32_16x16x32_bf16 v[122:125], v[142:145], v[202:205], v[122:125]
	v_mfma_f32_16x16x32_bf16 v[110:113], v[134:137], v[210:213], v[110:113]
	v_mfma_f32_16x16x32_bf16 v[106:109], v[142:145], v[210:213], v[106:109]
	v_mfma_f32_16x16x32_bf16 v[94:97], v[134:137], v[218:221], v[94:97]
	v_mfma_f32_16x16x32_bf16 v[90:93], v[142:145], v[218:221], v[90:93]
	v_mfma_f32_16x16x32_bf16 v[78:81], v[134:137], v[230:233], v[78:81]
	v_mfma_f32_16x16x32_bf16 v[74:77], v[142:145], v[230:233], v[74:77]
	v_mfma_f32_16x16x32_bf16 v[118:121], v[178:181], v[198:201], v[118:121]
	v_mfma_f32_16x16x32_bf16 v[114:117], v[190:193], v[198:201], v[114:117]
	v_mfma_f32_16x16x32_bf16 v[102:105], v[178:181], v[206:209], v[102:105]
	v_mfma_f32_16x16x32_bf16 v[98:101], v[190:193], v[206:209], v[98:101]
	v_mfma_f32_16x16x32_bf16 v[86:89], v[178:181], v[214:217], v[86:89]
	v_mfma_f32_16x16x32_bf16 v[82:85], v[190:193], v[214:217], v[82:85]
	v_mfma_f32_16x16x32_bf16 v[70:73], v[178:181], v[222:225], v[70:73]
	v_mfma_f32_16x16x32_bf16 v[66:69], v[190:193], v[222:225], v[66:69]
	v_mfma_f32_16x16x32_bf16 v[118:121], v[182:185], v[202:205], v[118:121]
	v_mfma_f32_16x16x32_bf16 v[114:117], v[194:197], v[202:205], v[114:117]
	v_mfma_f32_16x16x32_bf16 v[102:105], v[182:185], v[210:213], v[102:105]
	v_mfma_f32_16x16x32_bf16 v[98:101], v[194:197], v[210:213], v[98:101]
	v_mfma_f32_16x16x32_bf16 v[86:89], v[182:185], v[218:221], v[86:89]
	v_mfma_f32_16x16x32_bf16 v[82:85], v[194:197], v[218:221], v[82:85]
	v_mfma_f32_16x16x32_bf16 v[70:73], v[182:185], v[230:233], v[70:73]
	v_mfma_f32_16x16x32_bf16 v[66:69], v[194:197], v[230:233], v[66:69]
	s_setprio 0
	s_barrier
	s_add_i32 s45, s76, s61
	v_lshl_add_u64 v[186:187], s[42:43], 0, v[146:147]
	s_mov_b32 m0, s45
	ds_read_b128 v[198:201], v189 offset:16384
	ds_read_b128 v[202:205], v189 offset:17408
	ds_read_b128 v[206:209], v189 offset:18432
	ds_read_b128 v[210:213], v189 offset:19456
	ds_read_b128 v[214:217], v189 offset:20480
	ds_read_b128 v[218:221], v189 offset:21504
	ds_read_b128 v[222:225], v189 offset:22528
	ds_read_b128 v[230:233], v189 offset:23552
	global_load_lds_dwordx4 v[186:187], off
	s_add_i32 m0, s45, 0x2000
	s_add_u32 s54, s42, 0x80000
	v_lshl_add_u64 v[226:227], s[42:43], 0, v[148:149]
	s_addc_u32 s55, s43, 0
	s_add_i32 s45, s77, s61
	global_load_lds_dwordx4 v[226:227], off
	v_lshl_add_u64 v[234:235], s[54:55], 0, v[146:147]
	s_mov_b32 m0, s45
	v_lshl_add_u64 v[236:237], s[52:53], 0, v[152:153]
	global_load_lds_dwordx4 v[234:235], off
	v_lshl_add_u64 v[234:235], s[54:55], 0, v[148:149]
	s_add_i32 m0, s45, 0x2000
	s_nop 0
	global_load_lds_dwordx4 v[234:235], off
	v_lshl_add_u64 v[234:235], s[52:53], 0, v[150:151]
	s_mov_b32 m0, s62
	s_nop 0
	global_load_lds_dwordx4 v[234:235], off
	s_mov_b32 m0, s63
	s_nop 0
	global_load_lds_dwordx4 v[236:237], off
	s_waitcnt vmcnt(8)
	s_waitcnt lgkmcnt(0)
	s_barrier
	s_setprio 1
	s_waitcnt lgkmcnt(0)
	v_mfma_f32_16x16x32_bf16 v[54:57], v[130:133], v[198:201], v[54:57]
	v_mfma_f32_16x16x32_bf16 v[50:53], v[138:141], v[198:201], v[50:53]
	v_mfma_f32_16x16x32_bf16 v[38:41], v[130:133], v[206:209], v[38:41]
	v_mfma_f32_16x16x32_bf16 v[34:37], v[138:141], v[206:209], v[34:37]
	v_mfma_f32_16x16x32_bf16 v[22:25], v[130:133], v[214:217], v[22:25]
	v_mfma_f32_16x16x32_bf16 v[18:21], v[138:141], v[214:217], v[18:21]
	v_mfma_f32_16x16x32_bf16 v[6:9], v[130:133], v[222:225], v[6:9]
	v_mfma_f32_16x16x32_bf16 v[2:5], v[138:141], v[222:225], v[2:5]
	v_mfma_f32_16x16x32_bf16 v[54:57], v[134:137], v[202:205], v[54:57]
	v_mfma_f32_16x16x32_bf16 v[50:53], v[142:145], v[202:205], v[50:53]
	v_mfma_f32_16x16x32_bf16 v[38:41], v[134:137], v[210:213], v[38:41]
	v_mfma_f32_16x16x32_bf16 v[34:37], v[142:145], v[210:213], v[34:37]
	v_mfma_f32_16x16x32_bf16 v[22:25], v[134:137], v[218:221], v[22:25]
	v_mfma_f32_16x16x32_bf16 v[18:21], v[142:145], v[218:221], v[18:21]
	v_mfma_f32_16x16x32_bf16 v[6:9], v[134:137], v[230:233], v[6:9]
	v_mfma_f32_16x16x32_bf16 v[2:5], v[142:145], v[230:233], v[2:5]
	v_mfma_f32_16x16x32_bf16 v[58:61], v[178:181], v[198:201], v[58:61]
	v_mfma_f32_16x16x32_bf16 v[62:65], v[190:193], v[198:201], v[62:65]
	v_mfma_f32_16x16x32_bf16 v[42:45], v[178:181], v[206:209], v[42:45]
	v_mfma_f32_16x16x32_bf16 v[46:49], v[190:193], v[206:209], v[46:49]
	v_mfma_f32_16x16x32_bf16 v[26:29], v[178:181], v[214:217], v[26:29]
	v_mfma_f32_16x16x32_bf16 v[30:33], v[190:193], v[214:217], v[30:33]
	v_mfma_f32_16x16x32_bf16 v[10:13], v[178:181], v[222:225], v[10:13]
	v_mfma_f32_16x16x32_bf16 v[14:17], v[190:193], v[222:225], v[14:17]
	v_mfma_f32_16x16x32_bf16 v[58:61], v[182:185], v[202:205], v[58:61]
	v_mfma_f32_16x16x32_bf16 v[62:65], v[194:197], v[202:205], v[62:65]
	v_mfma_f32_16x16x32_bf16 v[42:45], v[182:185], v[210:213], v[42:45]
	v_mfma_f32_16x16x32_bf16 v[46:49], v[194:197], v[210:213], v[46:49]
	v_mfma_f32_16x16x32_bf16 v[26:29], v[182:185], v[218:221], v[26:29]
	v_mfma_f32_16x16x32_bf16 v[30:33], v[194:197], v[218:221], v[30:33]
	v_mfma_f32_16x16x32_bf16 v[10:13], v[182:185], v[230:233], v[10:13]
	v_mfma_f32_16x16x32_bf16 v[14:17], v[194:197], v[230:233], v[14:17]
	s_setprio 0
	s_barrier
	s_add_i32 s45, 0, 0x18000
	s_add_i32 s47, 0, 0x1c000
	v_add_u32_e32 v142, s45, v163
	v_add_u32_e32 v158, s47, v163
	ds_read_b128 v[130:133], v142
	ds_read_b128 v[134:137], v142 offset:1024
	ds_read_b128 v[138:141], v142 offset:2048
	ds_read_b128 v[142:145], v142 offset:3072
	ds_read_b128 v[178:181], v158
	ds_read_b128 v[182:185], v158 offset:1024
	ds_read_b128 v[190:193], v158 offset:2048
	ds_read_b128 v[194:197], v158 offset:3072
	s_mov_b32 m0, s64
	v_lshl_add_u64 v[238:239], s[52:53], 0, v[154:155]
	ds_read_b128 v[198:201], v189 offset:32768
	ds_read_b128 v[202:205], v189 offset:33792
	ds_read_b128 v[206:209], v189 offset:34816
	ds_read_b128 v[210:213], v189 offset:35840
	ds_read_b128 v[214:217], v189 offset:36864
	ds_read_b128 v[218:221], v189 offset:37888
	ds_read_b128 v[222:225], v189 offset:38912
	ds_read_b128 v[230:233], v189 offset:39936
	global_load_lds_dwordx4 v[238:239], off
	v_lshl_add_u64 v[238:239], s[52:53], 0, v[156:157]
	s_mov_b32 m0, s65
	s_nop 0
	global_load_lds_dwordx4 v[238:239], off
	s_waitcnt vmcnt(8)
	s_waitcnt lgkmcnt(0)
	s_barrier
	s_setprio 1
	s_waitcnt lgkmcnt(0)
	v_mfma_f32_16x16x32_bf16 v[126:129], v[130:133], v[198:201], v[126:129]
	v_mfma_f32_16x16x32_bf16 v[122:125], v[138:141], v[198:201], v[122:125]
	v_mfma_f32_16x16x32_bf16 v[110:113], v[130:133], v[206:209], v[110:113]
	v_mfma_f32_16x16x32_bf16 v[106:109], v[138:141], v[206:209], v[106:109]
	v_mfma_f32_16x16x32_bf16 v[94:97], v[130:133], v[214:217], v[94:97]
	v_mfma_f32_16x16x32_bf16 v[90:93], v[138:141], v[214:217], v[90:93]
	v_mfma_f32_16x16x32_bf16 v[78:81], v[130:133], v[222:225], v[78:81]
	v_mfma_f32_16x16x32_bf16 v[74:77], v[138:141], v[222:225], v[74:77]
	v_mfma_f32_16x16x32_bf16 v[126:129], v[134:137], v[202:205], v[126:129]
	v_mfma_f32_16x16x32_bf16 v[122:125], v[142:145], v[202:205], v[122:125]
	v_mfma_f32_16x16x32_bf16 v[110:113], v[134:137], v[210:213], v[110:113]
	v_mfma_f32_16x16x32_bf16 v[106:109], v[142:145], v[210:213], v[106:109]
	v_mfma_f32_16x16x32_bf16 v[94:97], v[134:137], v[218:221], v[94:97]
	v_mfma_f32_16x16x32_bf16 v[90:93], v[142:145], v[218:221], v[90:93]
	v_mfma_f32_16x16x32_bf16 v[78:81], v[134:137], v[230:233], v[78:81]
	v_mfma_f32_16x16x32_bf16 v[74:77], v[142:145], v[230:233], v[74:77]
	v_mfma_f32_16x16x32_bf16 v[118:121], v[178:181], v[198:201], v[118:121]
	v_mfma_f32_16x16x32_bf16 v[114:117], v[190:193], v[198:201], v[114:117]
	v_mfma_f32_16x16x32_bf16 v[102:105], v[178:181], v[206:209], v[102:105]
	v_mfma_f32_16x16x32_bf16 v[98:101], v[190:193], v[206:209], v[98:101]
	v_mfma_f32_16x16x32_bf16 v[86:89], v[178:181], v[214:217], v[86:89]
	v_mfma_f32_16x16x32_bf16 v[82:85], v[190:193], v[214:217], v[82:85]
	v_mfma_f32_16x16x32_bf16 v[70:73], v[178:181], v[222:225], v[70:73]
	v_mfma_f32_16x16x32_bf16 v[66:69], v[190:193], v[222:225], v[66:69]
	v_mfma_f32_16x16x32_bf16 v[118:121], v[182:185], v[202:205], v[118:121]
	v_mfma_f32_16x16x32_bf16 v[114:117], v[194:197], v[202:205], v[114:117]
	v_mfma_f32_16x16x32_bf16 v[102:105], v[182:185], v[210:213], v[102:105]
	v_mfma_f32_16x16x32_bf16 v[98:101], v[194:197], v[210:213], v[98:101]
	v_mfma_f32_16x16x32_bf16 v[86:89], v[182:185], v[218:221], v[86:89]
	v_mfma_f32_16x16x32_bf16 v[82:85], v[194:197], v[218:221], v[82:85]
	v_mfma_f32_16x16x32_bf16 v[70:73], v[182:185], v[230:233], v[70:73]
	v_mfma_f32_16x16x32_bf16 v[66:69], v[194:197], v[230:233], v[66:69]
	s_setprio 0
	s_barrier
	s_add_i32 s45, s45, s61
	v_lshl_add_u64 v[186:187], v[186:187], 0, s[18:19]
	s_mov_b32 m0, s45
	ds_read_b128 v[198:201], v189 offset:49152
	ds_read_b128 v[202:205], v189 offset:50176
	ds_read_b128 v[206:209], v189 offset:51200
	ds_read_b128 v[210:213], v189 offset:52224
	ds_read_b128 v[214:217], v189 offset:53248
	ds_read_b128 v[218:221], v189 offset:54272
	ds_read_b128 v[222:225], v189 offset:55296
	ds_read_b128 v[230:233], v189 offset:56320
	global_load_lds_dwordx4 v[186:187], off
	s_add_i32 m0, s45, 0x2000
	s_add_u32 s42, s42, 0x80080
	v_lshl_add_u64 v[186:187], v[226:227], 0, s[18:19]
	s_addc_u32 s43, s43, 0
	s_add_i32 s45, s47, s61
	global_load_lds_dwordx4 v[186:187], off
	v_lshl_add_u64 v[186:187], s[42:43], 0, v[146:147]
	s_mov_b32 m0, s45
	s_nop 0
	global_load_lds_dwordx4 v[186:187], off
	v_lshl_add_u64 v[186:187], s[42:43], 0, v[148:149]
	s_add_i32 m0, s45, 0x2000
	s_nop 0
	global_load_lds_dwordx4 v[186:187], off
	v_lshl_add_u64 v[186:187], v[234:235], 0, s[18:19]
	s_mov_b32 m0, s68
	s_nop 0
	global_load_lds_dwordx4 v[186:187], off
	v_lshl_add_u64 v[186:187], v[236:237], 0, s[18:19]
	s_mov_b32 m0, s69
	s_nop 0
	global_load_lds_dwordx4 v[186:187], off
	s_waitcnt vmcnt(8)
	s_waitcnt lgkmcnt(0)
	s_barrier
	s_setprio 1
	s_waitcnt lgkmcnt(0)
	v_mfma_f32_16x16x32_bf16 v[54:57], v[130:133], v[198:201], v[54:57]
	v_mfma_f32_16x16x32_bf16 v[50:53], v[138:141], v[198:201], v[50:53]
	v_mfma_f32_16x16x32_bf16 v[38:41], v[130:133], v[206:209], v[38:41]
	v_mfma_f32_16x16x32_bf16 v[34:37], v[138:141], v[206:209], v[34:37]
	v_mfma_f32_16x16x32_bf16 v[22:25], v[130:133], v[214:217], v[22:25]
	v_mfma_f32_16x16x32_bf16 v[18:21], v[138:141], v[214:217], v[18:21]
	v_mfma_f32_16x16x32_bf16 v[6:9], v[130:133], v[222:225], v[6:9]
	v_mfma_f32_16x16x32_bf16 v[2:5], v[138:141], v[222:225], v[2:5]
	v_mfma_f32_16x16x32_bf16 v[54:57], v[134:137], v[202:205], v[54:57]
	v_mfma_f32_16x16x32_bf16 v[50:53], v[142:145], v[202:205], v[50:53]
	v_mfma_f32_16x16x32_bf16 v[38:41], v[134:137], v[210:213], v[38:41]
	v_mfma_f32_16x16x32_bf16 v[34:37], v[142:145], v[210:213], v[34:37]
	v_mfma_f32_16x16x32_bf16 v[22:25], v[134:137], v[218:221], v[22:25]
	v_mfma_f32_16x16x32_bf16 v[18:21], v[142:145], v[218:221], v[18:21]
	v_mfma_f32_16x16x32_bf16 v[6:9], v[134:137], v[230:233], v[6:9]
	v_mfma_f32_16x16x32_bf16 v[2:5], v[142:145], v[230:233], v[2:5]
	v_mfma_f32_16x16x32_bf16 v[58:61], v[178:181], v[198:201], v[58:61]
	v_mfma_f32_16x16x32_bf16 v[62:65], v[190:193], v[198:201], v[62:65]
	v_mfma_f32_16x16x32_bf16 v[42:45], v[178:181], v[206:209], v[42:45]
	v_mfma_f32_16x16x32_bf16 v[46:49], v[190:193], v[206:209], v[46:49]
	v_mfma_f32_16x16x32_bf16 v[26:29], v[178:181], v[214:217], v[26:29]
	v_mfma_f32_16x16x32_bf16 v[30:33], v[190:193], v[214:217], v[30:33]
	v_mfma_f32_16x16x32_bf16 v[10:13], v[178:181], v[222:225], v[10:13]
	v_mfma_f32_16x16x32_bf16 v[14:17], v[190:193], v[222:225], v[14:17]
	v_mfma_f32_16x16x32_bf16 v[58:61], v[182:185], v[202:205], v[58:61]
	v_mfma_f32_16x16x32_bf16 v[62:65], v[194:197], v[202:205], v[62:65]
	v_mfma_f32_16x16x32_bf16 v[42:45], v[182:185], v[210:213], v[42:45]
	v_mfma_f32_16x16x32_bf16 v[46:49], v[194:197], v[210:213], v[46:49]
	v_mfma_f32_16x16x32_bf16 v[26:29], v[182:185], v[218:221], v[26:29]
	v_mfma_f32_16x16x32_bf16 v[30:33], v[194:197], v[218:221], v[30:33]
	v_mfma_f32_16x16x32_bf16 v[10:13], v[182:185], v[230:233], v[10:13]
	v_mfma_f32_16x16x32_bf16 v[14:17], v[194:197], v[230:233], v[14:17]
	s_setprio 0
	s_barrier
	s_add_i32 s33, s33, 2
	s_add_u32 s8, s8, 0x100
	s_addc_u32 s9, s9, 0
	s_add_u32 s5, s5, 0x100
	s_addc_u32 s14, s14, 0
	s_cmp_gt_u32 s33, 29
	s_cbranch_scc0 .LBB0_289
	s_and_b64 vcc, exec, s[20:21]
	s_cbranch_vccz .LBB0_292
	s_barrier

.LBB0_421:
	ds_read_b128 v[18:21], v196
	ds_read_b128 v[22:25], v196 offset:1024
	ds_read_b128 v[26:29], v196 offset:2048
	ds_read_b128 v[30:33], v196 offset:3072
	ds_read_b128 v[2:5], v197
	ds_read_b128 v[6:9], v197 offset:1024
	ds_read_b128 v[10:13], v197 offset:2048
	ds_read_b128 v[14:17], v197 offset:3072
	s_add_u32 s38, s36, 0x80
	s_addc_u32 s39, s37, 0
	s_cmp_eq_u32 s59, 12
	s_cselect_b32 s41, s29, s39
	s_cselect_b32 s40, s28, s38
	s_cselect_b32 s39, s31, s58
	s_cselect_b32 s38, s30, s27
	v_lshl_add_u64 v[224:225], s[36:37], 0, v[180:181]
	s_add_i32 m0, s35, 0xc000
	ds_read_b128 v[186:189], v198
	ds_read_b128 v[190:193], v198 offset:1024
	ds_read_b128 v[200:203], v198 offset:2048
	ds_read_b128 v[204:207], v198 offset:3072
	ds_read_b128 v[208:211], v198 offset:4096
	ds_read_b128 v[212:215], v198 offset:5120
	ds_read_b128 v[216:219], v198 offset:6144
	ds_read_b128 v[220:223], v198 offset:7168
	global_load_lds_dwordx4 v[224:225], off
	v_lshl_add_u64 v[224:225], s[36:37], 0, v[178:179]
	s_add_i32 m0, s35, 0xe000
	s_nop 0
	global_load_lds_dwordx4 v[224:225], off
	s_waitcnt vmcnt(8)
	s_waitcnt lgkmcnt(0)
	s_barrier
	s_setprio 1
	s_waitcnt lgkmcnt(0)
	s_nop 1
	v_mfma_f32_16x16x128_f8f6f4 v[158:161], v[18:25], v[186:193], v[158:161]
	v_mfma_f32_16x16x128_f8f6f4 v[154:157], v[26:33], v[186:193], v[154:157]
	v_mfma_f32_16x16x128_f8f6f4 v[142:145], v[18:25], v[200:207], v[142:145]
	v_mfma_f32_16x16x128_f8f6f4 v[138:141], v[26:33], v[200:207], v[138:141]
	v_mfma_f32_16x16x128_f8f6f4 v[126:129], v[18:25], v[208:215], v[126:129]
	v_mfma_f32_16x16x128_f8f6f4 v[122:125], v[26:33], v[208:215], v[122:125]
	v_mfma_f32_16x16x128_f8f6f4 v[110:113], v[18:25], v[216:223], v[110:113]
	v_mfma_f32_16x16x128_f8f6f4 v[106:109], v[26:33], v[216:223], v[106:109]
	s_nop 1
	v_mfma_f32_16x16x128_f8f6f4 v[150:153], v[2:9], v[186:193], v[150:153]
	v_mfma_f32_16x16x128_f8f6f4 v[146:149], v[10:17], v[186:193], v[146:149]
	v_mfma_f32_16x16x128_f8f6f4 v[134:137], v[2:9], v[200:207], v[134:137]
	v_mfma_f32_16x16x128_f8f6f4 v[130:133], v[10:17], v[200:207], v[130:133]
	v_mfma_f32_16x16x128_f8f6f4 v[118:121], v[2:9], v[208:215], v[118:121]
	v_mfma_f32_16x16x128_f8f6f4 v[114:117], v[10:17], v[208:215], v[114:117]
	v_mfma_f32_16x16x128_f8f6f4 v[102:105], v[2:9], v[216:223], v[102:105]
	v_mfma_f32_16x16x128_f8f6f4 v[98:101], v[10:17], v[216:223], v[98:101]
	s_setprio 0
	s_barrier
	s_add_i32 s60, s49, s42
	v_lshl_add_u64 v[186:187], s[38:39], 0, v[162:163]
	s_mov_b32 m0, s60
	ds_read_b128 v[200:203], v198 offset:16384
	ds_read_b128 v[204:207], v198 offset:17408
	ds_read_b128 v[208:211], v198 offset:18432
	ds_read_b128 v[212:215], v198 offset:19456
	ds_read_b128 v[216:219], v198 offset:20480
	ds_read_b128 v[220:223], v198 offset:21504
	ds_read_b128 v[230:233], v198 offset:22528
	ds_read_b128 v[234:237], v198 offset:23552
	global_load_lds_dwordx4 v[186:187], off
	s_add_i32 m0, s60, 0x2000
	s_add_u32 s60, s38, 0x40000
	v_lshl_add_u64 v[188:189], s[38:39], 0, v[164:165]
	s_addc_u32 s61, s39, 0
	s_add_i32 s62, s53, s42
	global_load_lds_dwordx4 v[188:189], off
	v_lshl_add_u64 v[190:191], s[60:61], 0, v[162:163]
	s_mov_b32 m0, s62
	v_lshl_add_u64 v[192:193], s[40:41], 0, v[168:169]
	global_load_lds_dwordx4 v[190:191], off
	v_lshl_add_u64 v[190:191], s[60:61], 0, v[164:165]
	s_add_i32 m0, s62, 0x2000
	s_nop 0
	global_load_lds_dwordx4 v[190:191], off
	v_lshl_add_u64 v[190:191], s[40:41], 0, v[166:167]
	s_mov_b32 m0, s35
	s_nop 0
	global_load_lds_dwordx4 v[190:191], off
	s_mov_b32 m0, s43
	s_nop 0
	global_load_lds_dwordx4 v[192:193], off
	s_waitcnt vmcnt(8)
	s_waitcnt lgkmcnt(0)
	s_barrier
	s_setprio 1
	s_waitcnt lgkmcnt(0)
	s_nop 1
	v_mfma_f32_16x16x128_f8f6f4 v[90:93], v[18:25], v[200:207], v[90:93]
	v_mfma_f32_16x16x128_f8f6f4 v[82:85], v[26:33], v[200:207], v[82:85]
	v_mfma_f32_16x16x128_f8f6f4 v[70:73], v[18:25], v[208:215], v[70:73]
	v_mfma_f32_16x16x128_f8f6f4 v[66:69], v[26:33], v[208:215], v[66:69]
	v_mfma_f32_16x16x128_f8f6f4 v[54:57], v[18:25], v[216:223], v[54:57]
	v_mfma_f32_16x16x128_f8f6f4 v[50:53], v[26:33], v[216:223], v[50:53]
	v_mfma_f32_16x16x128_f8f6f4 v[38:41], v[18:25], v[230:237], v[38:41]
	v_mfma_f32_16x16x128_f8f6f4 v[34:37], v[26:33], v[230:237], v[34:37]
	s_nop 1
	v_mfma_f32_16x16x128_f8f6f4 v[94:97], v[2:9], v[200:207], v[94:97]
	v_mfma_f32_16x16x128_f8f6f4 v[86:89], v[10:17], v[200:207], v[86:89]
	v_mfma_f32_16x16x128_f8f6f4 v[78:81], v[2:9], v[208:215], v[78:81]
	v_mfma_f32_16x16x128_f8f6f4 v[74:77], v[10:17], v[208:215], v[74:77]
	v_mfma_f32_16x16x128_f8f6f4 v[62:65], v[2:9], v[216:223], v[62:65]
	v_mfma_f32_16x16x128_f8f6f4 v[58:61], v[10:17], v[216:223], v[58:61]
	v_mfma_f32_16x16x128_f8f6f4 v[46:49], v[2:9], v[230:237], v[46:49]
	v_mfma_f32_16x16x128_f8f6f4 v[42:45], v[10:17], v[230:237], v[42:45]
	s_setprio 0
	s_barrier
	s_add_i32 s60, 0, 0x18000
	s_add_i32 s61, 0, 0x1c000
	v_add_u32_e32 v14, s60, v194
	v_add_u32_e32 v30, s61, v194
	ds_read_b128 v[2:5], v14
	ds_read_b128 v[6:9], v14 offset:1024
	ds_read_b128 v[10:13], v14 offset:2048
	ds_read_b128 v[14:17], v14 offset:3072
	ds_read_b128 v[18:21], v30
	ds_read_b128 v[22:25], v30 offset:1024
	ds_read_b128 v[26:29], v30 offset:2048
	ds_read_b128 v[30:33], v30 offset:3072
	s_mov_b32 m0, s44
	v_lshl_add_u64 v[224:225], s[40:41], 0, v[170:171]
	ds_read_b128 v[200:203], v198 offset:32768
	ds_read_b128 v[204:207], v198 offset:33792
	ds_read_b128 v[208:211], v198 offset:34816
	ds_read_b128 v[212:215], v198 offset:35840
	ds_read_b128 v[216:219], v198 offset:36864
	ds_read_b128 v[220:223], v198 offset:37888
	ds_read_b128 v[230:233], v198 offset:38912
	ds_read_b128 v[234:237], v198 offset:39936
	global_load_lds_dwordx4 v[224:225], off
	v_lshl_add_u64 v[224:225], s[40:41], 0, v[172:173]
	s_mov_b32 m0, s45
	s_nop 0
	global_load_lds_dwordx4 v[224:225], off
	s_waitcnt vmcnt(8)
	s_waitcnt lgkmcnt(0)
	s_barrier
	s_setprio 1
	s_waitcnt lgkmcnt(0)
	s_nop 1
	v_mfma_f32_16x16x128_f8f6f4 v[158:161], v[2:9], v[200:207], v[158:161]
	v_mfma_f32_16x16x128_f8f6f4 v[154:157], v[10:17], v[200:207], v[154:157]
	v_mfma_f32_16x16x128_f8f6f4 v[142:145], v[2:9], v[208:215], v[142:145]
	v_mfma_f32_16x16x128_f8f6f4 v[138:141], v[10:17], v[208:215], v[138:141]
	v_mfma_f32_16x16x128_f8f6f4 v[126:129], v[2:9], v[216:223], v[126:129]
	v_mfma_f32_16x16x128_f8f6f4 v[122:125], v[10:17], v[216:223], v[122:125]
	v_mfma_f32_16x16x128_f8f6f4 v[110:113], v[2:9], v[230:237], v[110:113]
	v_mfma_f32_16x16x128_f8f6f4 v[106:109], v[10:17], v[230:237], v[106:109]
	s_nop 1
	v_mfma_f32_16x16x128_f8f6f4 v[150:153], v[18:25], v[200:207], v[150:153]
	v_mfma_f32_16x16x128_f8f6f4 v[146:149], v[26:33], v[200:207], v[146:149]
	v_mfma_f32_16x16x128_f8f6f4 v[134:137], v[18:25], v[208:215], v[134:137]
	v_mfma_f32_16x16x128_f8f6f4 v[130:133], v[26:33], v[208:215], v[130:133]
	v_mfma_f32_16x16x128_f8f6f4 v[118:121], v[18:25], v[216:223], v[118:121]
	v_mfma_f32_16x16x128_f8f6f4 v[114:117], v[26:33], v[216:223], v[114:117]
	v_mfma_f32_16x16x128_f8f6f4 v[102:105], v[18:25], v[230:237], v[102:105]
	v_mfma_f32_16x16x128_f8f6f4 v[98:101], v[26:33], v[230:237], v[98:101]
	s_setprio 0
	s_barrier
	s_add_i32 s40, s60, s42
	v_lshl_add_u64 v[186:187], v[186:187], 0, s[14:15]
	s_mov_b32 m0, s40
	ds_read_b128 v[200:203], v198 offset:49152
	ds_read_b128 v[204:207], v198 offset:50176
	ds_read_b128 v[208:211], v198 offset:51200
	ds_read_b128 v[212:215], v198 offset:52224
	ds_read_b128 v[216:219], v198 offset:53248
	ds_read_b128 v[220:223], v198 offset:54272
	ds_read_b128 v[230:233], v198 offset:55296
	ds_read_b128 v[234:237], v198 offset:56320
	global_load_lds_dwordx4 v[186:187], off
	s_add_i32 m0, s40, 0x2000
	s_add_u32 s38, s38, 0x40080
	v_lshl_add_u64 v[186:187], v[188:189], 0, s[14:15]
	s_addc_u32 s39, s39, 0
	s_add_i32 s40, s61, s42
	global_load_lds_dwordx4 v[186:187], off
	v_lshl_add_u64 v[186:187], s[38:39], 0, v[162:163]
	s_mov_b32 m0, s40
	s_nop 0
	global_load_lds_dwordx4 v[186:187], off
	v_lshl_add_u64 v[186:187], s[38:39], 0, v[164:165]
	s_add_i32 m0, s40, 0x2000
	s_nop 0
	global_load_lds_dwordx4 v[186:187], off
	v_lshl_add_u64 v[186:187], v[190:191], 0, s[14:15]
	s_mov_b32 m0, s46
	s_nop 0
	global_load_lds_dwordx4 v[186:187], off
	v_lshl_add_u64 v[186:187], v[192:193], 0, s[14:15]
	s_mov_b32 m0, s47
	s_nop 0
	global_load_lds_dwordx4 v[186:187], off
	s_waitcnt vmcnt(8)
	s_waitcnt lgkmcnt(0)
	s_barrier
	s_setprio 1
	s_waitcnt lgkmcnt(0)
	s_nop 1
	v_mfma_f32_16x16x128_f8f6f4 v[90:93], v[2:9], v[200:207], v[90:93]
	v_mfma_f32_16x16x128_f8f6f4 v[82:85], v[10:17], v[200:207], v[82:85]
	v_mfma_f32_16x16x128_f8f6f4 v[70:73], v[2:9], v[208:215], v[70:73]
	v_mfma_f32_16x16x128_f8f6f4 v[66:69], v[10:17], v[208:215], v[66:69]
	v_mfma_f32_16x16x128_f8f6f4 v[54:57], v[2:9], v[216:223], v[54:57]
	v_mfma_f32_16x16x128_f8f6f4 v[50:53], v[10:17], v[216:223], v[50:53]
	v_mfma_f32_16x16x128_f8f6f4 v[38:41], v[2:9], v[230:237], v[38:41]
	v_mfma_f32_16x16x128_f8f6f4 v[34:37], v[10:17], v[230:237], v[34:37]
	s_nop 1
	v_mfma_f32_16x16x128_f8f6f4 v[94:97], v[18:25], v[200:207], v[94:97]
	v_mfma_f32_16x16x128_f8f6f4 v[86:89], v[26:33], v[200:207], v[86:89]
	v_mfma_f32_16x16x128_f8f6f4 v[78:81], v[18:25], v[208:215], v[78:81]
	v_mfma_f32_16x16x128_f8f6f4 v[74:77], v[26:33], v[208:215], v[74:77]
	v_mfma_f32_16x16x128_f8f6f4 v[62:65], v[18:25], v[216:223], v[62:65]
	v_mfma_f32_16x16x128_f8f6f4 v[58:61], v[26:33], v[216:223], v[58:61]
	v_mfma_f32_16x16x128_f8f6f4 v[46:49], v[18:25], v[230:237], v[46:49]
	v_mfma_f32_16x16x128_f8f6f4 v[42:45], v[26:33], v[230:237], v[42:45]
	s_setprio 0
	s_barrier
	s_add_i32 s59, s59, 2
	s_add_u32 s36, s36, 0x100
	s_addc_u32 s37, s37, 0
	s_add_u32 s27, s27, 0x100
	s_addc_u32 s58, s58, 0
	s_cmp_gt_u32 s59, 13
	s_cbranch_scc0 .LBB0_421
	s_and_b64 vcc, exec, s[2:3]
	s_cbranch_vccz .LBB0_424
	s_barrier

.LBB0_459:
	s_and_b64 s[46:47], s[38:39], exec
	s_cselect_b32 s48, s35, s43
	s_cselect_b32 s49, s34, s42
	s_cselect_b32 s66, s37, s45
	s_cselect_b32 s67, s36, s44
	s_add_u32 s42, s42, 0x80
	s_addc_u32 s43, s43, 0
	s_add_u32 s68, s44, 0x100
	s_addc_u32 s69, s45, 0
	s_mov_b32 s70, -2
	ds_read_b128 v[18:21], v194
	ds_read_b128 v[22:25], v194 offset:1024
	ds_read_b128 v[26:29], v194 offset:2048
	ds_read_b128 v[30:33], v194 offset:3072
	ds_read_b128 v[2:5], v195
	ds_read_b128 v[6:9], v195 offset:1024
	ds_read_b128 v[10:13], v195 offset:2048
	ds_read_b128 v[14:17], v195 offset:3072
	s_add_u32 s44, s42, 0x80
	s_addc_u32 s45, s43, 0
	s_cmp_eq_u32 s70, 12
	s_cselect_b32 s47, s48, s45
	s_cselect_b32 s46, s49, s44
	s_cselect_b32 s45, s66, s69
	s_cselect_b32 s44, s67, s68
	v_lshl_add_u64 v[222:223], s[42:43], 0, v[180:181]
	s_add_i32 m0, s41, 0xc000
	ds_read_b128 v[184:187], v196
	ds_read_b128 v[188:191], v196 offset:1024
	ds_read_b128 v[198:201], v196 offset:2048
	ds_read_b128 v[202:205], v196 offset:3072
	ds_read_b128 v[206:209], v196 offset:4096
	ds_read_b128 v[210:213], v196 offset:5120
	ds_read_b128 v[214:217], v196 offset:6144
	ds_read_b128 v[218:221], v196 offset:7168
	global_load_lds_dwordx4 v[222:223], off
	v_lshl_add_u64 v[222:223], s[42:43], 0, v[178:179]
	s_add_i32 m0, s41, 0xe000
	s_nop 0
	global_load_lds_dwordx4 v[222:223], off
	s_waitcnt vmcnt(8)
	s_waitcnt lgkmcnt(0)
	s_barrier
	s_setprio 1
	s_waitcnt lgkmcnt(0)
	s_nop 1
	v_mfma_f32_16x16x128_f8f6f4 v[158:161], v[18:25], v[184:191], 0
	v_mfma_f32_16x16x128_f8f6f4 v[154:157], v[26:33], v[184:191], 0
	v_mfma_f32_16x16x128_f8f6f4 v[142:145], v[18:25], v[198:205], 0
	v_mfma_f32_16x16x128_f8f6f4 v[138:141], v[26:33], v[198:205], 0
	v_mfma_f32_16x16x128_f8f6f4 v[126:129], v[18:25], v[206:213], 0
	v_mfma_f32_16x16x128_f8f6f4 v[122:125], v[26:33], v[206:213], 0
	v_mfma_f32_16x16x128_f8f6f4 v[110:113], v[18:25], v[214:221], 0
	v_mfma_f32_16x16x128_f8f6f4 v[106:109], v[26:33], v[214:221], 0
	s_nop 1
	v_mfma_f32_16x16x128_f8f6f4 v[150:153], v[2:9], v[184:191], 0
	v_mfma_f32_16x16x128_f8f6f4 v[146:149], v[10:17], v[184:191], 0
	v_mfma_f32_16x16x128_f8f6f4 v[134:137], v[2:9], v[198:205], 0
	v_mfma_f32_16x16x128_f8f6f4 v[130:133], v[10:17], v[198:205], 0
	v_mfma_f32_16x16x128_f8f6f4 v[118:121], v[2:9], v[206:213], 0
	v_mfma_f32_16x16x128_f8f6f4 v[114:117], v[10:17], v[206:213], 0
	v_mfma_f32_16x16x128_f8f6f4 v[102:105], v[2:9], v[214:221], 0
	v_mfma_f32_16x16x128_f8f6f4 v[98:101], v[10:17], v[214:221], 0
	s_setprio 0
	s_barrier
	s_add_i32 s71, s61, s53
	v_lshl_add_u64 v[184:185], s[44:45], 0, v[162:163]
	s_mov_b32 m0, s71
	ds_read_b128 v[198:201], v196 offset:16384
	ds_read_b128 v[202:205], v196 offset:17408
	ds_read_b128 v[206:209], v196 offset:18432
	ds_read_b128 v[210:213], v196 offset:19456
	ds_read_b128 v[214:217], v196 offset:20480
	ds_read_b128 v[218:221], v196 offset:21504
	ds_read_b128 v[230:233], v196 offset:22528
	ds_read_b128 v[234:237], v196 offset:23552
	global_load_lds_dwordx4 v[184:185], off
	s_add_i32 m0, s71, 0x2000
	s_add_u32 s72, s44, 0x40000
	v_lshl_add_u64 v[186:187], s[44:45], 0, v[164:165]
	s_addc_u32 s73, s45, 0
	s_add_i32 s71, s62, s53
	global_load_lds_dwordx4 v[186:187], off
	v_lshl_add_u64 v[188:189], s[72:73], 0, v[162:163]
	s_mov_b32 m0, s71
	v_lshl_add_u64 v[190:191], s[46:47], 0, v[168:169]
	global_load_lds_dwordx4 v[188:189], off
	v_lshl_add_u64 v[188:189], s[72:73], 0, v[164:165]
	s_add_i32 m0, s71, 0x2000
	s_nop 0
	global_load_lds_dwordx4 v[188:189], off
	v_lshl_add_u64 v[188:189], s[46:47], 0, v[166:167]
	s_mov_b32 m0, s41
	s_nop 0
	global_load_lds_dwordx4 v[188:189], off
	s_mov_b32 m0, s54
	s_nop 0
	global_load_lds_dwordx4 v[190:191], off
	s_waitcnt vmcnt(8)
	s_waitcnt lgkmcnt(0)
	s_barrier
	s_setprio 1
	s_waitcnt lgkmcnt(0)
	s_nop 1
	v_mfma_f32_16x16x128_f8f6f4 v[90:93], v[18:25], v[198:205], 0
	v_mfma_f32_16x16x128_f8f6f4 v[82:85], v[26:33], v[198:205], 0
	v_mfma_f32_16x16x128_f8f6f4 v[70:73], v[18:25], v[206:213], 0
	v_mfma_f32_16x16x128_f8f6f4 v[66:69], v[26:33], v[206:213], 0
	v_mfma_f32_16x16x128_f8f6f4 v[54:57], v[18:25], v[214:221], 0
	v_mfma_f32_16x16x128_f8f6f4 v[50:53], v[26:33], v[214:221], 0
	v_mfma_f32_16x16x128_f8f6f4 v[38:41], v[18:25], v[230:237], 0
	v_mfma_f32_16x16x128_f8f6f4 v[34:37], v[26:33], v[230:237], 0
	s_nop 1
	v_mfma_f32_16x16x128_f8f6f4 v[94:97], v[2:9], v[198:205], 0
	v_mfma_f32_16x16x128_f8f6f4 v[86:89], v[10:17], v[198:205], 0
	v_mfma_f32_16x16x128_f8f6f4 v[78:81], v[2:9], v[206:213], 0
	v_mfma_f32_16x16x128_f8f6f4 v[74:77], v[10:17], v[206:213], 0
	v_mfma_f32_16x16x128_f8f6f4 v[62:65], v[2:9], v[214:221], 0
	v_mfma_f32_16x16x128_f8f6f4 v[58:61], v[10:17], v[214:221], 0
	v_mfma_f32_16x16x128_f8f6f4 v[46:49], v[2:9], v[230:237], 0
	v_mfma_f32_16x16x128_f8f6f4 v[42:45], v[10:17], v[230:237], 0
	s_setprio 0
	s_barrier
	s_add_i32 s71, 0, 0x18000
	s_add_i32 s72, 0, 0x1c000
	v_add_u32_e32 v14, s71, v192
	v_add_u32_e32 v30, s72, v192
	ds_read_b128 v[2:5], v14
	ds_read_b128 v[6:9], v14 offset:1024
	ds_read_b128 v[10:13], v14 offset:2048
	ds_read_b128 v[14:17], v14 offset:3072
	ds_read_b128 v[18:21], v30
	ds_read_b128 v[22:25], v30 offset:1024
	ds_read_b128 v[26:29], v30 offset:2048
	ds_read_b128 v[30:33], v30 offset:3072
	s_mov_b32 m0, s55
	v_lshl_add_u64 v[222:223], s[46:47], 0, v[170:171]
	ds_read_b128 v[198:201], v196 offset:32768
	ds_read_b128 v[202:205], v196 offset:33792
	ds_read_b128 v[206:209], v196 offset:34816
	ds_read_b128 v[210:213], v196 offset:35840
	ds_read_b128 v[214:217], v196 offset:36864
	ds_read_b128 v[218:221], v196 offset:37888
	ds_read_b128 v[230:233], v196 offset:38912
	ds_read_b128 v[234:237], v196 offset:39936
	global_load_lds_dwordx4 v[222:223], off
	v_lshl_add_u64 v[222:223], s[46:47], 0, v[172:173]
	s_mov_b32 m0, s58
	s_nop 0
	global_load_lds_dwordx4 v[222:223], off
	s_waitcnt vmcnt(8)
	s_waitcnt lgkmcnt(0)
	s_barrier
	s_setprio 1
	s_waitcnt lgkmcnt(0)
	s_nop 1
	v_mfma_f32_16x16x128_f8f6f4 v[158:161], v[2:9], v[198:205], v[158:161]
	v_mfma_f32_16x16x128_f8f6f4 v[154:157], v[10:17], v[198:205], v[154:157]
	v_mfma_f32_16x16x128_f8f6f4 v[142:145], v[2:9], v[206:213], v[142:145]
	v_mfma_f32_16x16x128_f8f6f4 v[138:141], v[10:17], v[206:213], v[138:141]
	v_mfma_f32_16x16x128_f8f6f4 v[126:129], v[2:9], v[214:221], v[126:129]
	v_mfma_f32_16x16x128_f8f6f4 v[122:125], v[10:17], v[214:221], v[122:125]
	v_mfma_f32_16x16x128_f8f6f4 v[110:113], v[2:9], v[230:237], v[110:113]
	v_mfma_f32_16x16x128_f8f6f4 v[106:109], v[10:17], v[230:237], v[106:109]
	s_nop 1
	v_mfma_f32_16x16x128_f8f6f4 v[150:153], v[18:25], v[198:205], v[150:153]
	v_mfma_f32_16x16x128_f8f6f4 v[146:149], v[26:33], v[198:205], v[146:149]
	v_mfma_f32_16x16x128_f8f6f4 v[134:137], v[18:25], v[206:213], v[134:137]
	v_mfma_f32_16x16x128_f8f6f4 v[130:133], v[26:33], v[206:213], v[130:133]
	v_mfma_f32_16x16x128_f8f6f4 v[118:121], v[18:25], v[214:221], v[118:121]
	v_mfma_f32_16x16x128_f8f6f4 v[114:117], v[26:33], v[214:221], v[114:117]
	v_mfma_f32_16x16x128_f8f6f4 v[102:105], v[18:25], v[230:237], v[102:105]
	v_mfma_f32_16x16x128_f8f6f4 v[98:101], v[26:33], v[230:237], v[98:101]
	s_setprio 0
	s_barrier
	s_add_i32 s46, s71, s53
	v_lshl_add_u64 v[184:185], v[184:185], 0, s[12:13]
	s_mov_b32 m0, s46
	ds_read_b128 v[198:201], v196 offset:49152
	ds_read_b128 v[202:205], v196 offset:50176
	ds_read_b128 v[206:209], v196 offset:51200
	ds_read_b128 v[210:213], v196 offset:52224
	ds_read_b128 v[214:217], v196 offset:53248
	ds_read_b128 v[218:221], v196 offset:54272
	ds_read_b128 v[230:233], v196 offset:55296
	ds_read_b128 v[234:237], v196 offset:56320
	global_load_lds_dwordx4 v[184:185], off
	s_add_i32 m0, s46, 0x2000
	s_add_u32 s44, s44, 0x40080
	v_lshl_add_u64 v[184:185], v[186:187], 0, s[12:13]
	s_addc_u32 s45, s45, 0
	s_add_i32 s46, s72, s53
	global_load_lds_dwordx4 v[184:185], off
	v_lshl_add_u64 v[184:185], s[44:45], 0, v[162:163]
	s_mov_b32 m0, s46
	s_nop 0
	global_load_lds_dwordx4 v[184:185], off
	v_lshl_add_u64 v[184:185], s[44:45], 0, v[164:165]
	s_add_i32 m0, s46, 0x2000
	s_nop 0
	global_load_lds_dwordx4 v[184:185], off
	v_lshl_add_u64 v[184:185], v[188:189], 0, s[12:13]
	s_mov_b32 m0, s59
	s_nop 0
	global_load_lds_dwordx4 v[184:185], off
	v_lshl_add_u64 v[184:185], v[190:191], 0, s[12:13]
	s_mov_b32 m0, s60
	s_nop 0
	global_load_lds_dwordx4 v[184:185], off
	s_waitcnt vmcnt(8)
	s_waitcnt lgkmcnt(0)
	s_barrier
	s_setprio 1
	s_waitcnt lgkmcnt(0)
	s_nop 1
	v_mfma_f32_16x16x128_f8f6f4 v[90:93], v[2:9], v[198:205], v[90:93]
	v_mfma_f32_16x16x128_f8f6f4 v[82:85], v[10:17], v[198:205], v[82:85]
	v_mfma_f32_16x16x128_f8f6f4 v[70:73], v[2:9], v[206:213], v[70:73]
	v_mfma_f32_16x16x128_f8f6f4 v[66:69], v[10:17], v[206:213], v[66:69]
	v_mfma_f32_16x16x128_f8f6f4 v[54:57], v[2:9], v[214:221], v[54:57]
	v_mfma_f32_16x16x128_f8f6f4 v[50:53], v[10:17], v[214:221], v[50:53]
	v_mfma_f32_16x16x128_f8f6f4 v[38:41], v[2:9], v[230:237], v[38:41]
	v_mfma_f32_16x16x128_f8f6f4 v[34:37], v[10:17], v[230:237], v[34:37]
	s_nop 1
	v_mfma_f32_16x16x128_f8f6f4 v[94:97], v[18:25], v[198:205], v[94:97]
	v_mfma_f32_16x16x128_f8f6f4 v[86:89], v[26:33], v[198:205], v[86:89]
	v_mfma_f32_16x16x128_f8f6f4 v[78:81], v[18:25], v[206:213], v[78:81]
	v_mfma_f32_16x16x128_f8f6f4 v[74:77], v[26:33], v[206:213], v[74:77]
	v_mfma_f32_16x16x128_f8f6f4 v[62:65], v[18:25], v[214:221], v[62:65]
	v_mfma_f32_16x16x128_f8f6f4 v[58:61], v[26:33], v[214:221], v[58:61]
	v_mfma_f32_16x16x128_f8f6f4 v[46:49], v[18:25], v[230:237], v[46:49]
	v_mfma_f32_16x16x128_f8f6f4 v[42:45], v[26:33], v[230:237], v[42:45]
	s_setprio 0
	s_barrier
	s_add_i32 s70, s70, 2
	s_add_u32 s42, s42, 0x100
	s_addc_u32 s43, s43, 0
	s_add_u32 s68, s68, 0x100
	s_addc_u32 s69, s69, 0
	s_cmp_gt_u32 s70, 13
	s_cbranch_scc0 .LBB0_460
	s_branch .Lmy_pexit_p1b
.LBB0_460:
	ds_read_b128 v[18:21], v194
	ds_read_b128 v[22:25], v194 offset:1024
	ds_read_b128 v[26:29], v194 offset:2048
	ds_read_b128 v[30:33], v194 offset:3072
	ds_read_b128 v[2:5], v195
	ds_read_b128 v[6:9], v195 offset:1024
	ds_read_b128 v[10:13], v195 offset:2048
	ds_read_b128 v[14:17], v195 offset:3072
	s_add_u32 s44, s42, 0x80
	s_addc_u32 s45, s43, 0
	s_cmp_eq_u32 s70, 12
	s_cselect_b32 s47, s48, s45
	s_cselect_b32 s46, s49, s44
	s_cselect_b32 s45, s66, s69
	s_cselect_b32 s44, s67, s68
	v_lshl_add_u64 v[222:223], s[42:43], 0, v[180:181]
	s_add_i32 m0, s41, 0xc000
	ds_read_b128 v[184:187], v196
	ds_read_b128 v[188:191], v196 offset:1024
	ds_read_b128 v[198:201], v196 offset:2048
	ds_read_b128 v[202:205], v196 offset:3072
	ds_read_b128 v[206:209], v196 offset:4096
	ds_read_b128 v[210:213], v196 offset:5120
	ds_read_b128 v[214:217], v196 offset:6144
	ds_read_b128 v[218:221], v196 offset:7168
	global_load_lds_dwordx4 v[222:223], off
	v_lshl_add_u64 v[222:223], s[42:43], 0, v[178:179]
	s_add_i32 m0, s41, 0xe000
	s_nop 0
	global_load_lds_dwordx4 v[222:223], off
	s_waitcnt vmcnt(8)
	s_waitcnt lgkmcnt(0)
	s_barrier
	s_setprio 1
	s_waitcnt lgkmcnt(0)
	s_nop 1
	v_mfma_f32_16x16x128_f8f6f4 v[158:161], v[18:25], v[184:191], v[158:161]
	v_mfma_f32_16x16x128_f8f6f4 v[154:157], v[26:33], v[184:191], v[154:157]
	v_mfma_f32_16x16x128_f8f6f4 v[142:145], v[18:25], v[198:205], v[142:145]
	v_mfma_f32_16x16x128_f8f6f4 v[138:141], v[26:33], v[198:205], v[138:141]
	v_mfma_f32_16x16x128_f8f6f4 v[126:129], v[18:25], v[206:213], v[126:129]
	v_mfma_f32_16x16x128_f8f6f4 v[122:125], v[26:33], v[206:213], v[122:125]
	v_mfma_f32_16x16x128_f8f6f4 v[110:113], v[18:25], v[214:221], v[110:113]
	v_mfma_f32_16x16x128_f8f6f4 v[106:109], v[26:33], v[214:221], v[106:109]
	s_nop 1
	v_mfma_f32_16x16x128_f8f6f4 v[150:153], v[2:9], v[184:191], v[150:153]
	v_mfma_f32_16x16x128_f8f6f4 v[146:149], v[10:17], v[184:191], v[146:149]
	v_mfma_f32_16x16x128_f8f6f4 v[134:137], v[2:9], v[198:205], v[134:137]
	v_mfma_f32_16x16x128_f8f6f4 v[130:133], v[10:17], v[198:205], v[130:133]
	v_mfma_f32_16x16x128_f8f6f4 v[118:121], v[2:9], v[206:213], v[118:121]
	v_mfma_f32_16x16x128_f8f6f4 v[114:117], v[10:17], v[206:213], v[114:117]
	v_mfma_f32_16x16x128_f8f6f4 v[102:105], v[2:9], v[214:221], v[102:105]
	v_mfma_f32_16x16x128_f8f6f4 v[98:101], v[10:17], v[214:221], v[98:101]
	s_setprio 0
	s_barrier
	s_add_i32 s71, s61, s53
	v_lshl_add_u64 v[184:185], s[44:45], 0, v[162:163]
	s_mov_b32 m0, s71
	ds_read_b128 v[198:201], v196 offset:16384
	ds_read_b128 v[202:205], v196 offset:17408
	ds_read_b128 v[206:209], v196 offset:18432
	ds_read_b128 v[210:213], v196 offset:19456
	ds_read_b128 v[214:217], v196 offset:20480
	ds_read_b128 v[218:221], v196 offset:21504
	ds_read_b128 v[230:233], v196 offset:22528
	ds_read_b128 v[234:237], v196 offset:23552
	global_load_lds_dwordx4 v[184:185], off
	s_add_i32 m0, s71, 0x2000
	s_add_u32 s72, s44, 0x40000
	v_lshl_add_u64 v[186:187], s[44:45], 0, v[164:165]
	s_addc_u32 s73, s45, 0
	s_add_i32 s71, s62, s53
	global_load_lds_dwordx4 v[186:187], off
	v_lshl_add_u64 v[188:189], s[72:73], 0, v[162:163]
	s_mov_b32 m0, s71
	v_lshl_add_u64 v[190:191], s[46:47], 0, v[168:169]
	global_load_lds_dwordx4 v[188:189], off
	v_lshl_add_u64 v[188:189], s[72:73], 0, v[164:165]
	s_add_i32 m0, s71, 0x2000
	s_nop 0
	global_load_lds_dwordx4 v[188:189], off
	v_lshl_add_u64 v[188:189], s[46:47], 0, v[166:167]
	s_mov_b32 m0, s41
	s_nop 0
	global_load_lds_dwordx4 v[188:189], off
	s_mov_b32 m0, s54
	s_nop 0
	global_load_lds_dwordx4 v[190:191], off
	s_waitcnt vmcnt(8)
	s_waitcnt lgkmcnt(0)
	s_barrier
	s_setprio 1
	s_waitcnt lgkmcnt(0)
	s_nop 1
	v_mfma_f32_16x16x128_f8f6f4 v[90:93], v[18:25], v[198:205], v[90:93]
	v_mfma_f32_16x16x128_f8f6f4 v[82:85], v[26:33], v[198:205], v[82:85]
	v_mfma_f32_16x16x128_f8f6f4 v[70:73], v[18:25], v[206:213], v[70:73]
	v_mfma_f32_16x16x128_f8f6f4 v[66:69], v[26:33], v[206:213], v[66:69]
	v_mfma_f32_16x16x128_f8f6f4 v[54:57], v[18:25], v[214:221], v[54:57]
	v_mfma_f32_16x16x128_f8f6f4 v[50:53], v[26:33], v[214:221], v[50:53]
	v_mfma_f32_16x16x128_f8f6f4 v[38:41], v[18:25], v[230:237], v[38:41]
	v_mfma_f32_16x16x128_f8f6f4 v[34:37], v[26:33], v[230:237], v[34:37]
	s_nop 1
	v_mfma_f32_16x16x128_f8f6f4 v[94:97], v[2:9], v[198:205], v[94:97]
	v_mfma_f32_16x16x128_f8f6f4 v[86:89], v[10:17], v[198:205], v[86:89]
	v_mfma_f32_16x16x128_f8f6f4 v[78:81], v[2:9], v[206:213], v[78:81]
	v_mfma_f32_16x16x128_f8f6f4 v[74:77], v[10:17], v[206:213], v[74:77]
	v_mfma_f32_16x16x128_f8f6f4 v[62:65], v[2:9], v[214:221], v[62:65]
	v_mfma_f32_16x16x128_f8f6f4 v[58:61], v[10:17], v[214:221], v[58:61]
	v_mfma_f32_16x16x128_f8f6f4 v[46:49], v[2:9], v[230:237], v[46:49]
	v_mfma_f32_16x16x128_f8f6f4 v[42:45], v[10:17], v[230:237], v[42:45]
	s_setprio 0
	s_barrier
	s_add_i32 s71, 0, 0x18000
	s_add_i32 s72, 0, 0x1c000
	v_add_u32_e32 v14, s71, v192
	v_add_u32_e32 v30, s72, v192
	ds_read_b128 v[2:5], v14
	ds_read_b128 v[6:9], v14 offset:1024
	ds_read_b128 v[10:13], v14 offset:2048
	ds_read_b128 v[14:17], v14 offset:3072
	ds_read_b128 v[18:21], v30
	ds_read_b128 v[22:25], v30 offset:1024
	ds_read_b128 v[26:29], v30 offset:2048
	ds_read_b128 v[30:33], v30 offset:3072
	s_mov_b32 m0, s55
	v_lshl_add_u64 v[222:223], s[46:47], 0, v[170:171]
	ds_read_b128 v[198:201], v196 offset:32768
	ds_read_b128 v[202:205], v196 offset:33792
	ds_read_b128 v[206:209], v196 offset:34816
	ds_read_b128 v[210:213], v196 offset:35840
	ds_read_b128 v[214:217], v196 offset:36864
	ds_read_b128 v[218:221], v196 offset:37888
	ds_read_b128 v[230:233], v196 offset:38912
	ds_read_b128 v[234:237], v196 offset:39936
	global_load_lds_dwordx4 v[222:223], off
	v_lshl_add_u64 v[222:223], s[46:47], 0, v[172:173]
	s_mov_b32 m0, s58
	s_nop 0
	global_load_lds_dwordx4 v[222:223], off
	s_waitcnt vmcnt(8)
	s_waitcnt lgkmcnt(0)
	s_barrier
	s_setprio 1
	s_waitcnt lgkmcnt(0)
	s_nop 1
	v_mfma_f32_16x16x128_f8f6f4 v[158:161], v[2:9], v[198:205], v[158:161]
	v_mfma_f32_16x16x128_f8f6f4 v[154:157], v[10:17], v[198:205], v[154:157]
	v_mfma_f32_16x16x128_f8f6f4 v[142:145], v[2:9], v[206:213], v[142:145]
	v_mfma_f32_16x16x128_f8f6f4 v[138:141], v[10:17], v[206:213], v[138:141]
	v_mfma_f32_16x16x128_f8f6f4 v[126:129], v[2:9], v[214:221], v[126:129]
	v_mfma_f32_16x16x128_f8f6f4 v[122:125], v[10:17], v[214:221], v[122:125]
	v_mfma_f32_16x16x128_f8f6f4 v[110:113], v[2:9], v[230:237], v[110:113]
	v_mfma_f32_16x16x128_f8f6f4 v[106:109], v[10:17], v[230:237], v[106:109]
	s_nop 1
	v_mfma_f32_16x16x128_f8f6f4 v[150:153], v[18:25], v[198:205], v[150:153]
	v_mfma_f32_16x16x128_f8f6f4 v[146:149], v[26:33], v[198:205], v[146:149]
	v_mfma_f32_16x16x128_f8f6f4 v[134:137], v[18:25], v[206:213], v[134:137]
	v_mfma_f32_16x16x128_f8f6f4 v[130:133], v[26:33], v[206:213], v[130:133]
	v_mfma_f32_16x16x128_f8f6f4 v[118:121], v[18:25], v[214:221], v[118:121]
	v_mfma_f32_16x16x128_f8f6f4 v[114:117], v[26:33], v[214:221], v[114:117]
	v_mfma_f32_16x16x128_f8f6f4 v[102:105], v[18:25], v[230:237], v[102:105]
	v_mfma_f32_16x16x128_f8f6f4 v[98:101], v[26:33], v[230:237], v[98:101]
	s_setprio 0
	s_barrier
	s_add_i32 s46, s71, s53
	v_lshl_add_u64 v[184:185], v[184:185], 0, s[12:13]
	s_mov_b32 m0, s46
	ds_read_b128 v[198:201], v196 offset:49152
	ds_read_b128 v[202:205], v196 offset:50176
	ds_read_b128 v[206:209], v196 offset:51200
	ds_read_b128 v[210:213], v196 offset:52224
	ds_read_b128 v[214:217], v196 offset:53248
	ds_read_b128 v[218:221], v196 offset:54272
	ds_read_b128 v[230:233], v196 offset:55296
	ds_read_b128 v[234:237], v196 offset:56320
	global_load_lds_dwordx4 v[184:185], off
	s_add_i32 m0, s46, 0x2000
	s_add_u32 s44, s44, 0x40080
	v_lshl_add_u64 v[184:185], v[186:187], 0, s[12:13]
	s_addc_u32 s45, s45, 0
	s_add_i32 s46, s72, s53
	global_load_lds_dwordx4 v[184:185], off
	v_lshl_add_u64 v[184:185], s[44:45], 0, v[162:163]
	s_mov_b32 m0, s46
	s_nop 0
	global_load_lds_dwordx4 v[184:185], off
	v_lshl_add_u64 v[184:185], s[44:45], 0, v[164:165]
	s_add_i32 m0, s46, 0x2000
	s_nop 0
	global_load_lds_dwordx4 v[184:185], off
	v_lshl_add_u64 v[184:185], v[188:189], 0, s[12:13]
	s_mov_b32 m0, s59
	s_nop 0
	global_load_lds_dwordx4 v[184:185], off
	v_lshl_add_u64 v[184:185], v[190:191], 0, s[12:13]
	s_mov_b32 m0, s60
	s_nop 0
	global_load_lds_dwordx4 v[184:185], off
	s_waitcnt vmcnt(8)
	s_waitcnt lgkmcnt(0)
	s_barrier
	s_setprio 1
	s_waitcnt lgkmcnt(0)
	s_nop 1
	v_mfma_f32_16x16x128_f8f6f4 v[90:93], v[2:9], v[198:205], v[90:93]
	v_mfma_f32_16x16x128_f8f6f4 v[82:85], v[10:17], v[198:205], v[82:85]
	v_mfma_f32_16x16x128_f8f6f4 v[70:73], v[2:9], v[206:213], v[70:73]
	v_mfma_f32_16x16x128_f8f6f4 v[66:69], v[10:17], v[206:213], v[66:69]
	v_mfma_f32_16x16x128_f8f6f4 v[54:57], v[2:9], v[214:221], v[54:57]
	v_mfma_f32_16x16x128_f8f6f4 v[50:53], v[10:17], v[214:221], v[50:53]
	v_mfma_f32_16x16x128_f8f6f4 v[38:41], v[2:9], v[230:237], v[38:41]
	v_mfma_f32_16x16x128_f8f6f4 v[34:37], v[10:17], v[230:237], v[34:37]
	s_nop 1
	v_mfma_f32_16x16x128_f8f6f4 v[94:97], v[18:25], v[198:205], v[94:97]
	v_mfma_f32_16x16x128_f8f6f4 v[86:89], v[26:33], v[198:205], v[86:89]
	v_mfma_f32_16x16x128_f8f6f4 v[78:81], v[18:25], v[206:213], v[78:81]
	v_mfma_f32_16x16x128_f8f6f4 v[74:77], v[26:33], v[206:213], v[74:77]
	v_mfma_f32_16x16x128_f8f6f4 v[62:65], v[18:25], v[214:221], v[62:65]
	v_mfma_f32_16x16x128_f8f6f4 v[58:61], v[26:33], v[214:221], v[58:61]
	v_mfma_f32_16x16x128_f8f6f4 v[46:49], v[18:25], v[230:237], v[46:49]
	v_mfma_f32_16x16x128_f8f6f4 v[42:45], v[26:33], v[230:237], v[42:45]
	s_setprio 0
	s_barrier
	s_add_i32 s70, s70, 2
	s_add_u32 s42, s42, 0x100
	s_addc_u32 s43, s43, 0
	s_add_u32 s68, s68, 0x100
	s_addc_u32 s69, s69, 0
	s_cmp_gt_u32 s70, 13
	s_cbranch_scc0 .LBB0_460

.LBB0_746:
	v_lshrrev_b32_e32 v7, 1, v6
	v_and_b32_e32 v133, 24, v7
	v_and_b32_e32 v132, 15, v6
	v_lshlrev_b32_e32 v7, 1, v133
	v_lshlrev_b32_e32 v6, 2, v6
	v_lshl_or_b32 v7, v132, 6, v7
	s_lshl_b32 s22, s33, 13
	v_and_b32_e32 v6, 32, v6
	v_bitop3_b32 v32, v7, s22, v6 bitop3:0xde
	s_lshl_b32 s22, s35, 5
	s_add_i32 s39, s86, s48
	s_and_b32 s35, s22, 0x60
	v_lshl_add_u64 v[8:9], v[28:29], 0, s[0:1]
	s_mov_b32 m0, s39
	s_add_i32 s41, s39, 0x2000
	s_lshl_b32 s22, s35, 7
	s_waitcnt vmcnt(2)
	s_barrier
	global_load_lds_dwordx4 v[8:9], off
	v_lshl_add_u64 v[10:11], v[30:31], 0, s[0:1]
	s_mov_b32 m0, s41
	s_add_i32 s40, s38, 0x8000
	s_add_i32 s42, s38, 0xa000
	v_bitop3_b32 v33, v7, s22, v6 bitop3:0xde
	global_load_lds_dwordx4 v[10:11], off
	v_lshl_add_u64 v[6:7], v[22:23], 0, s[0:1]
	s_mov_b32 m0, s40
	s_add_u32 s22, s20, 0x100080
	global_load_lds_dwordx4 v[6:7], off
	v_lshl_add_u64 v[12:13], v[24:25], 0, s[0:1]
	s_mov_b32 m0, s42
	s_addc_u32 s23, s21, 0
	s_add_i32 s43, s87, s48
	global_load_lds_dwordx4 v[12:13], off
	v_lshl_add_u64 v[14:15], s[22:23], 0, v[130:131]
	s_mov_b32 m0, s43
	s_add_i32 s44, s43, 0x2000
	global_load_lds_dwordx4 v[14:15], off
	v_lshl_add_u64 v[16:17], s[22:23], 0, v[18:19]
	s_mov_b32 m0, s44
	v_add_u32_e32 v235, s3, v33
	global_load_lds_dwordx4 v[16:17], off
	s_waitcnt vmcnt(6)
	s_barrier
	v_add_u32_e32 v226, 0, v32
	v_add_u32_e32 v227, s87, v33
	v_add_u32_e32 v229, s86, v33
	v_add_u32_e32 v234, s2, v33
	ds_read_b128 v[32:35], v235
	ds_read_b128 v[36:39], v235 offset:1024
	ds_read_b128 v[40:43], v235 offset:2048
	ds_read_b128 v[44:47], v235 offset:3072
	ds_read_b128 v[48:51], v234
	ds_read_b128 v[52:55], v234 offset:1024
	ds_read_b128 v[56:59], v234 offset:2048
	ds_read_b128 v[60:63], v234 offset:3072
	s_add_i32 s47, s3, s48
	s_add_i32 s52, s38, 0xc000
	s_add_i32 s50, s38, 0xe000
	s_add_i32 s46, s47, 0x2000
	s_add_u32 s22, s20, 0x100100
	s_addc_u32 s23, s21, 0
	s_add_i32 s49, s2, s48
	s_add_i32 s48, s49, 0x2000
	s_add_u32 s20, s20, 0x100180
	s_addc_u32 s21, s21, 0
	s_cmpk_gt_u32 s51, 0xff
	s_mov_b32 m0, s52
	v_lshl_add_u64 v[96:97], v[2:3], 0, s[0:1]
	ds_read_b128 v[64:67], v226
	ds_read_b128 v[68:71], v226 offset:1024
	ds_read_b128 v[72:75], v226 offset:2048
	ds_read_b128 v[76:79], v226 offset:3072
	ds_read_b128 v[80:83], v226 offset:4096
	ds_read_b128 v[84:87], v226 offset:5120
	ds_read_b128 v[88:91], v226 offset:6144
	ds_read_b128 v[92:95], v226 offset:7168
	global_load_lds_dwordx4 v[96:97], off
	v_lshl_add_u64 v[96:97], v[4:5], 0, s[0:1]
	s_mov_b32 m0, s50
	s_nop 0
	global_load_lds_dwordx4 v[96:97], off
	s_waitcnt vmcnt(8)
	s_waitcnt lgkmcnt(0)
	s_barrier
	s_setprio 1
	s_waitcnt lgkmcnt(0)
	v_mfma_f32_16x16x32_bf16 v[96:99], v[32:35], v[64:67], 0
	v_mfma_f32_16x16x32_bf16 v[100:103], v[40:43], v[64:67], 0
	v_mfma_f32_16x16x32_bf16 v[104:107], v[32:35], v[72:75], 0
	v_mfma_f32_16x16x32_bf16 v[108:111], v[40:43], v[72:75], 0
	v_mfma_f32_16x16x32_bf16 v[112:115], v[32:35], v[80:83], 0
	v_mfma_f32_16x16x32_bf16 v[116:119], v[40:43], v[80:83], 0
	v_mfma_f32_16x16x32_bf16 v[120:123], v[32:35], v[88:91], 0
	v_mfma_f32_16x16x32_bf16 v[124:127], v[40:43], v[88:91], 0
	v_mfma_f32_16x16x32_bf16 v[96:99], v[36:39], v[68:71], v[96:99]
	v_mfma_f32_16x16x32_bf16 v[100:103], v[44:47], v[68:71], v[100:103]
	v_mfma_f32_16x16x32_bf16 v[104:107], v[36:39], v[76:79], v[104:107]
	v_mfma_f32_16x16x32_bf16 v[108:111], v[44:47], v[76:79], v[108:111]
	v_mfma_f32_16x16x32_bf16 v[112:115], v[36:39], v[84:87], v[112:115]
	v_mfma_f32_16x16x32_bf16 v[116:119], v[44:47], v[84:87], v[116:119]
	v_mfma_f32_16x16x32_bf16 v[120:123], v[36:39], v[92:95], v[120:123]
	v_mfma_f32_16x16x32_bf16 v[124:127], v[44:47], v[92:95], v[124:127]
	v_mfma_f32_16x16x32_bf16 v[134:137], v[48:51], v[64:67], 0
	v_mfma_f32_16x16x32_bf16 v[64:67], v[56:59], v[64:67], 0
	v_mfma_f32_16x16x32_bf16 v[134:137], v[52:55], v[68:71], v[134:137]
	v_mfma_f32_16x16x32_bf16 v[64:67], v[60:63], v[68:71], v[64:67]
	v_mfma_f32_16x16x32_bf16 v[68:71], v[48:51], v[72:75], 0
	v_mfma_f32_16x16x32_bf16 v[72:75], v[56:59], v[72:75], 0
	v_mfma_f32_16x16x32_bf16 v[68:71], v[52:55], v[76:79], v[68:71]
	v_mfma_f32_16x16x32_bf16 v[72:75], v[60:63], v[76:79], v[72:75]
	v_mfma_f32_16x16x32_bf16 v[76:79], v[48:51], v[80:83], 0
	v_mfma_f32_16x16x32_bf16 v[80:83], v[56:59], v[80:83], 0
	v_mfma_f32_16x16x32_bf16 v[76:79], v[52:55], v[84:87], v[76:79]
	v_mfma_f32_16x16x32_bf16 v[80:83], v[60:63], v[84:87], v[80:83]
	v_mfma_f32_16x16x32_bf16 v[84:87], v[48:51], v[88:91], 0
	v_mfma_f32_16x16x32_bf16 v[88:91], v[56:59], v[88:91], 0
	v_mfma_f32_16x16x32_bf16 v[84:87], v[52:55], v[92:95], v[84:87]
	v_mfma_f32_16x16x32_bf16 v[88:91], v[60:63], v[92:95], v[88:91]
	s_setprio 0
	s_barrier
	s_mov_b32 m0, s47
	v_lshl_add_u64 v[128:129], v[28:29], 0, s[6:7]
	ds_read_b128 v[92:95], v226 offset:16384
	ds_read_b128 v[138:141], v226 offset:17408
	ds_read_b128 v[142:145], v226 offset:18432
	ds_read_b128 v[146:149], v226 offset:19456
	ds_read_b128 v[150:153], v226 offset:20480
	ds_read_b128 v[154:157], v226 offset:21504
	ds_read_b128 v[158:161], v226 offset:22528
	ds_read_b128 v[162:165], v226 offset:23552
	global_load_lds_dwordx4 v[128:129], off
	v_lshl_add_u64 v[128:129], v[30:31], 0, s[6:7]
	s_mov_b32 m0, s46
	s_nop 0
	global_load_lds_dwordx4 v[128:129], off
	v_lshl_add_u64 v[128:129], s[22:23], 0, v[130:131]
	s_mov_b32 m0, s49
	s_nop 0
	global_load_lds_dwordx4 v[128:129], off
	v_lshl_add_u64 v[128:129], s[22:23], 0, v[18:19]
	s_mov_b32 m0, s48
	s_nop 0
	global_load_lds_dwordx4 v[128:129], off
	v_lshl_add_u64 v[128:129], v[22:23], 0, s[6:7]
	s_mov_b32 m0, s38
	s_nop 0
	global_load_lds_dwordx4 v[128:129], off
	v_lshl_add_u64 v[128:129], v[24:25], 0, s[6:7]
	s_mov_b32 m0, s45
	s_nop 0
	global_load_lds_dwordx4 v[128:129], off
	s_waitcnt vmcnt(8)
	s_waitcnt lgkmcnt(0)
	s_barrier
	s_setprio 1
	s_waitcnt lgkmcnt(0)
	v_mfma_f32_16x16x32_bf16 v[166:169], v[32:35], v[92:95], 0
	v_mfma_f32_16x16x32_bf16 v[174:177], v[32:35], v[142:145], 0
	v_mfma_f32_16x16x32_bf16 v[182:185], v[32:35], v[150:153], 0
	v_mfma_f32_16x16x32_bf16 v[32:35], v[32:35], v[158:161], 0
	v_mfma_f32_16x16x32_bf16 v[166:169], v[36:39], v[138:141], v[166:169]
	v_mfma_f32_16x16x32_bf16 v[174:177], v[36:39], v[146:149], v[174:177]
	v_mfma_f32_16x16x32_bf16 v[182:185], v[36:39], v[154:157], v[182:185]
	v_mfma_f32_16x16x32_bf16 v[32:35], v[36:39], v[162:165], v[32:35]
	v_mfma_f32_16x16x32_bf16 v[36:39], v[40:43], v[158:161], 0
	v_mfma_f32_16x16x32_bf16 v[170:173], v[40:43], v[92:95], 0
	v_mfma_f32_16x16x32_bf16 v[178:181], v[40:43], v[142:145], 0
	v_mfma_f32_16x16x32_bf16 v[186:189], v[40:43], v[150:153], 0
	v_mfma_f32_16x16x32_bf16 v[36:39], v[44:47], v[162:165], v[36:39]
	v_mfma_f32_16x16x32_bf16 v[170:173], v[44:47], v[138:141], v[170:173]
	v_mfma_f32_16x16x32_bf16 v[178:181], v[44:47], v[146:149], v[178:181]
	v_mfma_f32_16x16x32_bf16 v[186:189], v[44:47], v[154:157], v[186:189]
	v_mfma_f32_16x16x32_bf16 v[40:43], v[48:51], v[92:95], 0
	v_mfma_f32_16x16x32_bf16 v[44:47], v[56:59], v[92:95], 0
	v_mfma_f32_16x16x32_bf16 v[40:43], v[52:55], v[138:141], v[40:43]
	v_mfma_f32_16x16x32_bf16 v[44:47], v[60:63], v[138:141], v[44:47]
	v_mfma_f32_16x16x32_bf16 v[92:95], v[48:51], v[142:145], 0
	v_mfma_f32_16x16x32_bf16 v[138:141], v[56:59], v[142:145], 0
	v_mfma_f32_16x16x32_bf16 v[142:145], v[48:51], v[150:153], 0
	v_mfma_f32_16x16x32_bf16 v[48:51], v[48:51], v[158:161], 0
	v_mfma_f32_16x16x32_bf16 v[92:95], v[52:55], v[146:149], v[92:95]
	v_mfma_f32_16x16x32_bf16 v[142:145], v[52:55], v[154:157], v[142:145]
	v_mfma_f32_16x16x32_bf16 v[48:51], v[52:55], v[162:165], v[48:51]
	v_mfma_f32_16x16x32_bf16 v[52:55], v[56:59], v[158:161], 0
	v_mfma_f32_16x16x32_bf16 v[138:141], v[60:63], v[146:149], v[138:141]
	v_mfma_f32_16x16x32_bf16 v[146:149], v[56:59], v[150:153], 0
	v_mfma_f32_16x16x32_bf16 v[52:55], v[60:63], v[162:165], v[52:55]
	v_mfma_f32_16x16x32_bf16 v[146:149], v[60:63], v[154:157], v[146:149]
	s_setprio 0
	s_barrier
	ds_read_b128 v[56:59], v229
	ds_read_b128 v[60:63], v229 offset:1024
	ds_read_b128 v[150:153], v229 offset:2048
	ds_read_b128 v[154:157], v229 offset:3072
	ds_read_b128 v[158:161], v227
	ds_read_b128 v[162:165], v227 offset:1024
	ds_read_b128 v[190:193], v227 offset:2048
	ds_read_b128 v[194:197], v227 offset:3072
	s_mov_b32 m0, s36
	v_lshl_add_u64 v[128:129], v[2:3], 0, s[6:7]
	ds_read_b128 v[198:201], v226 offset:32768
	ds_read_b128 v[202:205], v226 offset:33792
	ds_read_b128 v[206:209], v226 offset:34816
	ds_read_b128 v[210:213], v226 offset:35840
	ds_read_b128 v[214:217], v226 offset:36864
	ds_read_b128 v[218:221], v226 offset:37888
	ds_read_b128 v[222:225], v226 offset:38912
	ds_read_b128 v[230:233], v226 offset:39936
	global_load_lds_dwordx4 v[128:129], off
	v_lshl_add_u64 v[128:129], v[4:5], 0, s[6:7]
	s_mov_b32 m0, s37
	s_nop 0
	global_load_lds_dwordx4 v[128:129], off
	s_waitcnt vmcnt(8)
	s_waitcnt lgkmcnt(0)
	s_barrier
	s_setprio 1
	s_waitcnt lgkmcnt(0)
	v_mfma_f32_16x16x32_bf16 v[96:99], v[56:59], v[198:201], v[96:99]
	v_mfma_f32_16x16x32_bf16 v[100:103], v[150:153], v[198:201], v[100:103]
	v_mfma_f32_16x16x32_bf16 v[104:107], v[56:59], v[206:209], v[104:107]
	v_mfma_f32_16x16x32_bf16 v[108:111], v[150:153], v[206:209], v[108:111]
	v_mfma_f32_16x16x32_bf16 v[112:115], v[56:59], v[214:217], v[112:115]
	v_mfma_f32_16x16x32_bf16 v[116:119], v[150:153], v[214:217], v[116:119]
	v_mfma_f32_16x16x32_bf16 v[120:123], v[56:59], v[222:225], v[120:123]
	v_mfma_f32_16x16x32_bf16 v[124:127], v[150:153], v[222:225], v[124:127]
	v_mfma_f32_16x16x32_bf16 v[96:99], v[60:63], v[202:205], v[96:99]
	v_mfma_f32_16x16x32_bf16 v[100:103], v[154:157], v[202:205], v[100:103]
	v_mfma_f32_16x16x32_bf16 v[104:107], v[60:63], v[210:213], v[104:107]
	v_mfma_f32_16x16x32_bf16 v[108:111], v[154:157], v[210:213], v[108:111]
	v_mfma_f32_16x16x32_bf16 v[112:115], v[60:63], v[218:221], v[112:115]
	v_mfma_f32_16x16x32_bf16 v[116:119], v[154:157], v[218:221], v[116:119]
	v_mfma_f32_16x16x32_bf16 v[120:123], v[60:63], v[230:233], v[120:123]
	v_mfma_f32_16x16x32_bf16 v[124:127], v[154:157], v[230:233], v[124:127]
	v_mfma_f32_16x16x32_bf16 v[64:67], v[190:193], v[198:201], v[64:67]
	v_mfma_f32_16x16x32_bf16 v[68:71], v[158:161], v[206:209], v[68:71]
	v_mfma_f32_16x16x32_bf16 v[72:75], v[190:193], v[206:209], v[72:75]
	v_mfma_f32_16x16x32_bf16 v[76:79], v[158:161], v[214:217], v[76:79]
	v_mfma_f32_16x16x32_bf16 v[80:83], v[190:193], v[214:217], v[80:83]
	v_mfma_f32_16x16x32_bf16 v[84:87], v[158:161], v[222:225], v[84:87]
	v_mfma_f32_16x16x32_bf16 v[88:91], v[190:193], v[222:225], v[88:91]
	v_mfma_f32_16x16x32_bf16 v[134:137], v[158:161], v[198:201], v[134:137]
	v_mfma_f32_16x16x32_bf16 v[64:67], v[194:197], v[202:205], v[64:67]
	v_mfma_f32_16x16x32_bf16 v[68:71], v[162:165], v[210:213], v[68:71]
	v_mfma_f32_16x16x32_bf16 v[72:75], v[194:197], v[210:213], v[72:75]
	v_mfma_f32_16x16x32_bf16 v[76:79], v[162:165], v[218:221], v[76:79]
	v_mfma_f32_16x16x32_bf16 v[80:83], v[194:197], v[218:221], v[80:83]
	v_mfma_f32_16x16x32_bf16 v[84:87], v[162:165], v[230:233], v[84:87]
	v_mfma_f32_16x16x32_bf16 v[88:91], v[194:197], v[230:233], v[88:91]
	v_mfma_f32_16x16x32_bf16 v[134:137], v[162:165], v[202:205], v[134:137]
	s_setprio 0
	s_barrier
	s_mov_b32 m0, s39
	v_lshl_add_u64 v[128:129], v[28:29], 0, s[8:9]
	ds_read_b128 v[198:201], v226 offset:49152
	ds_read_b128 v[202:205], v226 offset:50176
	ds_read_b128 v[206:209], v226 offset:51200
	ds_read_b128 v[210:213], v226 offset:52224
	ds_read_b128 v[214:217], v226 offset:53248
	ds_read_b128 v[218:221], v226 offset:54272
	ds_read_b128 v[222:225], v226 offset:55296
	ds_read_b128 v[230:233], v226 offset:56320
	global_load_lds_dwordx4 v[128:129], off
	v_lshl_add_u64 v[128:129], v[30:31], 0, s[8:9]
	s_mov_b32 m0, s41
	v_lshl_add_u64 v[18:19], s[20:21], 0, v[18:19]
	global_load_lds_dwordx4 v[128:129], off
	v_lshl_add_u64 v[128:129], s[20:21], 0, v[130:131]
	s_mov_b32 m0, s43
	s_nop 0
	global_load_lds_dwordx4 v[128:129], off
	s_mov_b32 m0, s44
	s_nop 0
	global_load_lds_dwordx4 v[18:19], off
	v_lshl_add_u64 v[18:19], v[22:23], 0, s[8:9]
	s_mov_b32 m0, s40
	s_nop 0
	global_load_lds_dwordx4 v[18:19], off
	v_lshl_add_u64 v[18:19], v[24:25], 0, s[8:9]
	s_mov_b32 m0, s42
	s_nop 0
	global_load_lds_dwordx4 v[18:19], off
	s_waitcnt vmcnt(8)
	s_waitcnt lgkmcnt(0)
	s_barrier
	s_setprio 1
	s_waitcnt lgkmcnt(0)
	v_mfma_f32_16x16x32_bf16 v[32:35], v[56:59], v[222:225], v[32:35]
	v_mfma_f32_16x16x32_bf16 v[36:39], v[150:153], v[222:225], v[36:39]
	v_mfma_f32_16x16x32_bf16 v[166:169], v[56:59], v[198:201], v[166:169]
	v_mfma_f32_16x16x32_bf16 v[170:173], v[150:153], v[198:201], v[170:173]
	v_mfma_f32_16x16x32_bf16 v[174:177], v[56:59], v[206:209], v[174:177]
	v_mfma_f32_16x16x32_bf16 v[178:181], v[150:153], v[206:209], v[178:181]
	v_mfma_f32_16x16x32_bf16 v[182:185], v[56:59], v[214:217], v[182:185]
	v_mfma_f32_16x16x32_bf16 v[186:189], v[150:153], v[214:217], v[186:189]
	v_mfma_f32_16x16x32_bf16 v[32:35], v[60:63], v[230:233], v[32:35]
	v_mfma_f32_16x16x32_bf16 v[36:39], v[154:157], v[230:233], v[36:39]
	v_mfma_f32_16x16x32_bf16 v[166:169], v[60:63], v[202:205], v[166:169]
	v_mfma_f32_16x16x32_bf16 v[170:173], v[154:157], v[202:205], v[170:173]
	v_mfma_f32_16x16x32_bf16 v[174:177], v[60:63], v[210:213], v[174:177]
	v_mfma_f32_16x16x32_bf16 v[178:181], v[154:157], v[210:213], v[178:181]
	v_mfma_f32_16x16x32_bf16 v[182:185], v[60:63], v[218:221], v[182:185]
	v_mfma_f32_16x16x32_bf16 v[186:189], v[154:157], v[218:221], v[186:189]
	v_mfma_f32_16x16x32_bf16 v[40:43], v[158:161], v[198:201], v[40:43]
	v_mfma_f32_16x16x32_bf16 v[44:47], v[190:193], v[198:201], v[44:47]
	v_mfma_f32_16x16x32_bf16 v[56:59], v[158:161], v[206:209], v[92:95]
	v_mfma_f32_16x16x32_bf16 v[60:63], v[190:193], v[206:209], v[138:141]
	v_mfma_f32_16x16x32_bf16 v[92:95], v[158:161], v[214:217], v[142:145]
	v_mfma_f32_16x16x32_bf16 v[48:51], v[158:161], v[222:225], v[48:51]
	v_mfma_f32_16x16x32_bf16 v[52:55], v[190:193], v[222:225], v[52:55]
	v_mfma_f32_16x16x32_bf16 v[40:43], v[162:165], v[202:205], v[40:43]
	v_mfma_f32_16x16x32_bf16 v[44:47], v[194:197], v[202:205], v[44:47]
	v_mfma_f32_16x16x32_bf16 v[56:59], v[162:165], v[210:213], v[56:59]
	v_mfma_f32_16x16x32_bf16 v[60:63], v[194:197], v[210:213], v[60:63]
	v_mfma_f32_16x16x32_bf16 v[92:95], v[162:165], v[218:221], v[92:95]
	v_mfma_f32_16x16x32_bf16 v[138:141], v[190:193], v[214:217], v[146:149]
	v_mfma_f32_16x16x32_bf16 v[48:51], v[162:165], v[230:233], v[48:51]
	v_mfma_f32_16x16x32_bf16 v[52:55], v[194:197], v[230:233], v[52:55]
	v_mfma_f32_16x16x32_bf16 v[138:141], v[194:197], v[218:221], v[138:141]
	s_setprio 0
	s_barrier
	ds_read_b128 v[142:145], v235
	ds_read_b128 v[146:149], v235 offset:1024
	ds_read_b128 v[150:153], v235 offset:2048
	ds_read_b128 v[154:157], v235 offset:3072
	ds_read_b128 v[158:161], v234
	ds_read_b128 v[162:165], v234 offset:1024
	ds_read_b128 v[190:193], v234 offset:2048
	ds_read_b128 v[194:197], v234 offset:3072
	s_mov_b32 m0, s52
	v_lshl_add_u64 v[18:19], v[2:3], 0, s[8:9]
	ds_read_b128 v[198:201], v226
	ds_read_b128 v[202:205], v226 offset:1024
	ds_read_b128 v[206:209], v226 offset:2048
	ds_read_b128 v[210:213], v226 offset:3072
	ds_read_b128 v[214:217], v226 offset:4096
	ds_read_b128 v[218:221], v226 offset:5120
	ds_read_b128 v[222:225], v226 offset:6144
	ds_read_b128 v[230:233], v226 offset:7168
	global_load_lds_dwordx4 v[18:19], off
	v_lshl_add_u64 v[18:19], v[4:5], 0, s[8:9]
	s_mov_b32 m0, s50
	s_nop 0
	global_load_lds_dwordx4 v[18:19], off
	s_waitcnt vmcnt(8)
	s_waitcnt lgkmcnt(0)
	s_barrier
	s_setprio 1
	s_waitcnt lgkmcnt(0)
	v_mfma_f32_16x16x32_bf16 v[112:115], v[142:145], v[214:217], v[112:115]
	v_mfma_f32_16x16x32_bf16 v[234:237], v[146:149], v[218:221], v[112:115]
	v_mfma_f32_16x16x32_bf16 v[112:115], v[150:153], v[214:217], v[116:119]
	v_mfma_f32_16x16x32_bf16 v[238:241], v[154:157], v[218:221], v[112:115]
	v_mfma_f32_16x16x32_bf16 v[112:115], v[142:145], v[222:225], v[120:123]
	v_mfma_f32_16x16x32_bf16 v[96:99], v[142:145], v[198:201], v[96:99]
	v_mfma_f32_16x16x32_bf16 v[100:103], v[150:153], v[198:201], v[100:103]
	v_mfma_f32_16x16x32_bf16 v[104:107], v[142:145], v[206:209], v[104:107]
	v_mfma_f32_16x16x32_bf16 v[108:111], v[150:153], v[206:209], v[108:111]
	v_mfma_f32_16x16x32_bf16 v[242:245], v[146:149], v[230:233], v[112:115]
	v_mfma_f32_16x16x32_bf16 v[112:115], v[150:153], v[222:225], v[124:127]
	v_mfma_f32_16x16x32_bf16 v[96:99], v[146:149], v[202:205], v[96:99]
	v_mfma_f32_16x16x32_bf16 v[100:103], v[154:157], v[202:205], v[100:103]
	v_mfma_f32_16x16x32_bf16 v[104:107], v[146:149], v[210:213], v[104:107]
	v_mfma_f32_16x16x32_bf16 v[108:111], v[154:157], v[210:213], v[108:111]
	v_mfma_f32_16x16x32_bf16 v[122:125], v[154:157], v[230:233], v[112:115]
	v_mfma_f32_16x16x32_bf16 v[64:67], v[190:193], v[198:201], v[64:67]
	v_mfma_f32_16x16x32_bf16 v[112:115], v[158:161], v[198:201], v[134:137]
	v_mfma_f32_16x16x32_bf16 v[134:137], v[194:197], v[202:205], v[64:67]
	v_mfma_f32_16x16x32_bf16 v[64:67], v[158:161], v[206:209], v[68:71]
	v_mfma_f32_16x16x32_bf16 v[198:201], v[162:165], v[210:213], v[64:67]
	v_mfma_f32_16x16x32_bf16 v[64:67], v[190:193], v[206:209], v[72:75]
	v_mfma_f32_16x16x32_bf16 v[126:129], v[162:165], v[202:205], v[112:115]
	v_mfma_f32_16x16x32_bf16 v[202:205], v[194:197], v[210:213], v[64:67]
	v_mfma_f32_16x16x32_bf16 v[64:67], v[158:161], v[214:217], v[76:79]
	v_mfma_f32_16x16x32_bf16 v[74:77], v[162:165], v[218:221], v[64:67]
	v_mfma_f32_16x16x32_bf16 v[64:67], v[190:193], v[214:217], v[80:83]
	v_mfma_f32_16x16x32_bf16 v[78:81], v[194:197], v[218:221], v[64:67]
	v_mfma_f32_16x16x32_bf16 v[64:67], v[158:161], v[222:225], v[84:87]
	v_mfma_f32_16x16x32_bf16 v[82:85], v[162:165], v[230:233], v[64:67]
	v_mfma_f32_16x16x32_bf16 v[64:67], v[190:193], v[222:225], v[88:91]
	v_mfma_f32_16x16x32_bf16 v[86:89], v[194:197], v[230:233], v[64:67]
	s_setprio 0
	s_barrier
	s_mov_b32 m0, s47
	s_nop 3
	ds_read_b128 v[64:67], v226 offset:16384
	ds_read_b128 v[68:71], v226 offset:17408
	ds_read_b128 v[112:115], v226 offset:18432
	ds_read_b128 v[116:119], v226 offset:19456
	ds_read_b128 v[206:209], v226 offset:20480
	ds_read_b128 v[210:213], v226 offset:21504
	ds_read_b128 v[214:217], v226 offset:22528
	ds_read_b128 v[218:221], v226 offset:23552
	global_load_lds_dwordx4 v[28:29], off
	s_mov_b32 m0, s46
	s_nop 0
	global_load_lds_dwordx4 v[30:31], off
	s_mov_b32 m0, s49
	s_nop 0
	global_load_lds_dwordx4 v[26:27], off
	s_mov_b32 m0, s48
	s_nop 0
	global_load_lds_dwordx4 v[20:21], off
	s_mov_b32 m0, s38
	s_nop 0
	global_load_lds_dwordx4 v[22:23], off
	s_mov_b32 m0, s45
	s_nop 0
	global_load_lds_dwordx4 v[24:25], off
	s_waitcnt vmcnt(8)
	s_waitcnt lgkmcnt(0)
	s_barrier
	s_setprio 1
	s_waitcnt lgkmcnt(0)
	v_mfma_f32_16x16x32_bf16 v[18:21], v[142:145], v[64:67], v[166:169]
	v_mfma_f32_16x16x32_bf16 v[22:25], v[150:153], v[64:67], v[170:173]
	v_mfma_f32_16x16x32_bf16 v[26:29], v[142:145], v[112:115], v[174:177]
	v_mfma_f32_16x16x32_bf16 v[30:33], v[142:145], v[214:217], v[32:35]
	v_mfma_f32_16x16x32_bf16 v[18:21], v[146:149], v[68:71], v[18:21]
	v_mfma_f32_16x16x32_bf16 v[22:25], v[154:157], v[68:71], v[22:25]
	v_mfma_f32_16x16x32_bf16 v[26:29], v[146:149], v[116:119], v[26:29]
	v_mfma_f32_16x16x32_bf16 v[166:169], v[150:153], v[112:115], v[178:181]
	v_mfma_f32_16x16x32_bf16 v[170:173], v[142:145], v[206:209], v[182:185]
	v_mfma_f32_16x16x32_bf16 v[174:177], v[150:153], v[206:209], v[186:189]
	v_mfma_f32_16x16x32_bf16 v[30:33], v[146:149], v[218:221], v[30:33]
	v_mfma_f32_16x16x32_bf16 v[34:37], v[150:153], v[214:217], v[36:39]
	v_mfma_f32_16x16x32_bf16 v[166:169], v[154:157], v[116:119], v[166:169]
	v_mfma_f32_16x16x32_bf16 v[170:173], v[146:149], v[210:213], v[170:173]
	v_mfma_f32_16x16x32_bf16 v[174:177], v[154:157], v[210:213], v[174:177]
	v_mfma_f32_16x16x32_bf16 v[142:145], v[154:157], v[218:221], v[34:37]
	v_mfma_f32_16x16x32_bf16 v[34:37], v[158:161], v[64:67], v[40:43]
	v_mfma_f32_16x16x32_bf16 v[146:149], v[162:165], v[68:71], v[34:37]
	v_mfma_f32_16x16x32_bf16 v[34:37], v[190:193], v[64:67], v[44:47]
	v_mfma_f32_16x16x32_bf16 v[150:153], v[194:197], v[68:71], v[34:37]
	v_mfma_f32_16x16x32_bf16 v[34:37], v[158:161], v[112:115], v[56:59]
	v_mfma_f32_16x16x32_bf16 v[154:157], v[162:165], v[116:119], v[34:37]
	v_mfma_f32_16x16x32_bf16 v[34:37], v[190:193], v[112:115], v[60:63]
	v_mfma_f32_16x16x32_bf16 v[62:65], v[194:197], v[116:119], v[34:37]
	v_mfma_f32_16x16x32_bf16 v[34:37], v[158:161], v[206:209], v[92:95]
	v_mfma_f32_16x16x32_bf16 v[178:181], v[162:165], v[210:213], v[34:37]
	v_mfma_f32_16x16x32_bf16 v[34:37], v[190:193], v[206:209], v[138:141]
	v_mfma_f32_16x16x32_bf16 v[138:141], v[194:197], v[210:213], v[34:37]
	v_mfma_f32_16x16x32_bf16 v[34:37], v[158:161], v[214:217], v[48:51]
	v_mfma_f32_16x16x32_bf16 v[158:161], v[162:165], v[218:221], v[34:37]
	v_mfma_f32_16x16x32_bf16 v[34:37], v[190:193], v[214:217], v[52:55]
	v_mfma_f32_16x16x32_bf16 v[162:165], v[194:197], v[218:221], v[34:37]
	s_setprio 0
	s_barrier
	ds_read_b128 v[58:61], v229
	ds_read_b128 v[90:93], v229 offset:1024
	ds_read_b128 v[182:185], v229 offset:2048
	ds_read_b128 v[186:189], v229 offset:3072
	ds_read_b128 v[190:193], v227
	ds_read_b128 v[194:197], v227 offset:1024
	ds_read_b128 v[206:209], v227 offset:2048
	ds_read_b128 v[210:213], v227 offset:3072
	s_mov_b32 m0, s36
	ds_read_b128 v[42:45], v226 offset:32768
	ds_read_b128 v[46:49], v226 offset:33792
	ds_read_b128 v[50:53], v226 offset:34816
	ds_read_b128 v[54:57], v226 offset:35840
	ds_read_b128 v[214:217], v226 offset:36864
	ds_read_b128 v[218:221], v226 offset:37888
	ds_read_b128 v[222:225], v226 offset:38912
	ds_read_b128 v[230:233], v226 offset:39936
	global_load_lds_dwordx4 v[2:3], off
	s_mov_b32 m0, s37
	s_nop 0
	global_load_lds_dwordx4 v[4:5], off
	s_waitcnt vmcnt(8)
	s_waitcnt lgkmcnt(0)
	s_barrier
	s_setprio 1
	s_waitcnt lgkmcnt(0)
	v_mfma_f32_16x16x32_bf16 v[2:5], v[58:61], v[42:45], v[96:99]
	v_mfma_f32_16x16x32_bf16 v[114:117], v[90:93], v[46:49], v[2:5]
	v_mfma_f32_16x16x32_bf16 v[2:5], v[182:185], v[42:45], v[100:103]
	v_mfma_f32_16x16x32_bf16 v[118:121], v[186:189], v[46:49], v[2:5]
	v_mfma_f32_16x16x32_bf16 v[2:5], v[58:61], v[50:53], v[104:107]
	v_mfma_f32_16x16x32_bf16 v[98:101], v[90:93], v[54:57], v[2:5]
	v_mfma_f32_16x16x32_bf16 v[2:5], v[182:185], v[50:53], v[108:111]
	v_mfma_f32_16x16x32_bf16 v[102:105], v[186:189], v[54:57], v[2:5]
	v_mfma_f32_16x16x32_bf16 v[2:5], v[58:61], v[214:217], v[234:237]
	v_mfma_f32_16x16x32_bf16 v[66:69], v[90:93], v[218:221], v[2:5]
	v_mfma_f32_16x16x32_bf16 v[2:5], v[182:185], v[214:217], v[238:241]
	v_mfma_f32_16x16x32_bf16 v[70:73], v[186:189], v[218:221], v[2:5]
	v_mfma_f32_16x16x32_bf16 v[2:5], v[58:61], v[222:225], v[242:245]
	v_mfma_f32_16x16x32_bf16 v[34:37], v[90:93], v[230:233], v[2:5]
	v_mfma_f32_16x16x32_bf16 v[2:5], v[182:185], v[222:225], v[122:125]
	v_mfma_f32_16x16x32_bf16 v[38:41], v[186:189], v[230:233], v[2:5]
	v_mfma_f32_16x16x32_bf16 v[2:5], v[190:193], v[42:45], v[126:129]
	v_mfma_f32_16x16x32_bf16 v[122:125], v[194:197], v[46:49], v[2:5]
	v_mfma_f32_16x16x32_bf16 v[2:5], v[206:209], v[42:45], v[134:137]
	v_mfma_f32_16x16x32_bf16 v[126:129], v[210:213], v[46:49], v[2:5]
	v_mfma_f32_16x16x32_bf16 v[2:5], v[190:193], v[50:53], v[198:201]
	v_mfma_f32_16x16x32_bf16 v[106:109], v[194:197], v[54:57], v[2:5]
	v_mfma_f32_16x16x32_bf16 v[2:5], v[206:209], v[50:53], v[202:205]
	v_mfma_f32_16x16x32_bf16 v[110:113], v[210:213], v[54:57], v[2:5]
	v_mfma_f32_16x16x32_bf16 v[2:5], v[190:193], v[214:217], v[74:77]
	v_mfma_f32_16x16x32_bf16 v[74:77], v[194:197], v[218:221], v[2:5]
	v_mfma_f32_16x16x32_bf16 v[2:5], v[206:209], v[214:217], v[78:81]
	v_mfma_f32_16x16x32_bf16 v[78:81], v[210:213], v[218:221], v[2:5]
	v_mfma_f32_16x16x32_bf16 v[2:5], v[190:193], v[222:225], v[82:85]
	v_mfma_f32_16x16x32_bf16 v[42:45], v[194:197], v[230:233], v[2:5]
	v_mfma_f32_16x16x32_bf16 v[2:5], v[206:209], v[222:225], v[86:89]
	v_mfma_f32_16x16x32_bf16 v[46:49], v[210:213], v[230:233], v[2:5]
	s_setprio 0
	s_barrier
	s_mov_b32 m0, s39
	ds_read_b128 v[94:97], v226 offset:49152
	ds_read_b128 v[134:137], v226 offset:50176
	ds_read_b128 v[198:201], v226 offset:51200
	ds_read_b128 v[202:205], v226 offset:52224
	ds_read_b128 v[214:217], v226 offset:53248
	ds_read_b128 v[218:221], v226 offset:54272
	ds_read_b128 v[222:225], v226 offset:55296
	ds_read_b128 v[230:233], v226 offset:56320
	global_load_lds_dwordx4 v[8:9], off
	s_mov_b32 m0, s41
	s_nop 0
	global_load_lds_dwordx4 v[10:11], off
	s_mov_b32 m0, s43
	s_nop 0
	global_load_lds_dwordx4 v[14:15], off
	s_mov_b32 m0, s44
	s_nop 0
	global_load_lds_dwordx4 v[16:17], off
	s_mov_b32 m0, s40
	s_nop 0
	global_load_lds_dwordx4 v[6:7], off
	s_mov_b32 m0, s42
	s_nop 0
	global_load_lds_dwordx4 v[12:13], off
	s_waitcnt vmcnt(8)
	s_waitcnt lgkmcnt(0)
	s_barrier
	s_setprio 1
	s_waitcnt lgkmcnt(0)
	v_mfma_f32_16x16x32_bf16 v[2:5], v[58:61], v[94:97], v[18:21]
	v_mfma_f32_16x16x32_bf16 v[82:85], v[90:93], v[134:137], v[2:5]
	v_mfma_f32_16x16x32_bf16 v[2:5], v[182:185], v[94:97], v[22:25]
	v_mfma_f32_16x16x32_bf16 v[86:89], v[186:189], v[134:137], v[2:5]
	v_mfma_f32_16x16x32_bf16 v[2:5], v[58:61], v[198:201], v[26:29]
	v_mfma_f32_16x16x32_bf16 v[50:53], v[90:93], v[202:205], v[2:5]
	v_mfma_f32_16x16x32_bf16 v[2:5], v[182:185], v[198:201], v[166:169]
	v_mfma_f32_16x16x32_bf16 v[54:57], v[186:189], v[202:205], v[2:5]
	v_mfma_f32_16x16x32_bf16 v[2:5], v[58:61], v[214:217], v[170:173]
	v_mfma_f32_16x16x32_bf16 v[18:21], v[90:93], v[218:221], v[2:5]
	v_mfma_f32_16x16x32_bf16 v[2:5], v[182:185], v[214:217], v[174:177]
	v_mfma_f32_16x16x32_bf16 v[22:25], v[186:189], v[218:221], v[2:5]
	v_mfma_f32_16x16x32_bf16 v[2:5], v[58:61], v[222:225], v[30:33]
	v_mfma_f32_16x16x32_bf16 v[6:9], v[182:185], v[222:225], v[142:145]
	v_mfma_f32_16x16x32_bf16 v[2:5], v[90:93], v[230:233], v[2:5]
	v_mfma_f32_16x16x32_bf16 v[6:9], v[186:189], v[230:233], v[6:9]
	v_mfma_f32_16x16x32_bf16 v[10:13], v[190:193], v[94:97], v[146:149]
	v_mfma_f32_16x16x32_bf16 v[90:93], v[194:197], v[134:137], v[10:13]
	v_mfma_f32_16x16x32_bf16 v[10:13], v[206:209], v[94:97], v[150:153]
	v_mfma_f32_16x16x32_bf16 v[94:97], v[210:213], v[134:137], v[10:13]
	v_mfma_f32_16x16x32_bf16 v[10:13], v[190:193], v[198:201], v[154:157]
	v_mfma_f32_16x16x32_bf16 v[58:61], v[194:197], v[202:205], v[10:13]
	v_mfma_f32_16x16x32_bf16 v[10:13], v[206:209], v[198:201], v[62:65]
	v_mfma_f32_16x16x32_bf16 v[62:65], v[210:213], v[202:205], v[10:13]
	v_mfma_f32_16x16x32_bf16 v[10:13], v[190:193], v[214:217], v[178:181]
	v_mfma_f32_16x16x32_bf16 v[26:29], v[194:197], v[218:221], v[10:13]
	v_mfma_f32_16x16x32_bf16 v[10:13], v[206:209], v[214:217], v[138:141]
	v_mfma_f32_16x16x32_bf16 v[30:33], v[210:213], v[218:221], v[10:13]
	v_mfma_f32_16x16x32_bf16 v[10:13], v[190:193], v[222:225], v[158:161]
	v_mfma_f32_16x16x32_bf16 v[14:17], v[206:209], v[222:225], v[162:165]
	v_mfma_f32_16x16x32_bf16 v[10:13], v[194:197], v[230:233], v[10:13]
	v_mfma_f32_16x16x32_bf16 v[14:17], v[210:213], v[230:233], v[14:17]
	s_setprio 0
	s_barrier
	s_cbranch_scc1 .LBB0_741
	s_barrier
	s_branch .LBB0_741

.LBB0_1003:
	v_add_u32_e32 v3, s3, v174
	ds_read_b128 v[134:137], v3
	ds_read_b128 v[138:141], v3 offset:1024
	ds_read_b128 v[142:145], v3 offset:2048
	ds_read_b128 v[146:149], v3 offset:3072
	v_add_u32_e32 v3, s2, v174
	ds_read_b128 v[170:173], v3
	ds_read_b128 v[178:181], v3 offset:1024
	ds_read_b128 v[182:185], v3 offset:2048
	ds_read_b128 v[186:189], v3 offset:3072
	s_add_u32 s38, s36, 0x80
	s_addc_u32 s39, s37, 0
	s_cmp_eq_u32 s61, 12
	s_cselect_b32 s41, s29, s39
	s_cselect_b32 s40, s28, s38
	s_cselect_b32 s39, s31, s60
	s_cselect_b32 s38, s30, s27
	v_lshl_add_u64 v[4:5], s[36:37], 0, v[164:165]
	s_add_i32 m0, s46, 0xc000
	ds_read_b128 v[190:193], v177
	ds_read_b128 v[194:197], v177 offset:1024
	ds_read_b128 v[198:201], v177 offset:2048
	ds_read_b128 v[202:205], v177 offset:3072
	ds_read_b128 v[206:209], v177 offset:4096
	ds_read_b128 v[210:213], v177 offset:5120
	ds_read_b128 v[214:217], v177 offset:6144
	ds_read_b128 v[218:221], v177 offset:7168
	global_load_lds_dwordx4 v[4:5], off
	v_lshl_add_u64 v[4:5], s[36:37], 0, v[162:163]
	s_add_i32 m0, s46, 0xe000
	s_nop 0
	global_load_lds_dwordx4 v[4:5], off
	s_waitcnt vmcnt(8)
	s_waitcnt lgkmcnt(0)
	s_barrier
	s_setprio 1
	s_waitcnt lgkmcnt(0)
	v_mfma_f32_16x16x32_bf16 v[98:101], v[134:137], v[190:193], v[98:101]
	v_mfma_f32_16x16x32_bf16 v[94:97], v[142:145], v[190:193], v[94:97]
	v_mfma_f32_16x16x32_bf16 v[90:93], v[134:137], v[198:201], v[90:93]
	v_mfma_f32_16x16x32_bf16 v[86:89], v[142:145], v[198:201], v[86:89]
	v_mfma_f32_16x16x32_bf16 v[82:85], v[134:137], v[206:209], v[82:85]
	v_mfma_f32_16x16x32_bf16 v[78:81], v[142:145], v[206:209], v[78:81]
	v_mfma_f32_16x16x32_bf16 v[74:77], v[134:137], v[214:217], v[74:77]
	v_mfma_f32_16x16x32_bf16 v[70:73], v[142:145], v[214:217], v[70:73]
	v_mfma_f32_16x16x32_bf16 v[98:101], v[138:141], v[194:197], v[98:101]
	v_mfma_f32_16x16x32_bf16 v[94:97], v[146:149], v[194:197], v[94:97]
	v_mfma_f32_16x16x32_bf16 v[90:93], v[138:141], v[202:205], v[90:93]
	v_mfma_f32_16x16x32_bf16 v[86:89], v[146:149], v[202:205], v[86:89]
	v_mfma_f32_16x16x32_bf16 v[82:85], v[138:141], v[210:213], v[82:85]
	v_mfma_f32_16x16x32_bf16 v[78:81], v[146:149], v[210:213], v[78:81]
	v_mfma_f32_16x16x32_bf16 v[74:77], v[138:141], v[218:221], v[74:77]
	v_mfma_f32_16x16x32_bf16 v[70:73], v[146:149], v[218:221], v[70:73]
	v_mfma_f32_16x16x32_bf16 v[66:69], v[170:173], v[190:193], v[66:69]
	v_mfma_f32_16x16x32_bf16 v[62:65], v[182:185], v[190:193], v[62:65]
	v_mfma_f32_16x16x32_bf16 v[58:61], v[170:173], v[198:201], v[58:61]
	v_mfma_f32_16x16x32_bf16 v[54:57], v[182:185], v[198:201], v[54:57]
	v_mfma_f32_16x16x32_bf16 v[50:53], v[170:173], v[206:209], v[50:53]
	v_mfma_f32_16x16x32_bf16 v[46:49], v[182:185], v[206:209], v[46:49]
	v_mfma_f32_16x16x32_bf16 v[42:45], v[170:173], v[214:217], v[42:45]
	v_mfma_f32_16x16x32_bf16 v[38:41], v[182:185], v[214:217], v[38:41]
	v_mfma_f32_16x16x32_bf16 v[66:69], v[178:181], v[194:197], v[66:69]
	v_mfma_f32_16x16x32_bf16 v[62:65], v[186:189], v[194:197], v[62:65]
	v_mfma_f32_16x16x32_bf16 v[58:61], v[178:181], v[202:205], v[58:61]
	v_mfma_f32_16x16x32_bf16 v[54:57], v[186:189], v[202:205], v[54:57]
	v_mfma_f32_16x16x32_bf16 v[50:53], v[178:181], v[210:213], v[50:53]
	v_mfma_f32_16x16x32_bf16 v[46:49], v[186:189], v[210:213], v[46:49]
	v_mfma_f32_16x16x32_bf16 v[42:45], v[178:181], v[218:221], v[42:45]
	v_mfma_f32_16x16x32_bf16 v[38:41], v[186:189], v[218:221], v[38:41]
	s_setprio 0
	s_barrier
	s_add_i32 s62, s3, s45
	v_lshl_add_u64 v[222:223], s[38:39], 0, v[150:151]
	s_mov_b32 m0, s62
	ds_read_b128 v[190:193], v177 offset:16384
	ds_read_b128 v[194:197], v177 offset:17408
	ds_read_b128 v[198:201], v177 offset:18432
	ds_read_b128 v[202:205], v177 offset:19456
	ds_read_b128 v[206:209], v177 offset:20480
	ds_read_b128 v[210:213], v177 offset:21504
	ds_read_b128 v[214:217], v177 offset:22528
	ds_read_b128 v[218:221], v177 offset:23552
	global_load_lds_dwordx4 v[222:223], off
	s_add_i32 m0, s62, 0x2000
	s_add_u32 s62, s38, 0x80000
	v_lshl_add_u64 v[224:225], s[38:39], 0, v[152:153]
	s_addc_u32 s63, s39, 0
	s_add_i32 s64, s2, s45
	global_load_lds_dwordx4 v[224:225], off
	v_lshl_add_u64 v[4:5], s[62:63], 0, v[150:151]
	s_mov_b32 m0, s64
	v_lshl_add_u64 v[226:227], s[40:41], 0, v[154:155]
	global_load_lds_dwordx4 v[4:5], off
	v_lshl_add_u64 v[4:5], s[62:63], 0, v[152:153]
	s_add_i32 m0, s64, 0x2000
	v_lshl_add_u64 v[230:231], s[40:41], 0, v[156:157]
	global_load_lds_dwordx4 v[4:5], off
	s_mov_b32 m0, s46
	s_nop 0
	global_load_lds_dwordx4 v[226:227], off
	s_mov_b32 m0, s47
	s_nop 0
	global_load_lds_dwordx4 v[230:231], off
	s_waitcnt vmcnt(8)
	s_waitcnt lgkmcnt(0)
	s_barrier
	s_setprio 1
	s_waitcnt lgkmcnt(0)
	v_mfma_f32_16x16x32_bf16 v[34:37], v[134:137], v[190:193], v[34:37]
	v_mfma_f32_16x16x32_bf16 v[30:33], v[142:145], v[190:193], v[30:33]
	v_mfma_f32_16x16x32_bf16 v[26:29], v[134:137], v[198:201], v[26:29]
	v_mfma_f32_16x16x32_bf16 v[22:25], v[142:145], v[198:201], v[22:25]
	v_mfma_f32_16x16x32_bf16 v[18:21], v[134:137], v[206:209], v[18:21]
	v_mfma_f32_16x16x32_bf16 v[14:17], v[142:145], v[206:209], v[14:17]
	v_mfma_f32_16x16x32_bf16 v[10:13], v[134:137], v[214:217], v[10:13]
	v_mfma_f32_16x16x32_bf16 v[4:7], v[142:145], v[214:217], v[6:9]
	v_mfma_f32_16x16x32_bf16 v[34:37], v[138:141], v[194:197], v[34:37]
	v_mfma_f32_16x16x32_bf16 v[30:33], v[146:149], v[194:197], v[30:33]
	v_mfma_f32_16x16x32_bf16 v[26:29], v[138:141], v[202:205], v[26:29]
	v_mfma_f32_16x16x32_bf16 v[22:25], v[146:149], v[202:205], v[22:25]
	v_mfma_f32_16x16x32_bf16 v[18:21], v[138:141], v[210:213], v[18:21]
	v_mfma_f32_16x16x32_bf16 v[14:17], v[146:149], v[210:213], v[14:17]
	v_mfma_f32_16x16x32_bf16 v[10:13], v[138:141], v[218:221], v[10:13]
	v_mfma_f32_16x16x32_bf16 v[4:7], v[146:149], v[218:221], v[4:7]
	v_mfma_f32_16x16x32_bf16 v[102:105], v[170:173], v[190:193], v[102:105]
	v_mfma_f32_16x16x32_bf16 v[106:109], v[182:185], v[190:193], v[106:109]
	v_mfma_f32_16x16x32_bf16 v[110:113], v[170:173], v[198:201], v[110:113]
	v_mfma_f32_16x16x32_bf16 v[114:117], v[182:185], v[198:201], v[114:117]
	v_mfma_f32_16x16x32_bf16 v[118:121], v[170:173], v[206:209], v[118:121]
	v_mfma_f32_16x16x32_bf16 v[122:125], v[182:185], v[206:209], v[122:125]
	v_mfma_f32_16x16x32_bf16 v[126:129], v[170:173], v[214:217], v[126:129]
	v_mfma_f32_16x16x32_bf16 v[130:133], v[182:185], v[214:217], v[130:133]
	v_mfma_f32_16x16x32_bf16 v[102:105], v[178:181], v[194:197], v[102:105]
	v_mfma_f32_16x16x32_bf16 v[106:109], v[186:189], v[194:197], v[106:109]
	v_mfma_f32_16x16x32_bf16 v[110:113], v[178:181], v[202:205], v[110:113]
	v_mfma_f32_16x16x32_bf16 v[114:117], v[186:189], v[202:205], v[114:117]
	v_mfma_f32_16x16x32_bf16 v[118:121], v[178:181], v[210:213], v[118:121]
	v_mfma_f32_16x16x32_bf16 v[122:125], v[186:189], v[210:213], v[122:125]
	v_mfma_f32_16x16x32_bf16 v[126:129], v[178:181], v[218:221], v[126:129]
	v_mfma_f32_16x16x32_bf16 v[130:133], v[186:189], v[218:221], v[130:133]
	s_setprio 0
	s_barrier
	v_add_u32_e32 v3, s86, v174
	ds_read_b128 v[134:137], v3
	ds_read_b128 v[138:141], v3 offset:1024
	ds_read_b128 v[142:145], v3 offset:2048
	ds_read_b128 v[146:149], v3 offset:3072
	v_add_u32_e32 v3, s87, v174
	ds_read_b128 v[170:173], v3
	ds_read_b128 v[178:181], v3 offset:1024
	ds_read_b128 v[182:185], v3 offset:2048
	ds_read_b128 v[186:189], v3 offset:3072
	s_mov_b32 m0, s48
	v_lshl_add_u64 v[8:9], s[40:41], 0, v[158:159]
	ds_read_b128 v[190:193], v177 offset:32768
	ds_read_b128 v[194:197], v177 offset:33792
	ds_read_b128 v[198:201], v177 offset:34816
	ds_read_b128 v[202:205], v177 offset:35840
	ds_read_b128 v[206:209], v177 offset:36864
	ds_read_b128 v[210:213], v177 offset:37888
	ds_read_b128 v[214:217], v177 offset:38912
	ds_read_b128 v[218:221], v177 offset:39936
	global_load_lds_dwordx4 v[8:9], off
	v_lshl_add_u64 v[8:9], s[40:41], 0, v[160:161]
	s_mov_b32 m0, s49
	s_nop 0
	global_load_lds_dwordx4 v[8:9], off
	s_waitcnt vmcnt(8)
	s_waitcnt lgkmcnt(0)
	s_barrier
	s_setprio 1
	s_waitcnt lgkmcnt(0)
	v_mfma_f32_16x16x32_bf16 v[98:101], v[134:137], v[190:193], v[98:101]
	v_mfma_f32_16x16x32_bf16 v[94:97], v[142:145], v[190:193], v[94:97]
	v_mfma_f32_16x16x32_bf16 v[90:93], v[134:137], v[198:201], v[90:93]
	v_mfma_f32_16x16x32_bf16 v[86:89], v[142:145], v[198:201], v[86:89]
	v_mfma_f32_16x16x32_bf16 v[82:85], v[134:137], v[206:209], v[82:85]
	v_mfma_f32_16x16x32_bf16 v[78:81], v[142:145], v[206:209], v[78:81]
	v_mfma_f32_16x16x32_bf16 v[74:77], v[134:137], v[214:217], v[74:77]
	v_mfma_f32_16x16x32_bf16 v[70:73], v[142:145], v[214:217], v[70:73]
	v_mfma_f32_16x16x32_bf16 v[98:101], v[138:141], v[194:197], v[98:101]
	v_mfma_f32_16x16x32_bf16 v[94:97], v[146:149], v[194:197], v[94:97]
	v_mfma_f32_16x16x32_bf16 v[90:93], v[138:141], v[202:205], v[90:93]
	v_mfma_f32_16x16x32_bf16 v[86:89], v[146:149], v[202:205], v[86:89]
	v_mfma_f32_16x16x32_bf16 v[82:85], v[138:141], v[210:213], v[82:85]
	v_mfma_f32_16x16x32_bf16 v[78:81], v[146:149], v[210:213], v[78:81]
	v_mfma_f32_16x16x32_bf16 v[74:77], v[138:141], v[218:221], v[74:77]
	v_mfma_f32_16x16x32_bf16 v[70:73], v[146:149], v[218:221], v[70:73]
	v_mfma_f32_16x16x32_bf16 v[66:69], v[170:173], v[190:193], v[66:69]
	v_mfma_f32_16x16x32_bf16 v[62:65], v[182:185], v[190:193], v[62:65]
	v_mfma_f32_16x16x32_bf16 v[58:61], v[170:173], v[198:201], v[58:61]
	v_mfma_f32_16x16x32_bf16 v[54:57], v[182:185], v[198:201], v[54:57]
	v_mfma_f32_16x16x32_bf16 v[50:53], v[170:173], v[206:209], v[50:53]
	v_mfma_f32_16x16x32_bf16 v[46:49], v[182:185], v[206:209], v[46:49]
	v_mfma_f32_16x16x32_bf16 v[42:45], v[170:173], v[214:217], v[42:45]
	v_mfma_f32_16x16x32_bf16 v[38:41], v[182:185], v[214:217], v[38:41]
	v_mfma_f32_16x16x32_bf16 v[66:69], v[178:181], v[194:197], v[66:69]
	v_mfma_f32_16x16x32_bf16 v[62:65], v[186:189], v[194:197], v[62:65]
	v_mfma_f32_16x16x32_bf16 v[58:61], v[178:181], v[202:205], v[58:61]
	v_mfma_f32_16x16x32_bf16 v[54:57], v[186:189], v[202:205], v[54:57]
	v_mfma_f32_16x16x32_bf16 v[50:53], v[178:181], v[210:213], v[50:53]
	v_mfma_f32_16x16x32_bf16 v[46:49], v[186:189], v[210:213], v[46:49]
	v_mfma_f32_16x16x32_bf16 v[42:45], v[178:181], v[218:221], v[42:45]
	v_mfma_f32_16x16x32_bf16 v[38:41], v[186:189], v[218:221], v[38:41]
	s_setprio 0
	s_barrier
	s_add_i32 s40, s86, s45
	v_lshl_add_u64 v[8:9], v[222:223], 0, s[6:7]
	s_mov_b32 m0, s40
	ds_read_b128 v[190:193], v177 offset:49152
	ds_read_b128 v[194:197], v177 offset:50176
	ds_read_b128 v[198:201], v177 offset:51200
	ds_read_b128 v[202:205], v177 offset:52224
	ds_read_b128 v[206:209], v177 offset:53248
	ds_read_b128 v[210:213], v177 offset:54272
	ds_read_b128 v[214:217], v177 offset:55296
	ds_read_b128 v[218:221], v177 offset:56320
	global_load_lds_dwordx4 v[8:9], off
	s_add_i32 m0, s40, 0x2000
	s_add_u32 s38, s38, 0x80080
	v_lshl_add_u64 v[8:9], v[224:225], 0, s[6:7]
	s_addc_u32 s39, s39, 0
	s_add_i32 s40, s87, s45
	global_load_lds_dwordx4 v[8:9], off
	v_lshl_add_u64 v[8:9], s[38:39], 0, v[150:151]
	s_mov_b32 m0, s40
	s_nop 0
	global_load_lds_dwordx4 v[8:9], off
	v_lshl_add_u64 v[8:9], s[38:39], 0, v[152:153]
	s_add_i32 m0, s40, 0x2000
	s_nop 0
	global_load_lds_dwordx4 v[8:9], off
	v_lshl_add_u64 v[8:9], v[226:227], 0, s[6:7]
	s_mov_b32 m0, s51
	s_nop 0
	global_load_lds_dwordx4 v[8:9], off
	v_lshl_add_u64 v[8:9], v[230:231], 0, s[6:7]
	s_mov_b32 m0, s52
	s_nop 0
	global_load_lds_dwordx4 v[8:9], off
	s_waitcnt vmcnt(8)
	s_waitcnt lgkmcnt(0)
	s_barrier
	s_setprio 1
	s_waitcnt lgkmcnt(0)
	v_mfma_f32_16x16x32_bf16 v[34:37], v[134:137], v[190:193], v[34:37]
	v_mfma_f32_16x16x32_bf16 v[30:33], v[142:145], v[190:193], v[30:33]
	v_mfma_f32_16x16x32_bf16 v[26:29], v[134:137], v[198:201], v[26:29]
	v_mfma_f32_16x16x32_bf16 v[22:25], v[142:145], v[198:201], v[22:25]
	v_mfma_f32_16x16x32_bf16 v[18:21], v[134:137], v[206:209], v[18:21]
	v_mfma_f32_16x16x32_bf16 v[14:17], v[142:145], v[206:209], v[14:17]
	v_mfma_f32_16x16x32_bf16 v[8:11], v[134:137], v[214:217], v[10:13]
	v_mfma_f32_16x16x32_bf16 v[4:7], v[142:145], v[214:217], v[4:7]
	v_mfma_f32_16x16x32_bf16 v[34:37], v[138:141], v[194:197], v[34:37]
	v_mfma_f32_16x16x32_bf16 v[30:33], v[146:149], v[194:197], v[30:33]
	v_mfma_f32_16x16x32_bf16 v[26:29], v[138:141], v[202:205], v[26:29]
	v_mfma_f32_16x16x32_bf16 v[22:25], v[146:149], v[202:205], v[22:25]
	v_mfma_f32_16x16x32_bf16 v[18:21], v[138:141], v[210:213], v[18:21]
	v_mfma_f32_16x16x32_bf16 v[14:17], v[146:149], v[210:213], v[14:17]
	v_mfma_f32_16x16x32_bf16 v[10:13], v[138:141], v[218:221], v[8:11]
	v_mfma_f32_16x16x32_bf16 v[6:9], v[146:149], v[218:221], v[4:7]
	v_mfma_f32_16x16x32_bf16 v[102:105], v[170:173], v[190:193], v[102:105]
	v_mfma_f32_16x16x32_bf16 v[106:109], v[182:185], v[190:193], v[106:109]
	v_mfma_f32_16x16x32_bf16 v[110:113], v[170:173], v[198:201], v[110:113]
	v_mfma_f32_16x16x32_bf16 v[114:117], v[182:185], v[198:201], v[114:117]
	v_mfma_f32_16x16x32_bf16 v[118:121], v[170:173], v[206:209], v[118:121]
	v_mfma_f32_16x16x32_bf16 v[122:125], v[182:185], v[206:209], v[122:125]
	v_mfma_f32_16x16x32_bf16 v[126:129], v[170:173], v[214:217], v[126:129]
	v_mfma_f32_16x16x32_bf16 v[130:133], v[182:185], v[214:217], v[130:133]
	v_mfma_f32_16x16x32_bf16 v[102:105], v[178:181], v[194:197], v[102:105]
	v_mfma_f32_16x16x32_bf16 v[106:109], v[186:189], v[194:197], v[106:109]
	v_mfma_f32_16x16x32_bf16 v[110:113], v[178:181], v[202:205], v[110:113]
	v_mfma_f32_16x16x32_bf16 v[114:117], v[186:189], v[202:205], v[114:117]
	v_mfma_f32_16x16x32_bf16 v[118:121], v[178:181], v[210:213], v[118:121]
	v_mfma_f32_16x16x32_bf16 v[122:125], v[186:189], v[210:213], v[122:125]
	v_mfma_f32_16x16x32_bf16 v[126:129], v[178:181], v[218:221], v[126:129]
	v_mfma_f32_16x16x32_bf16 v[130:133], v[186:189], v[218:221], v[130:133]
	s_setprio 0
	s_barrier
	s_add_i32 s61, s61, 2
	s_add_u32 s36, s36, 0x100
	s_addc_u32 s37, s37, 0
	s_add_u32 s27, s27, 0x100
	s_addc_u32 s60, s60, 0
	s_cmp_gt_u32 s61, 13
	s_cbranch_scc0 .LBB0_1003
	s_and_b64 vcc, exec, s[10:11]
	s_cbranch_vccz .LBB0_1006
	s_barrier

.LBB0_1089:
	ds_read_b128 v[150:153], v156
	ds_read_b128 v[160:163], v156 offset:1024
	ds_read_b128 v[164:167], v156 offset:2048
	ds_read_b128 v[168:171], v156 offset:3072
	ds_read_b128 v[172:175], v157
	ds_read_b128 v[176:179], v157 offset:1024
	ds_read_b128 v[180:183], v157 offset:2048
	ds_read_b128 v[184:187], v157 offset:3072
	s_add_u32 s28, s26, 0x80
	s_addc_u32 s29, s27, 0
	s_cmp_eq_u32 s49, 28
	s_cselect_b32 s31, s23, s29
	s_cselect_b32 s30, s22, s28
	s_cselect_b32 s29, s25, s21
	s_cselect_b32 s28, s24, s19
	v_lshl_add_u64 v[220:221], s[26:27], 0, v[144:145]
	s_add_i32 m0, s38, 0xc000
	ds_read_b128 v[188:191], v158
	ds_read_b128 v[192:195], v158 offset:1024
	ds_read_b128 v[196:199], v158 offset:2048
	ds_read_b128 v[200:203], v158 offset:3072
	ds_read_b128 v[204:207], v158 offset:4096
	ds_read_b128 v[208:211], v158 offset:5120
	ds_read_b128 v[212:215], v158 offset:6144
	ds_read_b128 v[216:219], v158 offset:7168
	global_load_lds_dwordx4 v[220:221], off
	v_lshl_add_u64 v[220:221], s[26:27], 0, v[142:143]
	s_add_i32 m0, s38, 0xe000
	s_nop 0
	global_load_lds_dwordx4 v[220:221], off
	s_waitcnt vmcnt(8)
	s_waitcnt lgkmcnt(0)
	s_barrier
	s_setprio 1
	s_waitcnt lgkmcnt(0)
	v_mfma_f32_16x16x32_bf16 v[126:129], v[150:153], v[188:191], v[126:129]
	v_mfma_f32_16x16x32_bf16 v[122:125], v[164:167], v[188:191], v[122:125]
	v_mfma_f32_16x16x32_bf16 v[110:113], v[150:153], v[196:199], v[110:113]
	v_mfma_f32_16x16x32_bf16 v[106:109], v[164:167], v[196:199], v[106:109]
	v_mfma_f32_16x16x32_bf16 v[94:97], v[150:153], v[204:207], v[94:97]
	v_mfma_f32_16x16x32_bf16 v[90:93], v[164:167], v[204:207], v[90:93]
	v_mfma_f32_16x16x32_bf16 v[78:81], v[150:153], v[212:215], v[78:81]
	v_mfma_f32_16x16x32_bf16 v[74:77], v[164:167], v[212:215], v[74:77]
	v_mfma_f32_16x16x32_bf16 v[126:129], v[160:163], v[192:195], v[126:129]
	v_mfma_f32_16x16x32_bf16 v[122:125], v[168:171], v[192:195], v[122:125]
	v_mfma_f32_16x16x32_bf16 v[110:113], v[160:163], v[200:203], v[110:113]
	v_mfma_f32_16x16x32_bf16 v[106:109], v[168:171], v[200:203], v[106:109]
	v_mfma_f32_16x16x32_bf16 v[94:97], v[160:163], v[208:211], v[94:97]
	v_mfma_f32_16x16x32_bf16 v[90:93], v[168:171], v[208:211], v[90:93]
	v_mfma_f32_16x16x32_bf16 v[78:81], v[160:163], v[216:219], v[78:81]
	v_mfma_f32_16x16x32_bf16 v[74:77], v[168:171], v[216:219], v[74:77]
	v_mfma_f32_16x16x32_bf16 v[118:121], v[172:175], v[188:191], v[118:121]
	v_mfma_f32_16x16x32_bf16 v[114:117], v[180:183], v[188:191], v[114:117]
	v_mfma_f32_16x16x32_bf16 v[102:105], v[172:175], v[196:199], v[102:105]
	v_mfma_f32_16x16x32_bf16 v[98:101], v[180:183], v[196:199], v[98:101]
	v_mfma_f32_16x16x32_bf16 v[86:89], v[172:175], v[204:207], v[86:89]
	v_mfma_f32_16x16x32_bf16 v[82:85], v[180:183], v[204:207], v[82:85]
	v_mfma_f32_16x16x32_bf16 v[70:73], v[172:175], v[212:215], v[70:73]
	v_mfma_f32_16x16x32_bf16 v[66:69], v[180:183], v[212:215], v[66:69]
	v_mfma_f32_16x16x32_bf16 v[118:121], v[176:179], v[192:195], v[118:121]
	v_mfma_f32_16x16x32_bf16 v[114:117], v[184:187], v[192:195], v[114:117]
	v_mfma_f32_16x16x32_bf16 v[102:105], v[176:179], v[200:203], v[102:105]
	v_mfma_f32_16x16x32_bf16 v[98:101], v[184:187], v[200:203], v[98:101]
	v_mfma_f32_16x16x32_bf16 v[86:89], v[176:179], v[208:211], v[86:89]
	v_mfma_f32_16x16x32_bf16 v[82:85], v[184:187], v[208:211], v[82:85]
	v_mfma_f32_16x16x32_bf16 v[70:73], v[176:179], v[216:219], v[70:73]
	v_mfma_f32_16x16x32_bf16 v[66:69], v[184:187], v[216:219], v[66:69]
	s_setprio 0
	s_barrier
	s_add_i32 s50, s3, s37
	v_lshl_add_u64 v[220:221], s[28:29], 0, v[130:131]
	s_mov_b32 m0, s50
	ds_read_b128 v[188:191], v158 offset:16384
	ds_read_b128 v[192:195], v158 offset:17408
	ds_read_b128 v[196:199], v158 offset:18432
	ds_read_b128 v[200:203], v158 offset:19456
	ds_read_b128 v[204:207], v158 offset:20480
	ds_read_b128 v[208:211], v158 offset:21504
	ds_read_b128 v[212:215], v158 offset:22528
	ds_read_b128 v[216:219], v158 offset:23552
	global_load_lds_dwordx4 v[220:221], off
	s_add_i32 m0, s50, 0x2000
	s_add_u32 s50, s28, 0x80000
	v_lshl_add_u64 v[222:223], s[28:29], 0, v[132:133]
	s_addc_u32 s51, s29, 0
	s_add_i32 s52, s2, s37
	global_load_lds_dwordx4 v[222:223], off
	v_lshl_add_u64 v[224:225], s[50:51], 0, v[130:131]
	s_mov_b32 m0, s52
	v_lshl_add_u64 v[226:227], s[30:31], 0, v[136:137]
	global_load_lds_dwordx4 v[224:225], off
	v_lshl_add_u64 v[224:225], s[50:51], 0, v[132:133]
	s_add_i32 m0, s52, 0x2000
	s_nop 0
	global_load_lds_dwordx4 v[224:225], off
	v_lshl_add_u64 v[224:225], s[30:31], 0, v[134:135]
	s_mov_b32 m0, s38
	s_nop 0
	global_load_lds_dwordx4 v[224:225], off
	s_mov_b32 m0, s39
	s_nop 0
	global_load_lds_dwordx4 v[226:227], off
	s_waitcnt vmcnt(8)
	s_waitcnt lgkmcnt(0)
	s_barrier
	s_setprio 1
	s_waitcnt lgkmcnt(0)
	v_mfma_f32_16x16x32_bf16 v[54:57], v[150:153], v[188:191], v[54:57]
	v_mfma_f32_16x16x32_bf16 v[50:53], v[164:167], v[188:191], v[50:53]
	v_mfma_f32_16x16x32_bf16 v[38:41], v[150:153], v[196:199], v[38:41]
	v_mfma_f32_16x16x32_bf16 v[34:37], v[164:167], v[196:199], v[34:37]
	v_mfma_f32_16x16x32_bf16 v[22:25], v[150:153], v[204:207], v[22:25]
	v_mfma_f32_16x16x32_bf16 v[18:21], v[164:167], v[204:207], v[18:21]
	v_mfma_f32_16x16x32_bf16 v[6:9], v[150:153], v[212:215], v[6:9]
	v_mfma_f32_16x16x32_bf16 v[2:5], v[164:167], v[212:215], v[2:5]
	v_mfma_f32_16x16x32_bf16 v[54:57], v[160:163], v[192:195], v[54:57]
	v_mfma_f32_16x16x32_bf16 v[50:53], v[168:171], v[192:195], v[50:53]
	v_mfma_f32_16x16x32_bf16 v[38:41], v[160:163], v[200:203], v[38:41]
	v_mfma_f32_16x16x32_bf16 v[34:37], v[168:171], v[200:203], v[34:37]
	v_mfma_f32_16x16x32_bf16 v[22:25], v[160:163], v[208:211], v[22:25]
	v_mfma_f32_16x16x32_bf16 v[18:21], v[168:171], v[208:211], v[18:21]
	v_mfma_f32_16x16x32_bf16 v[6:9], v[160:163], v[216:219], v[6:9]
	v_mfma_f32_16x16x32_bf16 v[2:5], v[168:171], v[216:219], v[2:5]
	v_mfma_f32_16x16x32_bf16 v[62:65], v[172:175], v[188:191], v[62:65]
	v_mfma_f32_16x16x32_bf16 v[58:61], v[180:183], v[188:191], v[58:61]
	v_mfma_f32_16x16x32_bf16 v[46:49], v[172:175], v[196:199], v[46:49]
	v_mfma_f32_16x16x32_bf16 v[42:45], v[180:183], v[196:199], v[42:45]
	v_mfma_f32_16x16x32_bf16 v[30:33], v[172:175], v[204:207], v[30:33]
	v_mfma_f32_16x16x32_bf16 v[26:29], v[180:183], v[204:207], v[26:29]
	v_mfma_f32_16x16x32_bf16 v[14:17], v[172:175], v[212:215], v[14:17]
	v_mfma_f32_16x16x32_bf16 v[10:13], v[180:183], v[212:215], v[10:13]
	v_mfma_f32_16x16x32_bf16 v[62:65], v[176:179], v[192:195], v[62:65]
	v_mfma_f32_16x16x32_bf16 v[58:61], v[184:187], v[192:195], v[58:61]
	v_mfma_f32_16x16x32_bf16 v[46:49], v[176:179], v[200:203], v[46:49]
	v_mfma_f32_16x16x32_bf16 v[42:45], v[184:187], v[200:203], v[42:45]
	v_mfma_f32_16x16x32_bf16 v[30:33], v[176:179], v[208:211], v[30:33]
	v_mfma_f32_16x16x32_bf16 v[26:29], v[184:187], v[208:211], v[26:29]
	v_mfma_f32_16x16x32_bf16 v[14:17], v[176:179], v[216:219], v[14:17]
	v_mfma_f32_16x16x32_bf16 v[10:13], v[184:187], v[216:219], v[10:13]
	s_setprio 0
	s_barrier
	v_add_u32_e32 v168, s86, v154
	v_add_u32_e32 v184, s87, v154
	ds_read_b128 v[150:153], v168
	ds_read_b128 v[160:163], v168 offset:1024
	ds_read_b128 v[164:167], v168 offset:2048
	ds_read_b128 v[168:171], v168 offset:3072
	ds_read_b128 v[172:175], v184
	ds_read_b128 v[176:179], v184 offset:1024
	ds_read_b128 v[180:183], v184 offset:2048
	ds_read_b128 v[184:187], v184 offset:3072
	s_mov_b32 m0, s40
	v_lshl_add_u64 v[230:231], s[30:31], 0, v[138:139]
	ds_read_b128 v[188:191], v158 offset:32768
	ds_read_b128 v[192:195], v158 offset:33792
	ds_read_b128 v[196:199], v158 offset:34816
	ds_read_b128 v[200:203], v158 offset:35840
	ds_read_b128 v[204:207], v158 offset:36864
	ds_read_b128 v[208:211], v158 offset:37888
	ds_read_b128 v[212:215], v158 offset:38912
	ds_read_b128 v[216:219], v158 offset:39936
	global_load_lds_dwordx4 v[230:231], off
	v_lshl_add_u64 v[230:231], s[30:31], 0, v[140:141]
	s_mov_b32 m0, s41
	s_nop 0
	global_load_lds_dwordx4 v[230:231], off
	s_waitcnt vmcnt(8)
	s_waitcnt lgkmcnt(0)
	s_barrier
	s_setprio 1
	s_waitcnt lgkmcnt(0)
	v_mfma_f32_16x16x32_bf16 v[126:129], v[150:153], v[188:191], v[126:129]
	v_mfma_f32_16x16x32_bf16 v[122:125], v[164:167], v[188:191], v[122:125]
	v_mfma_f32_16x16x32_bf16 v[110:113], v[150:153], v[196:199], v[110:113]
	v_mfma_f32_16x16x32_bf16 v[106:109], v[164:167], v[196:199], v[106:109]
	v_mfma_f32_16x16x32_bf16 v[94:97], v[150:153], v[204:207], v[94:97]
	v_mfma_f32_16x16x32_bf16 v[90:93], v[164:167], v[204:207], v[90:93]
	v_mfma_f32_16x16x32_bf16 v[78:81], v[150:153], v[212:215], v[78:81]
	v_mfma_f32_16x16x32_bf16 v[74:77], v[164:167], v[212:215], v[74:77]
	v_mfma_f32_16x16x32_bf16 v[126:129], v[160:163], v[192:195], v[126:129]
	v_mfma_f32_16x16x32_bf16 v[122:125], v[168:171], v[192:195], v[122:125]
	v_mfma_f32_16x16x32_bf16 v[110:113], v[160:163], v[200:203], v[110:113]
	v_mfma_f32_16x16x32_bf16 v[106:109], v[168:171], v[200:203], v[106:109]
	v_mfma_f32_16x16x32_bf16 v[94:97], v[160:163], v[208:211], v[94:97]
	v_mfma_f32_16x16x32_bf16 v[90:93], v[168:171], v[208:211], v[90:93]
	v_mfma_f32_16x16x32_bf16 v[78:81], v[160:163], v[216:219], v[78:81]
	v_mfma_f32_16x16x32_bf16 v[74:77], v[168:171], v[216:219], v[74:77]
	v_mfma_f32_16x16x32_bf16 v[118:121], v[172:175], v[188:191], v[118:121]
	v_mfma_f32_16x16x32_bf16 v[114:117], v[180:183], v[188:191], v[114:117]
	v_mfma_f32_16x16x32_bf16 v[102:105], v[172:175], v[196:199], v[102:105]
	v_mfma_f32_16x16x32_bf16 v[98:101], v[180:183], v[196:199], v[98:101]
	v_mfma_f32_16x16x32_bf16 v[86:89], v[172:175], v[204:207], v[86:89]
	v_mfma_f32_16x16x32_bf16 v[82:85], v[180:183], v[204:207], v[82:85]
	v_mfma_f32_16x16x32_bf16 v[70:73], v[172:175], v[212:215], v[70:73]
	v_mfma_f32_16x16x32_bf16 v[66:69], v[180:183], v[212:215], v[66:69]
	v_mfma_f32_16x16x32_bf16 v[118:121], v[176:179], v[192:195], v[118:121]
	v_mfma_f32_16x16x32_bf16 v[114:117], v[184:187], v[192:195], v[114:117]
	v_mfma_f32_16x16x32_bf16 v[102:105], v[176:179], v[200:203], v[102:105]
	v_mfma_f32_16x16x32_bf16 v[98:101], v[184:187], v[200:203], v[98:101]
	v_mfma_f32_16x16x32_bf16 v[86:89], v[176:179], v[208:211], v[86:89]
	v_mfma_f32_16x16x32_bf16 v[82:85], v[184:187], v[208:211], v[82:85]
	v_mfma_f32_16x16x32_bf16 v[70:73], v[176:179], v[216:219], v[70:73]
	v_mfma_f32_16x16x32_bf16 v[66:69], v[184:187], v[216:219], v[66:69]
	s_setprio 0
	s_barrier
	s_add_i32 s30, s86, s37
	v_lshl_add_u64 v[220:221], v[220:221], 0, s[14:15]
	s_mov_b32 m0, s30
	ds_read_b128 v[188:191], v158 offset:49152
	ds_read_b128 v[192:195], v158 offset:50176
	ds_read_b128 v[196:199], v158 offset:51200
	ds_read_b128 v[200:203], v158 offset:52224
	ds_read_b128 v[204:207], v158 offset:53248
	ds_read_b128 v[208:211], v158 offset:54272
	ds_read_b128 v[212:215], v158 offset:55296
	ds_read_b128 v[216:219], v158 offset:56320
	global_load_lds_dwordx4 v[220:221], off
	s_add_i32 m0, s30, 0x2000
	s_add_u32 s28, s28, 0x80080
	v_lshl_add_u64 v[220:221], v[222:223], 0, s[14:15]
	s_addc_u32 s29, s29, 0
	s_add_i32 s30, s87, s37
	global_load_lds_dwordx4 v[220:221], off
	v_lshl_add_u64 v[220:221], s[28:29], 0, v[130:131]
	s_mov_b32 m0, s30
	s_nop 0
	global_load_lds_dwordx4 v[220:221], off
	v_lshl_add_u64 v[220:221], s[28:29], 0, v[132:133]
	s_add_i32 m0, s30, 0x2000
	s_nop 0
	global_load_lds_dwordx4 v[220:221], off
	v_lshl_add_u64 v[220:221], v[224:225], 0, s[14:15]
	s_mov_b32 m0, s43
	s_nop 0
	global_load_lds_dwordx4 v[220:221], off
	v_lshl_add_u64 v[220:221], v[226:227], 0, s[14:15]
	s_mov_b32 m0, s44
	s_nop 0
	global_load_lds_dwordx4 v[220:221], off
	s_waitcnt vmcnt(8)
	s_waitcnt lgkmcnt(0)
	s_barrier
	s_setprio 1
	s_waitcnt lgkmcnt(0)
	v_mfma_f32_16x16x32_bf16 v[54:57], v[150:153], v[188:191], v[54:57]
	v_mfma_f32_16x16x32_bf16 v[50:53], v[164:167], v[188:191], v[50:53]
	v_mfma_f32_16x16x32_bf16 v[38:41], v[150:153], v[196:199], v[38:41]
	v_mfma_f32_16x16x32_bf16 v[34:37], v[164:167], v[196:199], v[34:37]
	v_mfma_f32_16x16x32_bf16 v[22:25], v[150:153], v[204:207], v[22:25]
	v_mfma_f32_16x16x32_bf16 v[18:21], v[164:167], v[204:207], v[18:21]
	v_mfma_f32_16x16x32_bf16 v[6:9], v[150:153], v[212:215], v[6:9]
	v_mfma_f32_16x16x32_bf16 v[2:5], v[164:167], v[212:215], v[2:5]
	v_mfma_f32_16x16x32_bf16 v[54:57], v[160:163], v[192:195], v[54:57]
	v_mfma_f32_16x16x32_bf16 v[50:53], v[168:171], v[192:195], v[50:53]
	v_mfma_f32_16x16x32_bf16 v[38:41], v[160:163], v[200:203], v[38:41]
	v_mfma_f32_16x16x32_bf16 v[34:37], v[168:171], v[200:203], v[34:37]
	v_mfma_f32_16x16x32_bf16 v[22:25], v[160:163], v[208:211], v[22:25]
	v_mfma_f32_16x16x32_bf16 v[18:21], v[168:171], v[208:211], v[18:21]
	v_mfma_f32_16x16x32_bf16 v[6:9], v[160:163], v[216:219], v[6:9]
	v_mfma_f32_16x16x32_bf16 v[2:5], v[168:171], v[216:219], v[2:5]
	v_mfma_f32_16x16x32_bf16 v[62:65], v[172:175], v[188:191], v[62:65]
	v_mfma_f32_16x16x32_bf16 v[58:61], v[180:183], v[188:191], v[58:61]
	v_mfma_f32_16x16x32_bf16 v[46:49], v[172:175], v[196:199], v[46:49]
	v_mfma_f32_16x16x32_bf16 v[42:45], v[180:183], v[196:199], v[42:45]
	v_mfma_f32_16x16x32_bf16 v[30:33], v[172:175], v[204:207], v[30:33]
	v_mfma_f32_16x16x32_bf16 v[26:29], v[180:183], v[204:207], v[26:29]
	v_mfma_f32_16x16x32_bf16 v[14:17], v[172:175], v[212:215], v[14:17]
	v_mfma_f32_16x16x32_bf16 v[10:13], v[180:183], v[212:215], v[10:13]
	v_mfma_f32_16x16x32_bf16 v[62:65], v[176:179], v[192:195], v[62:65]
	v_mfma_f32_16x16x32_bf16 v[58:61], v[184:187], v[192:195], v[58:61]
	v_mfma_f32_16x16x32_bf16 v[46:49], v[176:179], v[200:203], v[46:49]
	v_mfma_f32_16x16x32_bf16 v[42:45], v[184:187], v[200:203], v[42:45]
	v_mfma_f32_16x16x32_bf16 v[30:33], v[176:179], v[208:211], v[30:33]
	v_mfma_f32_16x16x32_bf16 v[26:29], v[184:187], v[208:211], v[26:29]
	v_mfma_f32_16x16x32_bf16 v[14:17], v[176:179], v[216:219], v[14:17]
	v_mfma_f32_16x16x32_bf16 v[10:13], v[184:187], v[216:219], v[10:13]
	s_setprio 0
	s_barrier
	s_add_i32 s49, s49, 2
	s_add_u32 s26, s26, 0x100
	s_addc_u32 s27, s27, 0
	s_add_u32 s19, s19, 0x100
	s_addc_u32 s21, s21, 0
	s_cmp_gt_u32 s49, 29
	s_cbranch_scc0 .LBB0_1089
	s_and_b64 vcc, exec, s[16:17]
	s_cbranch_vccz .LBB0_1092
	s_barrier

.LBB0_1346:
	s_ashr_i32 s17, s16, 31
	s_lshl_b64 s[24:25], s[16:17], 16
	s_add_i32 s17, s50, 0x80
	v_add_u32_e32 v202, s17, v1
	v_add_u32_e32 v203, s17, v190
	s_lshl_b32 s17, s16, 2
	s_add_i32 s17, s17, 0
	s_add_i32 s17, s17, 0x20000
	s_add_u32 s24, s18, s24
	s_addc_u32 s25, s19, s25
	v_mov_b32_e32 v175, v167
	v_mov_b32_e32 v173, v167
	s_add_u32 s56, s26, 0x100
	v_add_u32_e32 v200, s50, v1
	v_add_u32_e32 v201, s50, v190
	v_lshl_add_u64 v[178:179], s[10:11], 0, v[172:173]
	v_lshl_add_u64 v[180:181], s[10:11], 0, v[174:175]
	s_addc_u32 s57, s27, 0
	s_mov_b32 s58, -2
	s_mov_b64 s[26:27], 0
	s_xor_b64 s[28:29], s[22:23], -1
	v_mov_b32_e32 v169, v199
	v_mov_b32_e32 v171, v176
	v_mov_b32_e32 v173, v174
	v_mov_b32_e32 v175, v172
	s_add_u32 s30, s84, s26
	s_addc_u32 s31, s85, s27
	v_add_u32_e32 v2, s3, v193
	v_add_u32_e32 v14, s2, v193
	s_add_u32 s34, s30, 0x35400100
	ds_read_b128 v[18:21], v2
	ds_read_b128 v[22:25], v2 offset:1024
	ds_read_b128 v[26:29], v2 offset:2048
	ds_read_b128 v[30:33], v2 offset:3072
	ds_read_b128 v[2:5], v14
	ds_read_b128 v[6:9], v14 offset:1024
	ds_read_b128 v[10:13], v14 offset:2048
	ds_read_b128 v[14:17], v14 offset:3072
	s_addc_u32 s35, s31, 0
	s_add_u32 s59, s56, s26
	s_addc_u32 s60, s57, s27
	s_cmpk_eq_i32 s26, 0x700
	s_cselect_b64 vcc, -1, 0
	s_and_b64 s[30:31], vcc, exec
	v_cndmask_b32_e32 v166, v199, v169, vcc
	s_cselect_b32 s35, s5, s35
	s_cselect_b32 s34, s4, s34
	v_cndmask_b32_e32 v238, v176, v171, vcc
	v_cndmask_b32_e32 v229, v174, v173, vcc
	v_cndmask_b32_e32 v240, v172, v175, vcc
	s_cselect_b32 s31, s21, s60
	s_cselect_b32 s30, s20, s59
	v_lshl_add_u64 v[230:231], v[180:181], 0, s[26:27]
	s_add_i32 m0, s39, 0xc000
	ds_read_b128 v[182:185], v197
	ds_read_b128 v[186:189], v197 offset:1024
	ds_read_b128 v[204:207], v197 offset:2048
	ds_read_b128 v[208:211], v197 offset:3072
	ds_read_b128 v[212:215], v197 offset:4096
	ds_read_b128 v[216:219], v197 offset:5120
	ds_read_b128 v[220:223], v197 offset:6144
	ds_read_b128 v[224:227], v197 offset:7168
	global_load_lds_dwordx4 v[230:231], off
	v_lshl_add_u64 v[230:231], v[178:179], 0, s[26:27]
	s_add_i32 m0, s39, 0xe000
	s_nop 0
	global_load_lds_dwordx4 v[230:231], off
	s_waitcnt vmcnt(8)
	s_waitcnt lgkmcnt(0)
	s_barrier
	s_setprio 1
	s_waitcnt lgkmcnt(0)
	s_nop 1
	v_mfma_f32_16x16x128_f8f6f4 v[158:161], v[18:25], v[182:189], 0
	v_mfma_f32_16x16x128_f8f6f4 v[150:153], v[26:33], v[182:189], 0
	v_mfma_f32_16x16x128_f8f6f4 v[142:145], v[18:25], v[204:211], 0
	v_mfma_f32_16x16x128_f8f6f4 v[134:137], v[26:33], v[204:211], 0
	v_mfma_f32_16x16x128_f8f6f4 v[126:129], v[18:25], v[212:219], 0
	v_mfma_f32_16x16x128_f8f6f4 v[118:121], v[26:33], v[212:219], 0
	v_mfma_f32_16x16x128_f8f6f4 v[110:113], v[18:25], v[220:227], 0
	v_mfma_f32_16x16x128_f8f6f4 v[102:105], v[26:33], v[220:227], 0
	s_nop 1
	v_mfma_f32_16x16x128_f8f6f4 v[154:157], v[2:9], v[182:189], 0
	v_mfma_f32_16x16x128_f8f6f4 v[146:149], v[10:17], v[182:189], 0
	v_mfma_f32_16x16x128_f8f6f4 v[138:141], v[2:9], v[204:211], 0
	v_mfma_f32_16x16x128_f8f6f4 v[130:133], v[10:17], v[204:211], 0
	v_mfma_f32_16x16x128_f8f6f4 v[122:125], v[2:9], v[212:219], 0
	v_mfma_f32_16x16x128_f8f6f4 v[114:117], v[10:17], v[212:219], 0
	v_mfma_f32_16x16x128_f8f6f4 v[106:109], v[2:9], v[220:227], 0
	v_mfma_f32_16x16x128_f8f6f4 v[98:101], v[10:17], v[220:227], 0
	s_setprio 0
	s_barrier
	s_add_i32 s59, s3, s38
	v_lshl_add_u64 v[182:183], s[30:31], 0, v[164:165]
	s_mov_b32 m0, s59
	ds_read_b128 v[204:207], v197 offset:16384
	ds_read_b128 v[208:211], v197 offset:17408
	ds_read_b128 v[212:215], v197 offset:18432
	ds_read_b128 v[216:219], v197 offset:19456
	ds_read_b128 v[220:223], v197 offset:20480
	ds_read_b128 v[224:227], v197 offset:21504
	ds_read_b128 v[230:233], v197 offset:22528
	ds_read_b128 v[234:237], v197 offset:23552
	global_load_lds_dwordx4 v[182:183], off
	s_add_i32 m0, s59, 0x2000
	s_add_u32 s60, s30, 0x40000
	v_lshl_add_u64 v[184:185], s[30:31], 0, v[162:163]
	s_addc_u32 s61, s31, 0
	s_add_i32 s59, s2, s38
	global_load_lds_dwordx4 v[184:185], off
	v_lshl_add_u64 v[186:187], s[60:61], 0, v[164:165]
	s_mov_b32 m0, s59
	v_mov_b32_e32 v239, v167
	global_load_lds_dwordx4 v[186:187], off
	v_lshl_add_u64 v[186:187], s[60:61], 0, v[162:163]
	s_add_i32 m0, s59, 0x2000
	v_lshl_add_u64 v[188:189], s[34:35], 0, v[166:167]
	global_load_lds_dwordx4 v[186:187], off
	s_mov_b32 m0, s39
	v_lshl_add_u64 v[186:187], s[34:35], 0, v[238:239]
	global_load_lds_dwordx4 v166, s[34:35]
	s_mov_b32 m0, s40
	s_nop 0
	global_load_lds_dwordx4 v238, s[34:35]
	s_waitcnt vmcnt(8)
	s_waitcnt lgkmcnt(0)
	s_barrier
	s_setprio 1
	s_waitcnt lgkmcnt(0)
	s_nop 1
	v_mfma_f32_16x16x128_f8f6f4 v[94:97], v[18:25], v[204:211], 0
	v_mfma_f32_16x16x128_f8f6f4 v[86:89], v[26:33], v[204:211], 0
	v_mfma_f32_16x16x128_f8f6f4 v[78:81], v[18:25], v[212:219], 0
	v_mfma_f32_16x16x128_f8f6f4 v[66:69], v[26:33], v[212:219], 0
	v_mfma_f32_16x16x128_f8f6f4 v[54:57], v[18:25], v[220:227], 0
	v_mfma_f32_16x16x128_f8f6f4 v[46:49], v[26:33], v[220:227], 0
	v_mfma_f32_16x16x128_f8f6f4 v[38:41], v[18:25], v[230:237], 0
	v_mfma_f32_16x16x128_f8f6f4 v[34:37], v[26:33], v[230:237], 0
	s_nop 1
	v_mfma_f32_16x16x128_f8f6f4 v[90:93], v[2:9], v[204:211], 0
	v_mfma_f32_16x16x128_f8f6f4 v[82:85], v[10:17], v[204:211], 0
	v_mfma_f32_16x16x128_f8f6f4 v[74:77], v[2:9], v[212:219], 0
	v_mfma_f32_16x16x128_f8f6f4 v[58:61], v[10:17], v[212:219], 0
	v_mfma_f32_16x16x128_f8f6f4 v[70:73], v[2:9], v[220:227], 0
	v_mfma_f32_16x16x128_f8f6f4 v[62:65], v[10:17], v[220:227], 0
	v_mfma_f32_16x16x128_f8f6f4 v[50:53], v[2:9], v[230:237], 0
	v_mfma_f32_16x16x128_f8f6f4 v[42:45], v[10:17], v[230:237], 0
	s_setprio 0
	s_barrier
	v_add_u32_e32 v14, s86, v193
	v_add_u32_e32 v30, s87, v193
	ds_read_b128 v[2:5], v14
	ds_read_b128 v[6:9], v14 offset:1024
	ds_read_b128 v[10:13], v14 offset:2048
	ds_read_b128 v[14:17], v14 offset:3072
	ds_read_b128 v[18:21], v30
	ds_read_b128 v[22:25], v30 offset:1024
	ds_read_b128 v[26:29], v30 offset:2048
	ds_read_b128 v[30:33], v30 offset:3072
	s_mov_b32 m0, s41
	ds_read_b128 v[204:207], v197 offset:32768
	ds_read_b128 v[208:211], v197 offset:33792
	ds_read_b128 v[212:215], v197 offset:34816
	ds_read_b128 v[216:219], v197 offset:35840
	ds_read_b128 v[220:223], v197 offset:36864
	ds_read_b128 v[224:227], v197 offset:37888
	ds_read_b128 v[230:233], v197 offset:38912
	ds_read_b128 v[234:237], v197 offset:39936
	global_load_lds_dwordx4 v229, s[34:35]
	s_mov_b32 m0, s42
	s_nop 0
	global_load_lds_dwordx4 v240, s[34:35]
	s_waitcnt vmcnt(8)
	s_waitcnt lgkmcnt(0)
	s_barrier
	s_setprio 1
	s_waitcnt lgkmcnt(0)
	s_nop 1
	v_mfma_f32_16x16x128_f8f6f4 v[158:161], v[2:9], v[204:211], v[158:161]
	v_mfma_f32_16x16x128_f8f6f4 v[150:153], v[10:17], v[204:211], v[150:153]
	v_mfma_f32_16x16x128_f8f6f4 v[142:145], v[2:9], v[212:219], v[142:145]
	v_mfma_f32_16x16x128_f8f6f4 v[134:137], v[10:17], v[212:219], v[134:137]
	v_mfma_f32_16x16x128_f8f6f4 v[126:129], v[2:9], v[220:227], v[126:129]
	v_mfma_f32_16x16x128_f8f6f4 v[118:121], v[10:17], v[220:227], v[118:121]
	v_mfma_f32_16x16x128_f8f6f4 v[110:113], v[2:9], v[230:237], v[110:113]
	v_mfma_f32_16x16x128_f8f6f4 v[102:105], v[10:17], v[230:237], v[102:105]
	s_nop 1
	v_mfma_f32_16x16x128_f8f6f4 v[154:157], v[18:25], v[204:211], v[154:157]
	v_mfma_f32_16x16x128_f8f6f4 v[146:149], v[26:33], v[204:211], v[146:149]
	v_mfma_f32_16x16x128_f8f6f4 v[138:141], v[18:25], v[212:219], v[138:141]
	v_mfma_f32_16x16x128_f8f6f4 v[130:133], v[26:33], v[212:219], v[130:133]
	v_mfma_f32_16x16x128_f8f6f4 v[122:125], v[18:25], v[220:227], v[122:125]
	v_mfma_f32_16x16x128_f8f6f4 v[114:117], v[26:33], v[220:227], v[114:117]
	v_mfma_f32_16x16x128_f8f6f4 v[106:109], v[18:25], v[230:237], v[106:109]
	v_mfma_f32_16x16x128_f8f6f4 v[98:101], v[26:33], v[230:237], v[98:101]
	s_setprio 0
	s_barrier
	s_add_i32 s34, s86, s38
	v_lshl_add_u64 v[182:183], v[182:183], 0, s[8:9]
	s_mov_b32 m0, s34
	ds_read_b128 v[204:207], v197 offset:49152
	ds_read_b128 v[208:211], v197 offset:50176
	ds_read_b128 v[212:215], v197 offset:51200
	ds_read_b128 v[216:219], v197 offset:52224
	ds_read_b128 v[220:223], v197 offset:53248
	ds_read_b128 v[224:227], v197 offset:54272
	ds_read_b128 v[230:233], v197 offset:55296
	ds_read_b128 v[234:237], v197 offset:56320
	global_load_lds_dwordx4 v[182:183], off
	s_add_i32 m0, s34, 0x2000
	s_add_u32 s30, s30, 0x40080
	v_lshl_add_u64 v[182:183], v[184:185], 0, s[8:9]
	s_addc_u32 s31, s31, 0
	s_add_i32 s34, s87, s38
	global_load_lds_dwordx4 v[182:183], off
	v_lshl_add_u64 v[182:183], s[30:31], 0, v[164:165]
	s_mov_b32 m0, s34
	s_nop 0
	global_load_lds_dwordx4 v[182:183], off
	v_lshl_add_u64 v[182:183], s[30:31], 0, v[162:163]
	s_add_i32 m0, s34, 0x2000
	s_nop 0
	global_load_lds_dwordx4 v[182:183], off
	v_lshl_add_u64 v[182:183], v[188:189], 0, s[8:9]
	s_mov_b32 m0, s43
	s_nop 0
	global_load_lds_dwordx4 v[182:183], off
	v_lshl_add_u64 v[182:183], v[186:187], 0, s[8:9]
	s_mov_b32 m0, s44
	s_nop 0
	global_load_lds_dwordx4 v[182:183], off
	s_waitcnt vmcnt(8)
	s_waitcnt lgkmcnt(0)
	s_barrier
	s_setprio 1
	s_waitcnt lgkmcnt(0)
	s_nop 1
	v_mfma_f32_16x16x128_f8f6f4 v[94:97], v[2:9], v[204:211], v[94:97]
	v_mfma_f32_16x16x128_f8f6f4 v[86:89], v[10:17], v[204:211], v[86:89]
	v_mfma_f32_16x16x128_f8f6f4 v[78:81], v[2:9], v[212:219], v[78:81]
	v_mfma_f32_16x16x128_f8f6f4 v[66:69], v[10:17], v[212:219], v[66:69]
	v_mfma_f32_16x16x128_f8f6f4 v[54:57], v[2:9], v[220:227], v[54:57]
	v_mfma_f32_16x16x128_f8f6f4 v[46:49], v[10:17], v[220:227], v[46:49]
	v_mfma_f32_16x16x128_f8f6f4 v[38:41], v[2:9], v[230:237], v[38:41]
	v_mfma_f32_16x16x128_f8f6f4 v[34:37], v[10:17], v[230:237], v[34:37]
	s_nop 1
	v_mfma_f32_16x16x128_f8f6f4 v[90:93], v[18:25], v[204:211], v[90:93]
	v_mfma_f32_16x16x128_f8f6f4 v[82:85], v[26:33], v[204:211], v[82:85]
	v_mfma_f32_16x16x128_f8f6f4 v[74:77], v[18:25], v[212:219], v[74:77]
	v_mfma_f32_16x16x128_f8f6f4 v[58:61], v[26:33], v[212:219], v[58:61]
	v_mfma_f32_16x16x128_f8f6f4 v[70:73], v[18:25], v[220:227], v[70:73]
	v_mfma_f32_16x16x128_f8f6f4 v[62:65], v[26:33], v[220:227], v[62:65]
	v_mfma_f32_16x16x128_f8f6f4 v[50:53], v[18:25], v[230:237], v[50:53]
	v_mfma_f32_16x16x128_f8f6f4 v[42:45], v[26:33], v[230:237], v[42:45]
	s_setprio 0
	s_barrier
	s_add_i32 s58, s58, 2
	s_add_u32 s26, s26, 0x100
	s_addc_u32 s27, s27, 0
	s_cmp_gt_u32 s58, 13
	s_cbranch_scc1 .LBB0_1350
	s_branch .LBB0_1348
.LBB0_1347:
	s_add_u32 s30, s84, s26
	s_addc_u32 s31, s85, s27
	v_add_u32_e32 v2, s3, v193
	v_add_u32_e32 v14, s2, v193
	s_add_u32 s34, s30, 0x35400100
	ds_read_b128 v[18:21], v2
	ds_read_b128 v[22:25], v2 offset:1024
	ds_read_b128 v[26:29], v2 offset:2048
	ds_read_b128 v[30:33], v2 offset:3072
	ds_read_b128 v[2:5], v14
	ds_read_b128 v[6:9], v14 offset:1024
	ds_read_b128 v[10:13], v14 offset:2048
	ds_read_b128 v[14:17], v14 offset:3072
	s_addc_u32 s35, s31, 0
	s_add_u32 s59, s56, s26
	s_addc_u32 s60, s57, s27
	s_cmpk_eq_i32 s26, 0x700
	s_cselect_b64 vcc, -1, 0
	s_and_b64 s[30:31], vcc, exec
	v_cndmask_b32_e32 v166, v199, v169, vcc
	s_cselect_b32 s35, s5, s35
	s_cselect_b32 s34, s4, s34
	v_cndmask_b32_e32 v238, v176, v171, vcc
	v_cndmask_b32_e32 v229, v174, v173, vcc
	v_cndmask_b32_e32 v240, v172, v175, vcc
	s_cselect_b32 s31, s21, s60
	s_cselect_b32 s30, s20, s59
	v_lshl_add_u64 v[230:231], v[180:181], 0, s[26:27]
	s_add_i32 m0, s39, 0xc000
	ds_read_b128 v[182:185], v197
	ds_read_b128 v[186:189], v197 offset:1024
	ds_read_b128 v[204:207], v197 offset:2048
	ds_read_b128 v[208:211], v197 offset:3072
	ds_read_b128 v[212:215], v197 offset:4096
	ds_read_b128 v[216:219], v197 offset:5120
	ds_read_b128 v[220:223], v197 offset:6144
	ds_read_b128 v[224:227], v197 offset:7168
	global_load_lds_dwordx4 v[230:231], off
	v_lshl_add_u64 v[230:231], v[178:179], 0, s[26:27]
	s_add_i32 m0, s39, 0xe000
	s_nop 0
	global_load_lds_dwordx4 v[230:231], off
	s_waitcnt vmcnt(8)
	s_waitcnt lgkmcnt(0)
	s_barrier
	s_setprio 1
	s_waitcnt lgkmcnt(0)
	s_nop 1
	v_mfma_f32_16x16x128_f8f6f4 v[158:161], v[18:25], v[182:189], v[158:161]
	v_mfma_f32_16x16x128_f8f6f4 v[150:153], v[26:33], v[182:189], v[150:153]
	v_mfma_f32_16x16x128_f8f6f4 v[142:145], v[18:25], v[204:211], v[142:145]
	v_mfma_f32_16x16x128_f8f6f4 v[134:137], v[26:33], v[204:211], v[134:137]
	v_mfma_f32_16x16x128_f8f6f4 v[126:129], v[18:25], v[212:219], v[126:129]
	v_mfma_f32_16x16x128_f8f6f4 v[118:121], v[26:33], v[212:219], v[118:121]
	v_mfma_f32_16x16x128_f8f6f4 v[110:113], v[18:25], v[220:227], v[110:113]
	v_mfma_f32_16x16x128_f8f6f4 v[102:105], v[26:33], v[220:227], v[102:105]
	s_nop 1
	v_mfma_f32_16x16x128_f8f6f4 v[154:157], v[2:9], v[182:189], v[154:157]
	v_mfma_f32_16x16x128_f8f6f4 v[146:149], v[10:17], v[182:189], v[146:149]
	v_mfma_f32_16x16x128_f8f6f4 v[138:141], v[2:9], v[204:211], v[138:141]
	v_mfma_f32_16x16x128_f8f6f4 v[130:133], v[10:17], v[204:211], v[130:133]
	v_mfma_f32_16x16x128_f8f6f4 v[122:125], v[2:9], v[212:219], v[122:125]
	v_mfma_f32_16x16x128_f8f6f4 v[114:117], v[10:17], v[212:219], v[114:117]
	v_mfma_f32_16x16x128_f8f6f4 v[106:109], v[2:9], v[220:227], v[106:109]
	v_mfma_f32_16x16x128_f8f6f4 v[98:101], v[10:17], v[220:227], v[98:101]
	s_setprio 0
	s_barrier
	s_add_i32 s59, s3, s38
	v_lshl_add_u64 v[182:183], s[30:31], 0, v[164:165]
	s_mov_b32 m0, s59
	ds_read_b128 v[204:207], v197 offset:16384
	ds_read_b128 v[208:211], v197 offset:17408
	ds_read_b128 v[212:215], v197 offset:18432
	ds_read_b128 v[216:219], v197 offset:19456
	ds_read_b128 v[220:223], v197 offset:20480
	ds_read_b128 v[224:227], v197 offset:21504
	ds_read_b128 v[230:233], v197 offset:22528
	ds_read_b128 v[234:237], v197 offset:23552
	global_load_lds_dwordx4 v[182:183], off
	s_add_i32 m0, s59, 0x2000
	s_add_u32 s60, s30, 0x40000
	v_lshl_add_u64 v[184:185], s[30:31], 0, v[162:163]
	s_addc_u32 s61, s31, 0
	s_add_i32 s59, s2, s38
	global_load_lds_dwordx4 v[184:185], off
	v_lshl_add_u64 v[186:187], s[60:61], 0, v[164:165]
	s_mov_b32 m0, s59
	v_mov_b32_e32 v239, v167
	global_load_lds_dwordx4 v[186:187], off
	v_lshl_add_u64 v[186:187], s[60:61], 0, v[162:163]
	s_add_i32 m0, s59, 0x2000
	v_lshl_add_u64 v[188:189], s[34:35], 0, v[166:167]
	global_load_lds_dwordx4 v[186:187], off
	s_mov_b32 m0, s39
	v_lshl_add_u64 v[186:187], s[34:35], 0, v[238:239]
	global_load_lds_dwordx4 v166, s[34:35]
	s_mov_b32 m0, s40
	s_nop 0
	global_load_lds_dwordx4 v238, s[34:35]
	s_waitcnt vmcnt(8)
	s_waitcnt lgkmcnt(0)
	s_barrier
	s_setprio 1
	s_waitcnt lgkmcnt(0)
	s_nop 1
	v_mfma_f32_16x16x128_f8f6f4 v[94:97], v[18:25], v[204:211], v[94:97]
	v_mfma_f32_16x16x128_f8f6f4 v[86:89], v[26:33], v[204:211], v[86:89]
	v_mfma_f32_16x16x128_f8f6f4 v[78:81], v[18:25], v[212:219], v[78:81]
	v_mfma_f32_16x16x128_f8f6f4 v[66:69], v[26:33], v[212:219], v[66:69]
	v_mfma_f32_16x16x128_f8f6f4 v[54:57], v[18:25], v[220:227], v[54:57]
	v_mfma_f32_16x16x128_f8f6f4 v[46:49], v[26:33], v[220:227], v[46:49]
	v_mfma_f32_16x16x128_f8f6f4 v[38:41], v[18:25], v[230:237], v[38:41]
	v_mfma_f32_16x16x128_f8f6f4 v[34:37], v[26:33], v[230:237], v[34:37]
	s_nop 1
	v_mfma_f32_16x16x128_f8f6f4 v[90:93], v[2:9], v[204:211], v[90:93]
	v_mfma_f32_16x16x128_f8f6f4 v[82:85], v[10:17], v[204:211], v[82:85]
	v_mfma_f32_16x16x128_f8f6f4 v[74:77], v[2:9], v[212:219], v[74:77]
	v_mfma_f32_16x16x128_f8f6f4 v[58:61], v[10:17], v[212:219], v[58:61]
	v_mfma_f32_16x16x128_f8f6f4 v[70:73], v[2:9], v[220:227], v[70:73]
	v_mfma_f32_16x16x128_f8f6f4 v[62:65], v[10:17], v[220:227], v[62:65]
	v_mfma_f32_16x16x128_f8f6f4 v[50:53], v[2:9], v[230:237], v[50:53]
	v_mfma_f32_16x16x128_f8f6f4 v[42:45], v[10:17], v[230:237], v[42:45]
	s_setprio 0
	s_barrier
	v_add_u32_e32 v14, s86, v193
	v_add_u32_e32 v30, s87, v193
	ds_read_b128 v[2:5], v14
	ds_read_b128 v[6:9], v14 offset:1024
	ds_read_b128 v[10:13], v14 offset:2048
	ds_read_b128 v[14:17], v14 offset:3072
	ds_read_b128 v[18:21], v30
	ds_read_b128 v[22:25], v30 offset:1024
	ds_read_b128 v[26:29], v30 offset:2048
	ds_read_b128 v[30:33], v30 offset:3072
	s_mov_b32 m0, s41
	ds_read_b128 v[204:207], v197 offset:32768
	ds_read_b128 v[208:211], v197 offset:33792
	ds_read_b128 v[212:215], v197 offset:34816
	ds_read_b128 v[216:219], v197 offset:35840
	ds_read_b128 v[220:223], v197 offset:36864
	ds_read_b128 v[224:227], v197 offset:37888
	ds_read_b128 v[230:233], v197 offset:38912
	ds_read_b128 v[234:237], v197 offset:39936
	global_load_lds_dwordx4 v229, s[34:35]
	s_mov_b32 m0, s42
	s_nop 0
	global_load_lds_dwordx4 v240, s[34:35]
	s_waitcnt vmcnt(8)
	s_waitcnt lgkmcnt(0)
	s_barrier
	s_setprio 1
	s_waitcnt lgkmcnt(0)
	s_nop 1
	v_mfma_f32_16x16x128_f8f6f4 v[158:161], v[2:9], v[204:211], v[158:161]
	v_mfma_f32_16x16x128_f8f6f4 v[150:153], v[10:17], v[204:211], v[150:153]
	v_mfma_f32_16x16x128_f8f6f4 v[142:145], v[2:9], v[212:219], v[142:145]
	v_mfma_f32_16x16x128_f8f6f4 v[134:137], v[10:17], v[212:219], v[134:137]
	v_mfma_f32_16x16x128_f8f6f4 v[126:129], v[2:9], v[220:227], v[126:129]
	v_mfma_f32_16x16x128_f8f6f4 v[118:121], v[10:17], v[220:227], v[118:121]
	v_mfma_f32_16x16x128_f8f6f4 v[110:113], v[2:9], v[230:237], v[110:113]
	v_mfma_f32_16x16x128_f8f6f4 v[102:105], v[10:17], v[230:237], v[102:105]
	s_nop 1
	v_mfma_f32_16x16x128_f8f6f4 v[154:157], v[18:25], v[204:211], v[154:157]
	v_mfma_f32_16x16x128_f8f6f4 v[146:149], v[26:33], v[204:211], v[146:149]
	v_mfma_f32_16x16x128_f8f6f4 v[138:141], v[18:25], v[212:219], v[138:141]
	v_mfma_f32_16x16x128_f8f6f4 v[130:133], v[26:33], v[212:219], v[130:133]
	v_mfma_f32_16x16x128_f8f6f4 v[122:125], v[18:25], v[220:227], v[122:125]
	v_mfma_f32_16x16x128_f8f6f4 v[114:117], v[26:33], v[220:227], v[114:117]
	v_mfma_f32_16x16x128_f8f6f4 v[106:109], v[18:25], v[230:237], v[106:109]
	v_mfma_f32_16x16x128_f8f6f4 v[98:101], v[26:33], v[230:237], v[98:101]
	s_setprio 0
	s_barrier
	s_add_i32 s34, s86, s38
	v_lshl_add_u64 v[182:183], v[182:183], 0, s[8:9]
	s_mov_b32 m0, s34
	ds_read_b128 v[204:207], v197 offset:49152
	ds_read_b128 v[208:211], v197 offset:50176
	ds_read_b128 v[212:215], v197 offset:51200
	ds_read_b128 v[216:219], v197 offset:52224
	ds_read_b128 v[220:223], v197 offset:53248
	ds_read_b128 v[224:227], v197 offset:54272
	ds_read_b128 v[230:233], v197 offset:55296
	ds_read_b128 v[234:237], v197 offset:56320
	global_load_lds_dwordx4 v[182:183], off
	s_add_i32 m0, s34, 0x2000
	s_add_u32 s30, s30, 0x40080
	v_lshl_add_u64 v[182:183], v[184:185], 0, s[8:9]
	s_addc_u32 s31, s31, 0
	s_add_i32 s34, s87, s38
	global_load_lds_dwordx4 v[182:183], off
	v_lshl_add_u64 v[182:183], s[30:31], 0, v[164:165]
	s_mov_b32 m0, s34
	s_nop 0
	global_load_lds_dwordx4 v[182:183], off
	v_lshl_add_u64 v[182:183], s[30:31], 0, v[162:163]
	s_add_i32 m0, s34, 0x2000
	s_nop 0
	global_load_lds_dwordx4 v[182:183], off
	v_lshl_add_u64 v[182:183], v[188:189], 0, s[8:9]
	s_mov_b32 m0, s43
	s_nop 0
	global_load_lds_dwordx4 v[182:183], off
	v_lshl_add_u64 v[182:183], v[186:187], 0, s[8:9]
	s_mov_b32 m0, s44
	s_nop 0
	global_load_lds_dwordx4 v[182:183], off
	s_waitcnt vmcnt(8)
	s_waitcnt lgkmcnt(0)
	s_barrier
	s_setprio 1
	s_waitcnt lgkmcnt(0)
	s_nop 1
	v_mfma_f32_16x16x128_f8f6f4 v[94:97], v[2:9], v[204:211], v[94:97]
	v_mfma_f32_16x16x128_f8f6f4 v[86:89], v[10:17], v[204:211], v[86:89]
	v_mfma_f32_16x16x128_f8f6f4 v[78:81], v[2:9], v[212:219], v[78:81]
	v_mfma_f32_16x16x128_f8f6f4 v[66:69], v[10:17], v[212:219], v[66:69]
	v_mfma_f32_16x16x128_f8f6f4 v[54:57], v[2:9], v[220:227], v[54:57]
	v_mfma_f32_16x16x128_f8f6f4 v[46:49], v[10:17], v[220:227], v[46:49]
	v_mfma_f32_16x16x128_f8f6f4 v[38:41], v[2:9], v[230:237], v[38:41]
	v_mfma_f32_16x16x128_f8f6f4 v[34:37], v[10:17], v[230:237], v[34:37]
	s_nop 1
	v_mfma_f32_16x16x128_f8f6f4 v[90:93], v[18:25], v[204:211], v[90:93]
	v_mfma_f32_16x16x128_f8f6f4 v[82:85], v[26:33], v[204:211], v[82:85]
	v_mfma_f32_16x16x128_f8f6f4 v[74:77], v[18:25], v[212:219], v[74:77]
	v_mfma_f32_16x16x128_f8f6f4 v[58:61], v[26:33], v[212:219], v[58:61]
	v_mfma_f32_16x16x128_f8f6f4 v[70:73], v[18:25], v[220:227], v[70:73]
	v_mfma_f32_16x16x128_f8f6f4 v[62:65], v[26:33], v[220:227], v[62:65]
	v_mfma_f32_16x16x128_f8f6f4 v[50:53], v[18:25], v[230:237], v[50:53]
	v_mfma_f32_16x16x128_f8f6f4 v[42:45], v[26:33], v[230:237], v[42:45]
	s_setprio 0
	s_barrier
	s_add_i32 s58, s58, 2
	s_add_u32 s26, s26, 0x100
	s_addc_u32 s27, s27, 0
	s_cmp_gt_u32 s58, 13
	s_cbranch_scc1 .LBB0_1350

.LBB0_1418:
	s_add_u32 s26, s26, 0x80
	s_addc_u32 s27, s27, 0
	s_add_u32 s34, s30, 0x100
	s_addc_u32 s35, s31, 0
	s_mov_b32 s50, -2
	ds_read_b128 v[18:21], v192
	ds_read_b128 v[22:25], v192 offset:1024
	ds_read_b128 v[26:29], v192 offset:2048
	ds_read_b128 v[30:33], v192 offset:3072
	ds_read_b128 v[2:5], v193
	ds_read_b128 v[6:9], v193 offset:1024
	ds_read_b128 v[10:13], v193 offset:2048
	ds_read_b128 v[14:17], v193 offset:3072
	s_add_u32 s28, s26, 0x80
	s_addc_u32 s29, s27, 0
	s_cmp_eq_u32 s50, 12
	s_cselect_b32 s31, s19, s29
	s_cselect_b32 s30, s18, s28
	s_cselect_b32 s29, s21, s35
	s_cselect_b32 s28, s20, s34
	v_lshl_add_u64 v[220:221], s[26:27], 0, v[178:179]
	s_add_i32 m0, s38, 0xc000
	ds_read_b128 v[180:183], v194
	ds_read_b128 v[184:187], v194 offset:1024
	ds_read_b128 v[196:199], v194 offset:2048
	ds_read_b128 v[200:203], v194 offset:3072
	ds_read_b128 v[204:207], v194 offset:4096
	ds_read_b128 v[208:211], v194 offset:5120
	ds_read_b128 v[212:215], v194 offset:6144
	ds_read_b128 v[216:219], v194 offset:7168
	global_load_lds_dwordx4 v[220:221], off
	v_lshl_add_u64 v[220:221], s[26:27], 0, v[176:177]
	s_add_i32 m0, s38, 0xe000
	s_nop 0
	global_load_lds_dwordx4 v[220:221], off
	s_waitcnt vmcnt(8)
	s_waitcnt lgkmcnt(0)
	s_barrier
	s_setprio 1
	s_waitcnt lgkmcnt(0)
	s_nop 1
	v_mfma_f32_16x16x128_f8f6f4 v[158:161], v[18:25], v[180:187], 0
	v_mfma_f32_16x16x128_f8f6f4 v[154:157], v[26:33], v[180:187], 0
	v_mfma_f32_16x16x128_f8f6f4 v[142:145], v[18:25], v[196:203], 0
	v_mfma_f32_16x16x128_f8f6f4 v[138:141], v[26:33], v[196:203], 0
	v_mfma_f32_16x16x128_f8f6f4 v[126:129], v[18:25], v[204:211], 0
	v_mfma_f32_16x16x128_f8f6f4 v[122:125], v[26:33], v[204:211], 0
	v_mfma_f32_16x16x128_f8f6f4 v[110:113], v[18:25], v[212:219], 0
	v_mfma_f32_16x16x128_f8f6f4 v[106:109], v[26:33], v[212:219], 0
	s_nop 1
	v_mfma_f32_16x16x128_f8f6f4 v[150:153], v[2:9], v[180:187], 0
	v_mfma_f32_16x16x128_f8f6f4 v[146:149], v[10:17], v[180:187], 0
	v_mfma_f32_16x16x128_f8f6f4 v[134:137], v[2:9], v[196:203], 0
	v_mfma_f32_16x16x128_f8f6f4 v[130:133], v[10:17], v[196:203], 0
	v_mfma_f32_16x16x128_f8f6f4 v[118:121], v[2:9], v[204:211], 0
	v_mfma_f32_16x16x128_f8f6f4 v[114:117], v[10:17], v[204:211], 0
	v_mfma_f32_16x16x128_f8f6f4 v[94:97], v[2:9], v[212:219], 0
	v_mfma_f32_16x16x128_f8f6f4 v[90:93], v[10:17], v[212:219], 0
	s_setprio 0
	s_barrier
	s_add_i32 s51, s3, s37
	v_lshl_add_u64 v[180:181], s[28:29], 0, v[164:165]
	s_mov_b32 m0, s51
	ds_read_b128 v[196:199], v194 offset:16384
	ds_read_b128 v[200:203], v194 offset:17408
	ds_read_b128 v[204:207], v194 offset:18432
	ds_read_b128 v[208:211], v194 offset:19456
	ds_read_b128 v[212:215], v194 offset:20480
	ds_read_b128 v[216:219], v194 offset:21504
	ds_read_b128 v[220:223], v194 offset:22528
	ds_read_b128 v[224:227], v194 offset:23552
	global_load_lds_dwordx4 v[180:181], off
	s_add_i32 m0, s51, 0x2000
	s_add_u32 s52, s28, 0x40000
	v_lshl_add_u64 v[182:183], s[28:29], 0, v[162:163]
	s_addc_u32 s53, s29, 0
	s_add_i32 s51, s2, s37
	global_load_lds_dwordx4 v[182:183], off
	v_lshl_add_u64 v[184:185], s[52:53], 0, v[164:165]
	s_mov_b32 m0, s51
	v_lshl_add_u64 v[186:187], s[30:31], 0, v[168:169]
	global_load_lds_dwordx4 v[184:185], off
	v_lshl_add_u64 v[184:185], s[52:53], 0, v[162:163]
	s_add_i32 m0, s51, 0x2000
	s_nop 0
	global_load_lds_dwordx4 v[184:185], off
	v_lshl_add_u64 v[184:185], s[30:31], 0, v[166:167]
	s_mov_b32 m0, s38
	s_nop 0
	global_load_lds_dwordx4 v[184:185], off
	s_mov_b32 m0, s39
	s_nop 0
	global_load_lds_dwordx4 v[186:187], off
	s_waitcnt vmcnt(8)
	s_waitcnt lgkmcnt(0)
	s_barrier
	s_setprio 1
	s_waitcnt lgkmcnt(0)
	s_nop 1
	v_mfma_f32_16x16x128_f8f6f4 v[78:81], v[18:25], v[196:203], 0
	v_mfma_f32_16x16x128_f8f6f4 v[74:77], v[26:33], v[196:203], 0
	v_mfma_f32_16x16x128_f8f6f4 v[62:65], v[18:25], v[204:211], 0
	v_mfma_f32_16x16x128_f8f6f4 v[58:61], v[26:33], v[204:211], 0
	v_mfma_f32_16x16x128_f8f6f4 v[46:49], v[18:25], v[212:219], 0
	v_mfma_f32_16x16x128_f8f6f4 v[42:45], v[26:33], v[212:219], 0
	v_mfma_f32_16x16x128_f8f6f4 v[38:41], v[18:25], v[220:227], 0
	v_mfma_f32_16x16x128_f8f6f4 v[34:37], v[26:33], v[220:227], 0
	s_nop 1
	v_mfma_f32_16x16x128_f8f6f4 v[98:101], v[2:9], v[196:203], 0
	v_mfma_f32_16x16x128_f8f6f4 v[102:105], v[10:17], v[196:203], 0
	v_mfma_f32_16x16x128_f8f6f4 v[82:85], v[2:9], v[204:211], 0
	v_mfma_f32_16x16x128_f8f6f4 v[86:89], v[10:17], v[204:211], 0
	v_mfma_f32_16x16x128_f8f6f4 v[66:69], v[2:9], v[212:219], 0
	v_mfma_f32_16x16x128_f8f6f4 v[70:73], v[10:17], v[212:219], 0
	v_mfma_f32_16x16x128_f8f6f4 v[50:53], v[2:9], v[220:227], 0
	v_mfma_f32_16x16x128_f8f6f4 v[54:57], v[10:17], v[220:227], 0
	s_setprio 0
	s_barrier
	v_add_u32_e32 v14, s86, v188
	v_add_u32_e32 v30, s87, v188
	ds_read_b128 v[2:5], v14
	ds_read_b128 v[6:9], v14 offset:1024
	ds_read_b128 v[10:13], v14 offset:2048
	ds_read_b128 v[14:17], v14 offset:3072
	ds_read_b128 v[18:21], v30
	ds_read_b128 v[22:25], v30 offset:1024
	ds_read_b128 v[26:29], v30 offset:2048
	ds_read_b128 v[30:33], v30 offset:3072
	s_mov_b32 m0, s40
	v_lshl_add_u64 v[230:231], s[30:31], 0, v[170:171]
	ds_read_b128 v[196:199], v194 offset:32768
	ds_read_b128 v[200:203], v194 offset:33792
	ds_read_b128 v[204:207], v194 offset:34816
	ds_read_b128 v[208:211], v194 offset:35840
	ds_read_b128 v[212:215], v194 offset:36864
	ds_read_b128 v[216:219], v194 offset:37888
	ds_read_b128 v[220:223], v194 offset:38912
	ds_read_b128 v[224:227], v194 offset:39936
	global_load_lds_dwordx4 v[230:231], off
	v_lshl_add_u64 v[230:231], s[30:31], 0, v[172:173]
	s_mov_b32 m0, s41
	s_nop 0
	global_load_lds_dwordx4 v[230:231], off
	s_waitcnt vmcnt(8)
	s_waitcnt lgkmcnt(0)
	s_barrier
	s_setprio 1
	s_waitcnt lgkmcnt(0)
	s_nop 1
	v_mfma_f32_16x16x128_f8f6f4 v[158:161], v[2:9], v[196:203], v[158:161]
	v_mfma_f32_16x16x128_f8f6f4 v[154:157], v[10:17], v[196:203], v[154:157]
	v_mfma_f32_16x16x128_f8f6f4 v[142:145], v[2:9], v[204:211], v[142:145]
	v_mfma_f32_16x16x128_f8f6f4 v[138:141], v[10:17], v[204:211], v[138:141]
	v_mfma_f32_16x16x128_f8f6f4 v[126:129], v[2:9], v[212:219], v[126:129]
	v_mfma_f32_16x16x128_f8f6f4 v[122:125], v[10:17], v[212:219], v[122:125]
	v_mfma_f32_16x16x128_f8f6f4 v[110:113], v[2:9], v[220:227], v[110:113]
	v_mfma_f32_16x16x128_f8f6f4 v[106:109], v[10:17], v[220:227], v[106:109]
	s_nop 1
	v_mfma_f32_16x16x128_f8f6f4 v[150:153], v[18:25], v[196:203], v[150:153]
	v_mfma_f32_16x16x128_f8f6f4 v[146:149], v[26:33], v[196:203], v[146:149]
	v_mfma_f32_16x16x128_f8f6f4 v[134:137], v[18:25], v[204:211], v[134:137]
	v_mfma_f32_16x16x128_f8f6f4 v[130:133], v[26:33], v[204:211], v[130:133]
	v_mfma_f32_16x16x128_f8f6f4 v[118:121], v[18:25], v[212:219], v[118:121]
	v_mfma_f32_16x16x128_f8f6f4 v[114:117], v[26:33], v[212:219], v[114:117]
	v_mfma_f32_16x16x128_f8f6f4 v[94:97], v[18:25], v[220:227], v[94:97]
	v_mfma_f32_16x16x128_f8f6f4 v[90:93], v[26:33], v[220:227], v[90:93]
	s_setprio 0
	s_barrier
	s_add_i32 s30, s86, s37
	v_lshl_add_u64 v[180:181], v[180:181], 0, s[8:9]
	s_mov_b32 m0, s30
	ds_read_b128 v[196:199], v194 offset:49152
	ds_read_b128 v[200:203], v194 offset:50176
	ds_read_b128 v[204:207], v194 offset:51200
	ds_read_b128 v[208:211], v194 offset:52224
	ds_read_b128 v[212:215], v194 offset:53248
	ds_read_b128 v[216:219], v194 offset:54272
	ds_read_b128 v[220:223], v194 offset:55296
	ds_read_b128 v[224:227], v194 offset:56320
	global_load_lds_dwordx4 v[180:181], off
	s_add_i32 m0, s30, 0x2000
	s_add_u32 s28, s28, 0x40080
	v_lshl_add_u64 v[180:181], v[182:183], 0, s[8:9]
	s_addc_u32 s29, s29, 0
	s_add_i32 s30, s87, s37
	global_load_lds_dwordx4 v[180:181], off
	v_lshl_add_u64 v[180:181], s[28:29], 0, v[164:165]
	s_mov_b32 m0, s30
	s_nop 0
	global_load_lds_dwordx4 v[180:181], off
	v_lshl_add_u64 v[180:181], s[28:29], 0, v[162:163]
	s_add_i32 m0, s30, 0x2000
	s_nop 0
	global_load_lds_dwordx4 v[180:181], off
	v_lshl_add_u64 v[180:181], v[184:185], 0, s[8:9]
	s_mov_b32 m0, s43
	s_nop 0
	global_load_lds_dwordx4 v[180:181], off
	v_lshl_add_u64 v[180:181], v[186:187], 0, s[8:9]
	s_mov_b32 m0, s44
	s_nop 0
	global_load_lds_dwordx4 v[180:181], off
	s_waitcnt vmcnt(8)
	s_waitcnt lgkmcnt(0)
	s_barrier
	s_setprio 1
	s_waitcnt lgkmcnt(0)
	s_nop 1
	v_mfma_f32_16x16x128_f8f6f4 v[78:81], v[2:9], v[196:203], v[78:81]
	v_mfma_f32_16x16x128_f8f6f4 v[74:77], v[10:17], v[196:203], v[74:77]
	v_mfma_f32_16x16x128_f8f6f4 v[62:65], v[2:9], v[204:211], v[62:65]
	v_mfma_f32_16x16x128_f8f6f4 v[58:61], v[10:17], v[204:211], v[58:61]
	v_mfma_f32_16x16x128_f8f6f4 v[46:49], v[2:9], v[212:219], v[46:49]
	v_mfma_f32_16x16x128_f8f6f4 v[42:45], v[10:17], v[212:219], v[42:45]
	v_mfma_f32_16x16x128_f8f6f4 v[38:41], v[2:9], v[220:227], v[38:41]
	v_mfma_f32_16x16x128_f8f6f4 v[34:37], v[10:17], v[220:227], v[34:37]
	s_nop 1
	v_mfma_f32_16x16x128_f8f6f4 v[98:101], v[18:25], v[196:203], v[98:101]
	v_mfma_f32_16x16x128_f8f6f4 v[102:105], v[26:33], v[196:203], v[102:105]
	v_mfma_f32_16x16x128_f8f6f4 v[82:85], v[18:25], v[204:211], v[82:85]
	v_mfma_f32_16x16x128_f8f6f4 v[86:89], v[26:33], v[204:211], v[86:89]
	v_mfma_f32_16x16x128_f8f6f4 v[66:69], v[18:25], v[212:219], v[66:69]
	v_mfma_f32_16x16x128_f8f6f4 v[70:73], v[26:33], v[212:219], v[70:73]
	v_mfma_f32_16x16x128_f8f6f4 v[50:53], v[18:25], v[220:227], v[50:53]
	v_mfma_f32_16x16x128_f8f6f4 v[54:57], v[26:33], v[220:227], v[54:57]
	s_setprio 0
	s_barrier
	s_add_i32 s50, s50, 2
	s_add_u32 s26, s26, 0x100
	s_addc_u32 s27, s27, 0
	s_add_u32 s34, s34, 0x100
	s_addc_u32 s35, s35, 0
	s_cmp_gt_u32 s50, 13
	s_cbranch_scc0 .LBB0_1419
	s_branch .Lmy_pexit_p9
.LBB0_1419:
	ds_read_b128 v[18:21], v192
	ds_read_b128 v[22:25], v192 offset:1024
	ds_read_b128 v[26:29], v192 offset:2048
	ds_read_b128 v[30:33], v192 offset:3072
	ds_read_b128 v[2:5], v193
	ds_read_b128 v[6:9], v193 offset:1024
	ds_read_b128 v[10:13], v193 offset:2048
	ds_read_b128 v[14:17], v193 offset:3072
	s_add_u32 s28, s26, 0x80
	s_addc_u32 s29, s27, 0
	s_cmp_eq_u32 s50, 12
	s_cselect_b32 s31, s19, s29
	s_cselect_b32 s30, s18, s28
	s_cselect_b32 s29, s21, s35
	s_cselect_b32 s28, s20, s34
	v_lshl_add_u64 v[220:221], s[26:27], 0, v[178:179]
	s_add_i32 m0, s38, 0xc000
	ds_read_b128 v[180:183], v194
	ds_read_b128 v[184:187], v194 offset:1024
	ds_read_b128 v[196:199], v194 offset:2048
	ds_read_b128 v[200:203], v194 offset:3072
	ds_read_b128 v[204:207], v194 offset:4096
	ds_read_b128 v[208:211], v194 offset:5120
	ds_read_b128 v[212:215], v194 offset:6144
	ds_read_b128 v[216:219], v194 offset:7168
	global_load_lds_dwordx4 v[220:221], off
	v_lshl_add_u64 v[220:221], s[26:27], 0, v[176:177]
	s_add_i32 m0, s38, 0xe000
	s_nop 0
	global_load_lds_dwordx4 v[220:221], off
	s_waitcnt vmcnt(8)
	s_waitcnt lgkmcnt(0)
	s_barrier
	s_setprio 1
	s_waitcnt lgkmcnt(0)
	s_nop 1
	v_mfma_f32_16x16x128_f8f6f4 v[158:161], v[18:25], v[180:187], v[158:161]
	v_mfma_f32_16x16x128_f8f6f4 v[154:157], v[26:33], v[180:187], v[154:157]
	v_mfma_f32_16x16x128_f8f6f4 v[142:145], v[18:25], v[196:203], v[142:145]
	v_mfma_f32_16x16x128_f8f6f4 v[138:141], v[26:33], v[196:203], v[138:141]
	v_mfma_f32_16x16x128_f8f6f4 v[126:129], v[18:25], v[204:211], v[126:129]
	v_mfma_f32_16x16x128_f8f6f4 v[122:125], v[26:33], v[204:211], v[122:125]
	v_mfma_f32_16x16x128_f8f6f4 v[110:113], v[18:25], v[212:219], v[110:113]
	v_mfma_f32_16x16x128_f8f6f4 v[106:109], v[26:33], v[212:219], v[106:109]
	s_nop 1
	v_mfma_f32_16x16x128_f8f6f4 v[150:153], v[2:9], v[180:187], v[150:153]
	v_mfma_f32_16x16x128_f8f6f4 v[146:149], v[10:17], v[180:187], v[146:149]
	v_mfma_f32_16x16x128_f8f6f4 v[134:137], v[2:9], v[196:203], v[134:137]
	v_mfma_f32_16x16x128_f8f6f4 v[130:133], v[10:17], v[196:203], v[130:133]
	v_mfma_f32_16x16x128_f8f6f4 v[118:121], v[2:9], v[204:211], v[118:121]
	v_mfma_f32_16x16x128_f8f6f4 v[114:117], v[10:17], v[204:211], v[114:117]
	v_mfma_f32_16x16x128_f8f6f4 v[94:97], v[2:9], v[212:219], v[94:97]
	v_mfma_f32_16x16x128_f8f6f4 v[90:93], v[10:17], v[212:219], v[90:93]
	s_setprio 0
	s_barrier
	s_add_i32 s51, s3, s37
	v_lshl_add_u64 v[180:181], s[28:29], 0, v[164:165]
	s_mov_b32 m0, s51
	ds_read_b128 v[196:199], v194 offset:16384
	ds_read_b128 v[200:203], v194 offset:17408
	ds_read_b128 v[204:207], v194 offset:18432
	ds_read_b128 v[208:211], v194 offset:19456
	ds_read_b128 v[212:215], v194 offset:20480
	ds_read_b128 v[216:219], v194 offset:21504
	ds_read_b128 v[220:223], v194 offset:22528
	ds_read_b128 v[224:227], v194 offset:23552
	global_load_lds_dwordx4 v[180:181], off
	s_add_i32 m0, s51, 0x2000
	s_add_u32 s52, s28, 0x40000
	v_lshl_add_u64 v[182:183], s[28:29], 0, v[162:163]
	s_addc_u32 s53, s29, 0
	s_add_i32 s51, s2, s37
	global_load_lds_dwordx4 v[182:183], off
	v_lshl_add_u64 v[184:185], s[52:53], 0, v[164:165]
	s_mov_b32 m0, s51
	v_lshl_add_u64 v[186:187], s[30:31], 0, v[168:169]
	global_load_lds_dwordx4 v[184:185], off
	v_lshl_add_u64 v[184:185], s[52:53], 0, v[162:163]
	s_add_i32 m0, s51, 0x2000
	s_nop 0
	global_load_lds_dwordx4 v[184:185], off
	v_lshl_add_u64 v[184:185], s[30:31], 0, v[166:167]
	s_mov_b32 m0, s38
	s_nop 0
	global_load_lds_dwordx4 v[184:185], off
	s_mov_b32 m0, s39
	s_nop 0
	global_load_lds_dwordx4 v[186:187], off
	s_waitcnt vmcnt(8)
	s_waitcnt lgkmcnt(0)
	s_barrier
	s_setprio 1
	s_waitcnt lgkmcnt(0)
	s_nop 1
	v_mfma_f32_16x16x128_f8f6f4 v[78:81], v[18:25], v[196:203], v[78:81]
	v_mfma_f32_16x16x128_f8f6f4 v[74:77], v[26:33], v[196:203], v[74:77]
	v_mfma_f32_16x16x128_f8f6f4 v[62:65], v[18:25], v[204:211], v[62:65]
	v_mfma_f32_16x16x128_f8f6f4 v[58:61], v[26:33], v[204:211], v[58:61]
	v_mfma_f32_16x16x128_f8f6f4 v[46:49], v[18:25], v[212:219], v[46:49]
	v_mfma_f32_16x16x128_f8f6f4 v[42:45], v[26:33], v[212:219], v[42:45]
	v_mfma_f32_16x16x128_f8f6f4 v[38:41], v[18:25], v[220:227], v[38:41]
	v_mfma_f32_16x16x128_f8f6f4 v[34:37], v[26:33], v[220:227], v[34:37]
	s_nop 1
	v_mfma_f32_16x16x128_f8f6f4 v[98:101], v[2:9], v[196:203], v[98:101]
	v_mfma_f32_16x16x128_f8f6f4 v[102:105], v[10:17], v[196:203], v[102:105]
	v_mfma_f32_16x16x128_f8f6f4 v[82:85], v[2:9], v[204:211], v[82:85]
	v_mfma_f32_16x16x128_f8f6f4 v[86:89], v[10:17], v[204:211], v[86:89]
	v_mfma_f32_16x16x128_f8f6f4 v[66:69], v[2:9], v[212:219], v[66:69]
	v_mfma_f32_16x16x128_f8f6f4 v[70:73], v[10:17], v[212:219], v[70:73]
	v_mfma_f32_16x16x128_f8f6f4 v[50:53], v[2:9], v[220:227], v[50:53]
	v_mfma_f32_16x16x128_f8f6f4 v[54:57], v[10:17], v[220:227], v[54:57]
	s_setprio 0
	s_barrier
	v_add_u32_e32 v14, s86, v188
	v_add_u32_e32 v30, s87, v188
	ds_read_b128 v[2:5], v14
	ds_read_b128 v[6:9], v14 offset:1024
	ds_read_b128 v[10:13], v14 offset:2048
	ds_read_b128 v[14:17], v14 offset:3072
	ds_read_b128 v[18:21], v30
	ds_read_b128 v[22:25], v30 offset:1024
	ds_read_b128 v[26:29], v30 offset:2048
	ds_read_b128 v[30:33], v30 offset:3072
	s_mov_b32 m0, s40
	v_lshl_add_u64 v[230:231], s[30:31], 0, v[170:171]
	ds_read_b128 v[196:199], v194 offset:32768
	ds_read_b128 v[200:203], v194 offset:33792
	ds_read_b128 v[204:207], v194 offset:34816
	ds_read_b128 v[208:211], v194 offset:35840
	ds_read_b128 v[212:215], v194 offset:36864
	ds_read_b128 v[216:219], v194 offset:37888
	ds_read_b128 v[220:223], v194 offset:38912
	ds_read_b128 v[224:227], v194 offset:39936
	global_load_lds_dwordx4 v[230:231], off
	v_lshl_add_u64 v[230:231], s[30:31], 0, v[172:173]
	s_mov_b32 m0, s41
	s_nop 0
	global_load_lds_dwordx4 v[230:231], off
	s_waitcnt vmcnt(8)
	s_waitcnt lgkmcnt(0)
	s_barrier
	s_setprio 1
	s_waitcnt lgkmcnt(0)
	s_nop 1
	v_mfma_f32_16x16x128_f8f6f4 v[158:161], v[2:9], v[196:203], v[158:161]
	v_mfma_f32_16x16x128_f8f6f4 v[154:157], v[10:17], v[196:203], v[154:157]
	v_mfma_f32_16x16x128_f8f6f4 v[142:145], v[2:9], v[204:211], v[142:145]
	v_mfma_f32_16x16x128_f8f6f4 v[138:141], v[10:17], v[204:211], v[138:141]
	v_mfma_f32_16x16x128_f8f6f4 v[126:129], v[2:9], v[212:219], v[126:129]
	v_mfma_f32_16x16x128_f8f6f4 v[122:125], v[10:17], v[212:219], v[122:125]
	v_mfma_f32_16x16x128_f8f6f4 v[110:113], v[2:9], v[220:227], v[110:113]
	v_mfma_f32_16x16x128_f8f6f4 v[106:109], v[10:17], v[220:227], v[106:109]
	s_nop 1
	v_mfma_f32_16x16x128_f8f6f4 v[150:153], v[18:25], v[196:203], v[150:153]
	v_mfma_f32_16x16x128_f8f6f4 v[146:149], v[26:33], v[196:203], v[146:149]
	v_mfma_f32_16x16x128_f8f6f4 v[134:137], v[18:25], v[204:211], v[134:137]
	v_mfma_f32_16x16x128_f8f6f4 v[130:133], v[26:33], v[204:211], v[130:133]
	v_mfma_f32_16x16x128_f8f6f4 v[118:121], v[18:25], v[212:219], v[118:121]
	v_mfma_f32_16x16x128_f8f6f4 v[114:117], v[26:33], v[212:219], v[114:117]
	v_mfma_f32_16x16x128_f8f6f4 v[94:97], v[18:25], v[220:227], v[94:97]
	v_mfma_f32_16x16x128_f8f6f4 v[90:93], v[26:33], v[220:227], v[90:93]
	s_setprio 0
	s_barrier
	s_add_i32 s30, s86, s37
	v_lshl_add_u64 v[180:181], v[180:181], 0, s[8:9]
	s_mov_b32 m0, s30
	ds_read_b128 v[196:199], v194 offset:49152
	ds_read_b128 v[200:203], v194 offset:50176
	ds_read_b128 v[204:207], v194 offset:51200
	ds_read_b128 v[208:211], v194 offset:52224
	ds_read_b128 v[212:215], v194 offset:53248
	ds_read_b128 v[216:219], v194 offset:54272
	ds_read_b128 v[220:223], v194 offset:55296
	ds_read_b128 v[224:227], v194 offset:56320
	global_load_lds_dwordx4 v[180:181], off
	s_add_i32 m0, s30, 0x2000
	s_add_u32 s28, s28, 0x40080
	v_lshl_add_u64 v[180:181], v[182:183], 0, s[8:9]
	s_addc_u32 s29, s29, 0
	s_add_i32 s30, s87, s37
	global_load_lds_dwordx4 v[180:181], off
	v_lshl_add_u64 v[180:181], s[28:29], 0, v[164:165]
	s_mov_b32 m0, s30
	s_nop 0
	global_load_lds_dwordx4 v[180:181], off
	v_lshl_add_u64 v[180:181], s[28:29], 0, v[162:163]
	s_add_i32 m0, s30, 0x2000
	s_nop 0
	global_load_lds_dwordx4 v[180:181], off
	v_lshl_add_u64 v[180:181], v[184:185], 0, s[8:9]
	s_mov_b32 m0, s43
	s_nop 0
	global_load_lds_dwordx4 v[180:181], off
	v_lshl_add_u64 v[180:181], v[186:187], 0, s[8:9]
	s_mov_b32 m0, s44
	s_nop 0
	global_load_lds_dwordx4 v[180:181], off
	s_waitcnt vmcnt(8)
	s_waitcnt lgkmcnt(0)
	s_barrier
	s_setprio 1
	s_waitcnt lgkmcnt(0)
	s_nop 1
	v_mfma_f32_16x16x128_f8f6f4 v[78:81], v[2:9], v[196:203], v[78:81]
	v_mfma_f32_16x16x128_f8f6f4 v[74:77], v[10:17], v[196:203], v[74:77]
	v_mfma_f32_16x16x128_f8f6f4 v[62:65], v[2:9], v[204:211], v[62:65]
	v_mfma_f32_16x16x128_f8f6f4 v[58:61], v[10:17], v[204:211], v[58:61]
	v_mfma_f32_16x16x128_f8f6f4 v[46:49], v[2:9], v[212:219], v[46:49]
	v_mfma_f32_16x16x128_f8f6f4 v[42:45], v[10:17], v[212:219], v[42:45]
	v_mfma_f32_16x16x128_f8f6f4 v[38:41], v[2:9], v[220:227], v[38:41]
	v_mfma_f32_16x16x128_f8f6f4 v[34:37], v[10:17], v[220:227], v[34:37]
	s_nop 1
	v_mfma_f32_16x16x128_f8f6f4 v[98:101], v[18:25], v[196:203], v[98:101]
	v_mfma_f32_16x16x128_f8f6f4 v[102:105], v[26:33], v[196:203], v[102:105]
	v_mfma_f32_16x16x128_f8f6f4 v[82:85], v[18:25], v[204:211], v[82:85]
	v_mfma_f32_16x16x128_f8f6f4 v[86:89], v[26:33], v[204:211], v[86:89]
	v_mfma_f32_16x16x128_f8f6f4 v[66:69], v[18:25], v[212:219], v[66:69]
	v_mfma_f32_16x16x128_f8f6f4 v[70:73], v[26:33], v[212:219], v[70:73]
	v_mfma_f32_16x16x128_f8f6f4 v[50:53], v[18:25], v[220:227], v[50:53]
	v_mfma_f32_16x16x128_f8f6f4 v[54:57], v[26:33], v[220:227], v[54:57]
	s_setprio 0
	s_barrier
	s_add_i32 s50, s50, 2
	s_add_u32 s26, s26, 0x100
	s_addc_u32 s27, s27, 0
	s_add_u32 s34, s34, 0x100
	s_addc_u32 s35, s35, 0
	s_cmp_gt_u32 s50, 13
	s_cbranch_scc0 .LBB0_1419
